# v43 + the redundant s_waitcnt lgkmcnt(0) after the barrier at the head of each of the 48 MFMA phases removed
# speedup vs baseline: 1.0060x; 1.0060x over previous
; #define PG8_STAGE(bufoff, gbase, voff) do { _Pragma("unroll") for (int _i = 0; _i < 2; ++_i) \
;         __builtin_amdgcn_global_load_lds((const __attribute__((address_space(1))) unsigned*)((const __attribute__((address_space(1))) char*)(gbase) + (unsigned)lnd_v((int)(voff)[_i])), (LAS unsigned*)(lds + (bufoff) + ldsw + _i * 8192), 16, 0, 0); } while (0)
; #define PG8_LDA(dst, b, h) do { _Pragma("unroll") for (int m = 0; m < 4; ++m) _Pragma("unroll") for (int k = 0; k < 2; ++k) dst[m][k] = *(const LAS bf16x8*)(lds + PG8_SA(b, h) + aoff + m * 2048 + k * 1024); } while (0)
; #define PG8_LDB(dst, b, h) do { _Pragma("unroll") for (int n = 0; n < 2; ++n) _Pragma("unroll") for (int k = 0; k < 2; ++k) dst[n][k] = *(const LAS bf16x8*)(lds + PG8_SB(b, h) + boff + n * 2048 + k * 1024); } while (0)
; #define PG8_WAIT_V(n) asm volatile("s_waitcnt vmcnt(" #n ")" ::: "memory")
; #define PG8_WAIT_L(n) asm volatile("s_waitcnt lgkmcnt(" #n ")" ::: "memory")
; #define PG8_BAR __builtin_amdgcn_s_barrier()
; template <class Desc, class Epi>
; __device__ __forceinline__ void gemm_phase(const int wv_, LAS unsigned char* lds, const Desc& d, const Epi& E) {
;     ...
;         for (int t = 0; t < nt; t += 2) {
;             const bool last = (t == nt - 2);
;             unsigned sA0[2], sA1[2];
;             if constexpr (Desc::GATHER) { sA0[0] = last ? voffAn[0] : voffA[0]; sA0[1] = last ? voffAn[1] : voffA[1]; sA1[0] = last ? voffAn1[0] : voffA1[0]; sA1[1] = last ? voffAn1[1] : voffA1[1]; }
;             else { sA0[0] = voffA[0]; sA0[1] = voffA[1]; sA1[0] = voffA1[0]; sA1[1] = voffA1[1]; }
;             const char* a1 = cA + (size_t)(t + 1) * kstep;
;             const char* a2 = last ? nA : cA + (size_t)(t + 2) * kstep; const char* b2 = last ? nB : cB + (size_t)(t + 2) * kstep;
;             const char* a3 = a2 + kstep; const char* b3 = b2 + kstep;
;             PG8_LDB(B0, 0, 0); PG8_LDB(B1, 0, 1); PG8_SCHED; PG8_LDA(At, 0, 0); PG8_STAGE(PG8_SA(1, 1), a1, voffA1);
;             PG8_WAIT_V(8); PG8_WAIT_L(0); PG8_BAR; PG8_MMA(0, 0, At, B0); PG8_MMA(0, 1, At, B1); PG8_BAR; PG8_SCHED;
;             PG8_LDA(At, 0, 1); PG8_STAGE(PG8_SB(0, 0), b2, voffB); PG8_STAGE(PG8_SB(0, 1), b2 + hstepB, voffB); PG8_STAGE(PG8_SA(0, 0), a2, sA0);
;             PG8_WAIT_V(8); PG8_WAIT_L(0); PG8_BAR; PG8_MMA(1, 0, At, B0); PG8_MMA(1, 1, At, B1); PG8_BAR; PG8_SCHED;
.LBB0_662:
	ds_read_b128 v[154:157], v148
	ds_read_b128 v[158:161], v148 offset:1024
	ds_read_b128 v[162:165], v148 offset:2048
	ds_read_b128 v[166:169], v148 offset:3072
	ds_read_b128 v[170:173], v149
	ds_read_b128 v[174:177], v149 offset:1024
	ds_read_b128 v[178:181], v149 offset:2048
	ds_read_b128 v[182:185], v149 offset:3072
	s_add_u32 s2, s0, 0x80
	s_addc_u32 s3, s1, 0
	s_cmp_eq_u32 s60, 12
	s_cselect_b32 s3, s17, s3
	s_cselect_b32 s2, s16, s2
	s_cselect_b32 s27, s23, s59
	s_cselect_b32 s26, s22, s58
	v_mov_b32_e32 v128, v133
	s_mov_b32 m0, s42
	ds_read_b128 v[186:189], v150
	ds_read_b128 v[190:193], v150 offset:1024
	ds_read_b128 v[194:197], v150 offset:2048
	ds_read_b128 v[198:201], v150 offset:3072
	ds_read_b128 v[202:205], v150 offset:4096
	ds_read_b128 v[206:209], v150 offset:5120
	ds_read_b128 v[210:213], v150 offset:6144
	ds_read_b128 v[214:217], v150 offset:7168
	s_nop 0
	global_load_lds_dwordx4 v128, s[0:1]
	v_mov_b32_e32 v128, v136
	s_mov_b32 m0, s43
	s_nop 0
	global_load_lds_dwordx4 v128, s[0:1]
	s_waitcnt vmcnt(8)
	s_waitcnt lgkmcnt(0)
	s_barrier
	v_mfma_f32_16x16x32_bf16 v[124:127], v[154:157], v[186:189], v[124:127]
	v_mfma_f32_16x16x32_bf16 v[120:123], v[162:165], v[186:189], v[120:123]
	v_mfma_f32_16x16x32_bf16 v[108:111], v[154:157], v[194:197], v[108:111]
	v_mfma_f32_16x16x32_bf16 v[104:107], v[162:165], v[194:197], v[104:107]
	v_mfma_f32_16x16x32_bf16 v[92:95], v[154:157], v[202:205], v[92:95]
	v_mfma_f32_16x16x32_bf16 v[88:91], v[162:165], v[202:205], v[88:91]
	v_mfma_f32_16x16x32_bf16 v[76:79], v[154:157], v[210:213], v[76:79]
	v_mfma_f32_16x16x32_bf16 v[72:75], v[162:165], v[210:213], v[72:75]
	v_mfma_f32_16x16x32_bf16 v[124:127], v[158:161], v[190:193], v[124:127]
	v_mfma_f32_16x16x32_bf16 v[120:123], v[166:169], v[190:193], v[120:123]
	v_mfma_f32_16x16x32_bf16 v[108:111], v[158:161], v[198:201], v[108:111]
	v_mfma_f32_16x16x32_bf16 v[104:107], v[166:169], v[198:201], v[104:107]
	v_mfma_f32_16x16x32_bf16 v[92:95], v[158:161], v[206:209], v[92:95]
	v_mfma_f32_16x16x32_bf16 v[88:91], v[166:169], v[206:209], v[88:91]
	v_mfma_f32_16x16x32_bf16 v[76:79], v[158:161], v[214:217], v[76:79]
	v_mfma_f32_16x16x32_bf16 v[72:75], v[166:169], v[214:217], v[72:75]
	v_mfma_f32_16x16x32_bf16 v[116:119], v[170:173], v[186:189], v[116:119]
	v_mfma_f32_16x16x32_bf16 v[112:115], v[178:181], v[186:189], v[112:115]
	v_mfma_f32_16x16x32_bf16 v[100:103], v[170:173], v[194:197], v[100:103]
	v_mfma_f32_16x16x32_bf16 v[96:99], v[178:181], v[194:197], v[96:99]
	v_mfma_f32_16x16x32_bf16 v[84:87], v[170:173], v[202:205], v[84:87]
	v_mfma_f32_16x16x32_bf16 v[80:83], v[178:181], v[202:205], v[80:83]
	v_mfma_f32_16x16x32_bf16 v[68:71], v[170:173], v[210:213], v[68:71]
	v_mfma_f32_16x16x32_bf16 v[64:67], v[178:181], v[210:213], v[64:67]
	v_mfma_f32_16x16x32_bf16 v[116:119], v[174:177], v[190:193], v[116:119]
	v_mfma_f32_16x16x32_bf16 v[112:115], v[182:185], v[190:193], v[112:115]
	v_mfma_f32_16x16x32_bf16 v[100:103], v[174:177], v[198:201], v[100:103]
	v_mfma_f32_16x16x32_bf16 v[96:99], v[182:185], v[198:201], v[96:99]
	v_mfma_f32_16x16x32_bf16 v[84:87], v[174:177], v[206:209], v[84:87]
	v_mfma_f32_16x16x32_bf16 v[80:83], v[182:185], v[206:209], v[80:83]
	v_mfma_f32_16x16x32_bf16 v[68:71], v[174:177], v[214:217], v[68:71]
	v_mfma_f32_16x16x32_bf16 v[64:67], v[182:185], v[214:217], v[64:67]
	s_barrier
	v_mov_b32_e32 v128, v134
	s_mov_b32 m0, s44
	ds_read_b128 v[186:189], v150 offset:16384
	ds_read_b128 v[190:193], v150 offset:17408
	ds_read_b128 v[194:197], v150 offset:18432
	ds_read_b128 v[198:201], v150 offset:19456
	ds_read_b128 v[202:205], v150 offset:20480
	ds_read_b128 v[206:209], v150 offset:21504
	ds_read_b128 v[210:213], v150 offset:22528
	ds_read_b128 v[214:217], v150 offset:23552
	s_add_u32 s62, s26, 0x40000
	global_load_lds_dwordx4 v128, s[26:27]
	v_mov_b32_e32 v128, v137
	s_mov_b32 m0, s45
	s_addc_u32 s63, s27, 0
	global_load_lds_dwordx4 v128, s[26:27]
	v_mov_b32_e32 v128, v134
	s_mov_b32 m0, s46
	s_nop 0
	global_load_lds_dwordx4 v128, s[62:63]
	v_mov_b32_e32 v128, v137
	s_mov_b32 m0, s47
	s_nop 0
	global_load_lds_dwordx4 v128, s[62:63]
	v_mov_b32_e32 v128, v132
	s_mov_b32 m0, s36
	s_nop 0
	global_load_lds_dwordx4 v128, s[2:3]
	v_mov_b32_e32 v128, v135
	s_mov_b32 m0, s37
	s_nop 0
	global_load_lds_dwordx4 v128, s[2:3]
	s_waitcnt vmcnt(8)
	s_waitcnt lgkmcnt(0)
	s_barrier
	v_mfma_f32_16x16x32_bf16 v[60:63], v[154:157], v[186:189], v[60:63]
	v_mfma_f32_16x16x32_bf16 v[56:59], v[162:165], v[186:189], v[56:59]
	v_mfma_f32_16x16x32_bf16 v[44:47], v[154:157], v[194:197], v[44:47]
	v_mfma_f32_16x16x32_bf16 v[32:35], v[162:165], v[194:197], v[32:35]
	v_mfma_f32_16x16x32_bf16 v[16:19], v[154:157], v[202:205], v[16:19]
	v_mfma_f32_16x16x32_bf16 v[8:11], v[162:165], v[202:205], v[8:11]
	v_mfma_f32_16x16x32_bf16 v[4:7], v[154:157], v[210:213], v[4:7]
	v_mfma_f32_16x16x32_bf16 v[0:3], v[162:165], v[210:213], v[0:3]
	v_mfma_f32_16x16x32_bf16 v[60:63], v[158:161], v[190:193], v[60:63]
	v_mfma_f32_16x16x32_bf16 v[56:59], v[166:169], v[190:193], v[56:59]
	v_mfma_f32_16x16x32_bf16 v[44:47], v[158:161], v[198:201], v[44:47]
	v_mfma_f32_16x16x32_bf16 v[32:35], v[166:169], v[198:201], v[32:35]
	v_mfma_f32_16x16x32_bf16 v[16:19], v[158:161], v[206:209], v[16:19]
	v_mfma_f32_16x16x32_bf16 v[8:11], v[166:169], v[206:209], v[8:11]
	v_mfma_f32_16x16x32_bf16 v[4:7], v[158:161], v[214:217], v[4:7]
	v_mfma_f32_16x16x32_bf16 v[0:3], v[166:169], v[214:217], v[0:3]
	v_mfma_f32_16x16x32_bf16 v[52:55], v[170:173], v[186:189], v[52:55]
	v_mfma_f32_16x16x32_bf16 v[48:51], v[178:181], v[186:189], v[48:51]
	v_mfma_f32_16x16x32_bf16 v[28:31], v[170:173], v[194:197], v[28:31]
	v_mfma_f32_16x16x32_bf16 v[12:15], v[178:181], v[194:197], v[12:15]
	v_mfma_f32_16x16x32_bf16 v[36:39], v[170:173], v[202:205], v[36:39]
	v_mfma_f32_16x16x32_bf16 v[40:43], v[178:181], v[202:205], v[40:43]
	v_mfma_f32_16x16x32_bf16 v[20:23], v[170:173], v[210:213], v[20:23]
	v_mfma_f32_16x16x32_bf16 v[24:27], v[178:181], v[210:213], v[24:27]
	v_mfma_f32_16x16x32_bf16 v[52:55], v[174:177], v[190:193], v[52:55]
	v_mfma_f32_16x16x32_bf16 v[48:51], v[182:185], v[190:193], v[48:51]
	v_mfma_f32_16x16x32_bf16 v[28:31], v[174:177], v[198:201], v[28:31]
	v_mfma_f32_16x16x32_bf16 v[12:15], v[182:185], v[198:201], v[12:15]
	v_mfma_f32_16x16x32_bf16 v[36:39], v[174:177], v[206:209], v[36:39]
	v_mfma_f32_16x16x32_bf16 v[40:43], v[182:185], v[206:209], v[40:43]
	v_mfma_f32_16x16x32_bf16 v[20:23], v[174:177], v[214:217], v[20:23]
	v_mfma_f32_16x16x32_bf16 v[24:27], v[182:185], v[214:217], v[24:27]
	s_barrier
; #define PG8_STAGE(bufoff, gbase, voff) do { _Pragma("unroll") for (int _i = 0; _i < 2; ++_i) \
;         __builtin_amdgcn_global_load_lds((const __attribute__((address_space(1))) unsigned*)((const __attribute__((address_space(1))) char*)(gbase) + (unsigned)lnd_v((int)(voff)[_i])), (LAS unsigned*)(lds + (bufoff) + ldsw + _i * 8192), 16, 0, 0); } while (0)
; #define PG8_LDA(dst, b, h) do { _Pragma("unroll") for (int m = 0; m < 4; ++m) _Pragma("unroll") for (int k = 0; k < 2; ++k) dst[m][k] = *(const LAS bf16x8*)(lds + PG8_SA(b, h) + aoff + m * 2048 + k * 1024); } while (0)
; #define PG8_LDB(dst, b, h) do { _Pragma("unroll") for (int n = 0; n < 2; ++n) _Pragma("unroll") for (int k = 0; k < 2; ++k) dst[n][k] = *(const LAS bf16x8*)(lds + PG8_SB(b, h) + boff + n * 2048 + k * 1024); } while (0)
; #define PG8_MMA(ai, bj, At, Bt) do { __builtin_amdgcn_s_setprio(1); _Pragma("unroll") for (int m = 0; m < 4; ++m) _Pragma("unroll") for (int n = 0; n < 2; ++n) _Pragma("unroll") for (int k = 0; k < 2; ++k) \
;         acc[ai][bj][m][n] = __builtin_amdgcn_mfma_f32_16x16x32_bf16(Bt[n][k], At[m][k], acc[ai][bj][m][n], 0, 0, 0); __builtin_amdgcn_s_setprio(0); } while (0)
; #define PG8_WAIT_V(n) asm volatile("s_waitcnt vmcnt(" #n ")" ::: "memory")
; #define PG8_WAIT_L(n) asm volatile("s_waitcnt lgkmcnt(" #n ")" ::: "memory")
; #define PG8_BAR __builtin_amdgcn_s_barrier()
; #define PG8_SCHED __builtin_amdgcn_sched_barrier(0)
; template <class Desc, class Epi>
; __device__ __forceinline__ void gemm_phase(const int wv_, LAS unsigned char* lds, const Desc& d, const Epi& E) {
;     ...
;             PG8_LDB(B0, 1, 0); PG8_LDB(B1, 1, 1); PG8_SCHED; PG8_LDA(At, 1, 0); PG8_STAGE(PG8_SA(0, 1), a2, sA1);
;             PG8_WAIT_V(8); PG8_WAIT_L(0); PG8_BAR; PG8_MMA(0, 0, At, B0); PG8_MMA(0, 1, At, B1); PG8_BAR; PG8_SCHED;
;             PG8_LDA(At, 1, 1); PG8_STAGE(PG8_SB(1, 0), b3, voffB); PG8_STAGE(PG8_SB(1, 1), b3 + hstepB, voffB); PG8_STAGE(PG8_SA(1, 0), a3, sA0);
;             PG8_WAIT_V(8); PG8_WAIT_L(0); PG8_BAR; PG8_MMA(1, 0, At, B0); PG8_MMA(1, 1, At, B1); PG8_BAR; PG8_SCHED;
;         }
	ds_read_b128 v[154:157], v151
	ds_read_b128 v[158:161], v151 offset:1024
	ds_read_b128 v[162:165], v151 offset:2048
	ds_read_b128 v[166:169], v151 offset:3072
	ds_read_b128 v[170:173], v152
	ds_read_b128 v[174:177], v152 offset:1024
	ds_read_b128 v[178:181], v152 offset:2048
	ds_read_b128 v[182:185], v152 offset:3072
	v_mov_b32_e32 v128, v133
	s_mov_b32 m0, s38
	ds_read_b128 v[186:189], v150 offset:32768
	ds_read_b128 v[190:193], v150 offset:33792
	ds_read_b128 v[194:197], v150 offset:34816
	ds_read_b128 v[198:201], v150 offset:35840
	ds_read_b128 v[202:205], v150 offset:36864
	ds_read_b128 v[206:209], v150 offset:37888
	ds_read_b128 v[210:213], v150 offset:38912
	ds_read_b128 v[214:217], v150 offset:39936
	s_nop 0
	global_load_lds_dwordx4 v128, s[2:3]
	v_mov_b32_e32 v128, v136
	s_mov_b32 m0, s39
	s_nop 0
	global_load_lds_dwordx4 v128, s[2:3]
	s_waitcnt vmcnt(8)
	s_waitcnt lgkmcnt(0)
	s_barrier
	v_mfma_f32_16x16x32_bf16 v[124:127], v[154:157], v[186:189], v[124:127]
	v_mfma_f32_16x16x32_bf16 v[120:123], v[162:165], v[186:189], v[120:123]
	v_mfma_f32_16x16x32_bf16 v[108:111], v[154:157], v[194:197], v[108:111]
	v_mfma_f32_16x16x32_bf16 v[104:107], v[162:165], v[194:197], v[104:107]
	v_mfma_f32_16x16x32_bf16 v[92:95], v[154:157], v[202:205], v[92:95]
	v_mfma_f32_16x16x32_bf16 v[88:91], v[162:165], v[202:205], v[88:91]
	v_mfma_f32_16x16x32_bf16 v[76:79], v[154:157], v[210:213], v[76:79]
	v_mfma_f32_16x16x32_bf16 v[72:75], v[162:165], v[210:213], v[72:75]
	v_mfma_f32_16x16x32_bf16 v[124:127], v[158:161], v[190:193], v[124:127]
	v_mfma_f32_16x16x32_bf16 v[120:123], v[166:169], v[190:193], v[120:123]
	v_mfma_f32_16x16x32_bf16 v[108:111], v[158:161], v[198:201], v[108:111]
	v_mfma_f32_16x16x32_bf16 v[104:107], v[166:169], v[198:201], v[104:107]
	v_mfma_f32_16x16x32_bf16 v[92:95], v[158:161], v[206:209], v[92:95]
	v_mfma_f32_16x16x32_bf16 v[88:91], v[166:169], v[206:209], v[88:91]
	v_mfma_f32_16x16x32_bf16 v[76:79], v[158:161], v[214:217], v[76:79]
	v_mfma_f32_16x16x32_bf16 v[72:75], v[166:169], v[214:217], v[72:75]
	v_mfma_f32_16x16x32_bf16 v[116:119], v[170:173], v[186:189], v[116:119]
	v_mfma_f32_16x16x32_bf16 v[112:115], v[178:181], v[186:189], v[112:115]
	v_mfma_f32_16x16x32_bf16 v[100:103], v[170:173], v[194:197], v[100:103]
	v_mfma_f32_16x16x32_bf16 v[96:99], v[178:181], v[194:197], v[96:99]
	v_mfma_f32_16x16x32_bf16 v[84:87], v[170:173], v[202:205], v[84:87]
	v_mfma_f32_16x16x32_bf16 v[80:83], v[178:181], v[202:205], v[80:83]
	v_mfma_f32_16x16x32_bf16 v[68:71], v[170:173], v[210:213], v[68:71]
	v_mfma_f32_16x16x32_bf16 v[64:67], v[178:181], v[210:213], v[64:67]
	v_mfma_f32_16x16x32_bf16 v[116:119], v[174:177], v[190:193], v[116:119]
	v_mfma_f32_16x16x32_bf16 v[112:115], v[182:185], v[190:193], v[112:115]
	v_mfma_f32_16x16x32_bf16 v[100:103], v[174:177], v[198:201], v[100:103]
	v_mfma_f32_16x16x32_bf16 v[96:99], v[182:185], v[198:201], v[96:99]
	v_mfma_f32_16x16x32_bf16 v[84:87], v[174:177], v[206:209], v[84:87]
	v_mfma_f32_16x16x32_bf16 v[80:83], v[182:185], v[206:209], v[80:83]
	v_mfma_f32_16x16x32_bf16 v[68:71], v[174:177], v[214:217], v[68:71]
	v_mfma_f32_16x16x32_bf16 v[64:67], v[182:185], v[214:217], v[64:67]
	s_barrier
	v_mov_b32_e32 v128, v134
	ds_read_b128 v[186:189], v150 offset:49152
	ds_read_b128 v[190:193], v150 offset:50176
	ds_read_b128 v[194:197], v150 offset:51200
	ds_read_b128 v[198:201], v150 offset:52224
	ds_read_b128 v[202:205], v150 offset:53248
	ds_read_b128 v[206:209], v150 offset:54272
	ds_read_b128 v[210:213], v150 offset:55296
	ds_read_b128 v[214:217], v150 offset:56320
	s_mov_b32 m0, s48
	v_lshl_add_u64 v[130:131], s[26:27], 0, v[128:129]
	v_lshl_add_u64 v[130:131], v[130:131], 0, s[8:9]
	v_mov_b32_e32 v128, v137
	global_load_lds_dwordx4 v[130:131], off
	s_mov_b32 m0, s49
	v_lshl_add_u64 v[130:131], s[26:27], 0, v[128:129]
	v_lshl_add_u64 v[130:131], v[130:131], 0, s[8:9]
	s_add_u32 s26, s26, 0x40080
	v_mov_b32_e32 v128, v134
	global_load_lds_dwordx4 v[130:131], off
	s_addc_u32 s27, s27, 0
	s_mov_b32 m0, s50
	s_nop 0
	global_load_lds_dwordx4 v128, s[26:27]
	v_mov_b32_e32 v128, v137
	s_mov_b32 m0, s51
	s_nop 0
	global_load_lds_dwordx4 v128, s[26:27]
	v_mov_b32_e32 v128, v132
	s_mov_b32 m0, s40
	v_lshl_add_u64 v[130:131], s[2:3], 0, v[128:129]
	v_lshl_add_u64 v[130:131], v[130:131], 0, s[8:9]
	v_mov_b32_e32 v128, v135
	global_load_lds_dwordx4 v[130:131], off
	s_mov_b32 m0, s41
	v_lshl_add_u64 v[130:131], s[2:3], 0, v[128:129]
	v_lshl_add_u64 v[130:131], v[130:131], 0, s[8:9]
	global_load_lds_dwordx4 v[130:131], off
	s_waitcnt vmcnt(8)
	s_waitcnt lgkmcnt(0)
	s_barrier
	v_mfma_f32_16x16x32_bf16 v[60:63], v[154:157], v[186:189], v[60:63]
	v_mfma_f32_16x16x32_bf16 v[56:59], v[162:165], v[186:189], v[56:59]
	v_mfma_f32_16x16x32_bf16 v[44:47], v[154:157], v[194:197], v[44:47]
	v_mfma_f32_16x16x32_bf16 v[32:35], v[162:165], v[194:197], v[32:35]
	v_mfma_f32_16x16x32_bf16 v[16:19], v[154:157], v[202:205], v[16:19]
	v_mfma_f32_16x16x32_bf16 v[8:11], v[162:165], v[202:205], v[8:11]
	v_mfma_f32_16x16x32_bf16 v[4:7], v[154:157], v[210:213], v[4:7]
	v_mfma_f32_16x16x32_bf16 v[0:3], v[162:165], v[210:213], v[0:3]
	v_mfma_f32_16x16x32_bf16 v[60:63], v[158:161], v[190:193], v[60:63]
	v_mfma_f32_16x16x32_bf16 v[56:59], v[166:169], v[190:193], v[56:59]
	v_mfma_f32_16x16x32_bf16 v[44:47], v[158:161], v[198:201], v[44:47]
	v_mfma_f32_16x16x32_bf16 v[32:35], v[166:169], v[198:201], v[32:35]
	v_mfma_f32_16x16x32_bf16 v[16:19], v[158:161], v[206:209], v[16:19]
	v_mfma_f32_16x16x32_bf16 v[8:11], v[166:169], v[206:209], v[8:11]
	v_mfma_f32_16x16x32_bf16 v[4:7], v[158:161], v[214:217], v[4:7]
	v_mfma_f32_16x16x32_bf16 v[0:3], v[166:169], v[214:217], v[0:3]
	v_mfma_f32_16x16x32_bf16 v[52:55], v[170:173], v[186:189], v[52:55]
	v_mfma_f32_16x16x32_bf16 v[48:51], v[178:181], v[186:189], v[48:51]
	v_mfma_f32_16x16x32_bf16 v[28:31], v[170:173], v[194:197], v[28:31]
	v_mfma_f32_16x16x32_bf16 v[12:15], v[178:181], v[194:197], v[12:15]
	v_mfma_f32_16x16x32_bf16 v[36:39], v[170:173], v[202:205], v[36:39]
	v_mfma_f32_16x16x32_bf16 v[40:43], v[178:181], v[202:205], v[40:43]
	v_mfma_f32_16x16x32_bf16 v[20:23], v[170:173], v[210:213], v[20:23]
	v_mfma_f32_16x16x32_bf16 v[24:27], v[178:181], v[210:213], v[24:27]
	v_mfma_f32_16x16x32_bf16 v[52:55], v[174:177], v[190:193], v[52:55]
	v_mfma_f32_16x16x32_bf16 v[48:51], v[182:185], v[190:193], v[48:51]
	v_mfma_f32_16x16x32_bf16 v[28:31], v[174:177], v[198:201], v[28:31]
	v_mfma_f32_16x16x32_bf16 v[12:15], v[182:185], v[198:201], v[12:15]
	v_mfma_f32_16x16x32_bf16 v[36:39], v[174:177], v[206:209], v[36:39]
	v_mfma_f32_16x16x32_bf16 v[40:43], v[182:185], v[206:209], v[40:43]
	v_mfma_f32_16x16x32_bf16 v[20:23], v[174:177], v[214:217], v[20:23]
	v_mfma_f32_16x16x32_bf16 v[24:27], v[182:185], v[214:217], v[24:27]
	s_barrier
	s_add_i32 s60, s60, 2
	s_add_u32 s0, s0, 0x100
	s_addc_u32 s1, s1, 0
	s_add_u32 s58, s58, 0x100
	s_addc_u32 s59, s59, 0
	s_cmp_gt_u32 s60, 13
	s_cbranch_scc0 .LBB0_662
	s_and_b64 vcc, exec, s[14:15]
	s_cbranch_vccz .LBB0_665
	s_barrier

; #define PG8_STAGE(bufoff, gbase, voff) do { _Pragma("unroll") for (int _i = 0; _i < 2; ++_i) \
;         __builtin_amdgcn_global_load_lds((const __attribute__((address_space(1))) unsigned*)((const __attribute__((address_space(1))) char*)(gbase) + (unsigned)lnd_v((int)(voff)[_i])), (LAS unsigned*)(lds + (bufoff) + ldsw + _i * 8192), 16, 0, 0); } while (0)
; #define PG8_LDA(dst, b, h) do { _Pragma("unroll") for (int m = 0; m < 4; ++m) _Pragma("unroll") for (int k = 0; k < 2; ++k) dst[m][k] = *(const LAS bf16x8*)(lds + PG8_SA(b, h) + aoff + m * 2048 + k * 1024); } while (0)
; #define PG8_LDB(dst, b, h) do { _Pragma("unroll") for (int n = 0; n < 2; ++n) _Pragma("unroll") for (int k = 0; k < 2; ++k) dst[n][k] = *(const LAS bf16x8*)(lds + PG8_SB(b, h) + boff + n * 2048 + k * 1024); } while (0)
; #define PG8_WAIT_V(n) asm volatile("s_waitcnt vmcnt(" #n ")" ::: "memory")
; #define PG8_WAIT_L(n) asm volatile("s_waitcnt lgkmcnt(" #n ")" ::: "memory")
; #define PG8_BAR __builtin_amdgcn_s_barrier()
; #define PG8_SCHED __builtin_amdgcn_sched_barrier(0)
; template <class Desc, class Epi>
; __device__ __forceinline__ void gemm_phase(const int wv_, LAS unsigned char* lds, const Desc& d, const Epi& E) {
;     ...
;             const bool last = (t == nt - 2);
;             unsigned sA0[2], sA1[2];
;             if constexpr (Desc::GATHER) { sA0[0] = last ? voffAn[0] : voffA[0]; sA0[1] = last ? voffAn[1] : voffA[1]; sA1[0] = last ? voffAn1[0] : voffA1[0]; sA1[1] = last ? voffAn1[1] : voffA1[1]; }
;             else { sA0[0] = voffA[0]; sA0[1] = voffA[1]; sA1[0] = voffA1[0]; sA1[1] = voffA1[1]; }
;             const char* a1 = cA + (size_t)(t + 1) * kstep;
;             const char* a2 = last ? nA : cA + (size_t)(t + 2) * kstep; const char* b2 = last ? nB : cB + (size_t)(t + 2) * kstep;
;             const char* a3 = a2 + kstep; const char* b3 = b2 + kstep;
;             PG8_LDB(B0, 0, 0); PG8_LDB(B1, 0, 1); PG8_SCHED; PG8_LDA(At, 0, 0); PG8_STAGE(PG8_SA(1, 1), a1, voffA1);
;             PG8_WAIT_V(8); PG8_WAIT_L(0); PG8_BAR; PG8_MMA(0, 0, At, B0); PG8_MMA(0, 1, At, B1); PG8_BAR; PG8_SCHED;
;             PG8_LDA(At, 0, 1); PG8_STAGE(PG8_SB(0, 0), b2, voffB); PG8_STAGE(PG8_SB(0, 1), b2 + hstepB, voffB); PG8_STAGE(PG8_SA(0, 0), a2, sA0);
;             PG8_WAIT_V(8); PG8_WAIT_L(0); PG8_BAR; PG8_MMA(1, 0, At, B0); PG8_MMA(1, 1, At, B1); PG8_BAR; PG8_SCHED;
.LBB0_747:
	s_add_u32 s4, s2, 0x80
	s_addc_u32 s5, s3, 0
	s_add_i32 s63, 0, 0x10000
	s_cmp_eq_u32 s45, 12
	s_cselect_b32 s5, s47, s5
	s_cselect_b32 s4, s46, s4
	v_add_u32_e32 v96, s63, v139
	s_cselect_b32 s21, s49, s43
	s_cselect_b32 s20, s48, s29
	s_add_i32 s66, 0, 0x14000
	ds_read_b128 v[150:153], v96
	ds_read_b128 v[154:157], v96 offset:1024
	ds_read_b128 v[158:161], v96 offset:2048
	ds_read_b128 v[162:165], v96 offset:3072
	v_add_u32_e32 v96, s66, v139
	ds_read_b128 v[166:169], v96
	ds_read_b128 v[170:173], v96 offset:1024
	ds_read_b128 v[174:177], v96 offset:2048
	ds_read_b128 v[178:181], v96 offset:3072
	v_mov_b32_e32 v96, v133
	ds_read_b128 v[182:185], v149
	ds_read_b128 v[186:189], v149 offset:1024
	ds_read_b128 v[190:193], v149 offset:2048
	ds_read_b128 v[194:197], v149 offset:3072
	ds_read_b128 v[198:201], v149 offset:4096
	ds_read_b128 v[202:205], v149 offset:5120
	ds_read_b128 v[206:209], v149 offset:6144
	ds_read_b128 v[210:213], v149 offset:7168
	s_add_i32 m0, s55, 0xc000
	s_nop 0
	global_load_lds_dwordx4 v96, s[2:3]
	v_mov_b32_e32 v96, v136
	s_add_i32 m0, s55, 0xe000
	s_nop 0
	global_load_lds_dwordx4 v96, s[2:3]
	s_waitcnt vmcnt(8)
	s_waitcnt lgkmcnt(0)
	s_barrier
	v_mfma_f32_16x16x32_bf16 v[126:129], v[150:153], v[182:185], v[126:129]
	v_mfma_f32_16x16x32_bf16 v[122:125], v[158:161], v[182:185], v[122:125]
	v_mfma_f32_16x16x32_bf16 v[110:113], v[150:153], v[190:193], v[110:113]
	v_mfma_f32_16x16x32_bf16 v[106:109], v[158:161], v[190:193], v[106:109]
	v_mfma_f32_16x16x32_bf16 v[92:95], v[150:153], v[198:201], v[92:95]
	v_mfma_f32_16x16x32_bf16 v[88:91], v[158:161], v[198:201], v[88:91]
	v_mfma_f32_16x16x32_bf16 v[76:79], v[150:153], v[206:209], v[76:79]
	v_mfma_f32_16x16x32_bf16 v[72:75], v[158:161], v[206:209], v[72:75]
	v_mfma_f32_16x16x32_bf16 v[126:129], v[154:157], v[186:189], v[126:129]
	v_mfma_f32_16x16x32_bf16 v[122:125], v[162:165], v[186:189], v[122:125]
	v_mfma_f32_16x16x32_bf16 v[110:113], v[154:157], v[194:197], v[110:113]
	v_mfma_f32_16x16x32_bf16 v[106:109], v[162:165], v[194:197], v[106:109]
	v_mfma_f32_16x16x32_bf16 v[92:95], v[154:157], v[202:205], v[92:95]
	v_mfma_f32_16x16x32_bf16 v[88:91], v[162:165], v[202:205], v[88:91]
	v_mfma_f32_16x16x32_bf16 v[76:79], v[154:157], v[210:213], v[76:79]
	v_mfma_f32_16x16x32_bf16 v[72:75], v[162:165], v[210:213], v[72:75]
	v_mfma_f32_16x16x32_bf16 v[118:121], v[166:169], v[182:185], v[118:121]
	v_mfma_f32_16x16x32_bf16 v[114:117], v[174:177], v[182:185], v[114:117]
	v_mfma_f32_16x16x32_bf16 v[102:105], v[166:169], v[190:193], v[102:105]
	v_mfma_f32_16x16x32_bf16 v[98:101], v[174:177], v[190:193], v[98:101]
	v_mfma_f32_16x16x32_bf16 v[84:87], v[166:169], v[198:201], v[84:87]
	v_mfma_f32_16x16x32_bf16 v[80:83], v[174:177], v[198:201], v[80:83]
	v_mfma_f32_16x16x32_bf16 v[68:71], v[166:169], v[206:209], v[68:71]
	v_mfma_f32_16x16x32_bf16 v[64:67], v[174:177], v[206:209], v[64:67]
	v_mfma_f32_16x16x32_bf16 v[118:121], v[170:173], v[186:189], v[118:121]
	v_mfma_f32_16x16x32_bf16 v[114:117], v[178:181], v[186:189], v[114:117]
	v_mfma_f32_16x16x32_bf16 v[102:105], v[170:173], v[194:197], v[102:105]
	v_mfma_f32_16x16x32_bf16 v[98:101], v[178:181], v[194:197], v[98:101]
	v_mfma_f32_16x16x32_bf16 v[84:87], v[170:173], v[202:205], v[84:87]
	v_mfma_f32_16x16x32_bf16 v[80:83], v[178:181], v[202:205], v[80:83]
	v_mfma_f32_16x16x32_bf16 v[68:71], v[170:173], v[210:213], v[68:71]
	v_mfma_f32_16x16x32_bf16 v[64:67], v[178:181], v[210:213], v[64:67]
	s_barrier
	v_mov_b32_e32 v96, v134
	s_add_i32 s63, s63, s54
	ds_read_b128 v[182:185], v149 offset:16384
	ds_read_b128 v[186:189], v149 offset:17408
	ds_read_b128 v[190:193], v149 offset:18432
	ds_read_b128 v[194:197], v149 offset:19456
	ds_read_b128 v[198:201], v149 offset:20480
	ds_read_b128 v[202:205], v149 offset:21504
	ds_read_b128 v[206:209], v149 offset:22528
	ds_read_b128 v[210:213], v149 offset:23552
	s_mov_b32 m0, s63
	s_nop 0
	global_load_lds_dwordx4 v96, s[20:21]
	v_mov_b32_e32 v96, v137
	s_add_i32 m0, s63, 0x2000
	s_add_u32 s64, s20, 0x40000
	global_load_lds_dwordx4 v96, s[20:21]
	s_addc_u32 s65, s21, 0
	v_mov_b32_e32 v96, v134
	s_add_i32 s63, s66, s54
	s_mov_b32 m0, s63
	s_nop 0
	global_load_lds_dwordx4 v96, s[64:65]
	v_mov_b32_e32 v96, v137
	s_add_i32 m0, s63, 0x2000
	s_nop 0
	global_load_lds_dwordx4 v96, s[64:65]
	v_mov_b32_e32 v96, v132
	s_mov_b32 m0, s55
	s_nop 0
	global_load_lds_dwordx4 v96, s[4:5]
	v_mov_b32_e32 v96, v135
	s_mov_b32 m0, s56
	s_nop 0
	global_load_lds_dwordx4 v96, s[4:5]
	s_waitcnt vmcnt(8)
	s_waitcnt lgkmcnt(0)
	s_barrier
	v_mfma_f32_16x16x32_bf16 v[60:63], v[150:153], v[182:185], v[60:63]
	v_mfma_f32_16x16x32_bf16 v[56:59], v[158:161], v[182:185], v[56:59]
	v_mfma_f32_16x16x32_bf16 v[44:47], v[150:153], v[190:193], v[44:47]
	v_mfma_f32_16x16x32_bf16 v[32:35], v[158:161], v[190:193], v[32:35]
	v_mfma_f32_16x16x32_bf16 v[16:19], v[150:153], v[198:201], v[16:19]
	v_mfma_f32_16x16x32_bf16 v[8:11], v[158:161], v[198:201], v[8:11]
	v_mfma_f32_16x16x32_bf16 v[4:7], v[150:153], v[206:209], v[4:7]
	v_mfma_f32_16x16x32_bf16 v[0:3], v[158:161], v[206:209], v[0:3]
	v_mfma_f32_16x16x32_bf16 v[60:63], v[154:157], v[186:189], v[60:63]
	v_mfma_f32_16x16x32_bf16 v[56:59], v[162:165], v[186:189], v[56:59]
	v_mfma_f32_16x16x32_bf16 v[44:47], v[154:157], v[194:197], v[44:47]
	v_mfma_f32_16x16x32_bf16 v[32:35], v[162:165], v[194:197], v[32:35]
	v_mfma_f32_16x16x32_bf16 v[16:19], v[154:157], v[202:205], v[16:19]
	v_mfma_f32_16x16x32_bf16 v[8:11], v[162:165], v[202:205], v[8:11]
	v_mfma_f32_16x16x32_bf16 v[4:7], v[154:157], v[210:213], v[4:7]
	v_mfma_f32_16x16x32_bf16 v[0:3], v[162:165], v[210:213], v[0:3]
	v_mfma_f32_16x16x32_bf16 v[52:55], v[166:169], v[182:185], v[52:55]
	v_mfma_f32_16x16x32_bf16 v[48:51], v[174:177], v[182:185], v[48:51]
	v_mfma_f32_16x16x32_bf16 v[28:31], v[166:169], v[190:193], v[28:31]
	v_mfma_f32_16x16x32_bf16 v[12:15], v[174:177], v[190:193], v[12:15]
	v_mfma_f32_16x16x32_bf16 v[36:39], v[166:169], v[198:201], v[36:39]
	v_mfma_f32_16x16x32_bf16 v[40:43], v[174:177], v[198:201], v[40:43]
	v_mfma_f32_16x16x32_bf16 v[20:23], v[166:169], v[206:209], v[20:23]
	v_mfma_f32_16x16x32_bf16 v[24:27], v[174:177], v[206:209], v[24:27]
	v_mfma_f32_16x16x32_bf16 v[52:55], v[170:173], v[186:189], v[52:55]
	v_mfma_f32_16x16x32_bf16 v[48:51], v[178:181], v[186:189], v[48:51]
	v_mfma_f32_16x16x32_bf16 v[28:31], v[170:173], v[194:197], v[28:31]
	v_mfma_f32_16x16x32_bf16 v[12:15], v[178:181], v[194:197], v[12:15]
	v_mfma_f32_16x16x32_bf16 v[36:39], v[170:173], v[202:205], v[36:39]
	v_mfma_f32_16x16x32_bf16 v[40:43], v[178:181], v[202:205], v[40:43]
	v_mfma_f32_16x16x32_bf16 v[20:23], v[170:173], v[210:213], v[20:23]
	v_mfma_f32_16x16x32_bf16 v[24:27], v[178:181], v[210:213], v[24:27]
	s_barrier
; #define PG8_STAGE(bufoff, gbase, voff) do { _Pragma("unroll") for (int _i = 0; _i < 2; ++_i) \
;         __builtin_amdgcn_global_load_lds((const __attribute__((address_space(1))) unsigned*)((const __attribute__((address_space(1))) char*)(gbase) + (unsigned)lnd_v((int)(voff)[_i])), (LAS unsigned*)(lds + (bufoff) + ldsw + _i * 8192), 16, 0, 0); } while (0)
; #define PG8_LDA(dst, b, h) do { _Pragma("unroll") for (int m = 0; m < 4; ++m) _Pragma("unroll") for (int k = 0; k < 2; ++k) dst[m][k] = *(const LAS bf16x8*)(lds + PG8_SA(b, h) + aoff + m * 2048 + k * 1024); } while (0)
; #define PG8_LDB(dst, b, h) do { _Pragma("unroll") for (int n = 0; n < 2; ++n) _Pragma("unroll") for (int k = 0; k < 2; ++k) dst[n][k] = *(const LAS bf16x8*)(lds + PG8_SB(b, h) + boff + n * 2048 + k * 1024); } while (0)
; #define PG8_MMA(ai, bj, At, Bt) do { __builtin_amdgcn_s_setprio(1); _Pragma("unroll") for (int m = 0; m < 4; ++m) _Pragma("unroll") for (int n = 0; n < 2; ++n) _Pragma("unroll") for (int k = 0; k < 2; ++k) \
;         acc[ai][bj][m][n] = __builtin_amdgcn_mfma_f32_16x16x32_bf16(Bt[n][k], At[m][k], acc[ai][bj][m][n], 0, 0, 0); __builtin_amdgcn_s_setprio(0); } while (0)
; #define PG8_WAIT_V(n) asm volatile("s_waitcnt vmcnt(" #n ")" ::: "memory")
; #define PG8_WAIT_L(n) asm volatile("s_waitcnt lgkmcnt(" #n ")" ::: "memory")
; #define PG8_BAR __builtin_amdgcn_s_barrier()
; #define PG8_SCHED __builtin_amdgcn_sched_barrier(0)
; template <class Desc, class Epi>
; __device__ __forceinline__ void gemm_phase(const int wv_, LAS unsigned char* lds, const Desc& d, const Epi& E) {
;     ...
;             PG8_LDB(B0, 1, 0); PG8_LDB(B1, 1, 1); PG8_SCHED; PG8_LDA(At, 1, 0); PG8_STAGE(PG8_SA(0, 1), a2, sA1);
;             PG8_WAIT_V(8); PG8_WAIT_L(0); PG8_BAR; PG8_MMA(0, 0, At, B0); PG8_MMA(0, 1, At, B1); PG8_BAR; PG8_SCHED;
	s_add_i32 s63, 0, 0x18000
	v_add_u32_e32 v96, s63, v139
	s_add_i32 s64, 0, 0x1c000
	ds_read_b128 v[150:153], v96
	ds_read_b128 v[154:157], v96 offset:1024
	ds_read_b128 v[158:161], v96 offset:2048
	ds_read_b128 v[162:165], v96 offset:3072
	v_add_u32_e32 v96, s64, v139
	ds_read_b128 v[166:169], v96
	ds_read_b128 v[170:173], v96 offset:1024
	ds_read_b128 v[174:177], v96 offset:2048
	ds_read_b128 v[178:181], v96 offset:3072
	v_mov_b32_e32 v96, v133
	s_mov_b32 m0, s57
	ds_read_b128 v[182:185], v149 offset:32768
	ds_read_b128 v[186:189], v149 offset:33792
	ds_read_b128 v[190:193], v149 offset:34816
	ds_read_b128 v[194:197], v149 offset:35840
	ds_read_b128 v[198:201], v149 offset:36864
	ds_read_b128 v[202:205], v149 offset:37888
	ds_read_b128 v[206:209], v149 offset:38912
	ds_read_b128 v[210:213], v149 offset:39936
	s_nop 0
	global_load_lds_dwordx4 v96, s[4:5]
	v_mov_b32_e32 v96, v136
	s_mov_b32 m0, s58
	s_nop 0
	global_load_lds_dwordx4 v96, s[4:5]
	s_waitcnt vmcnt(8)
	s_waitcnt lgkmcnt(0)
	s_barrier
	v_mfma_f32_16x16x32_bf16 v[126:129], v[150:153], v[182:185], v[126:129]
	v_mfma_f32_16x16x32_bf16 v[122:125], v[158:161], v[182:185], v[122:125]
	v_mfma_f32_16x16x32_bf16 v[110:113], v[150:153], v[190:193], v[110:113]
	v_mfma_f32_16x16x32_bf16 v[106:109], v[158:161], v[190:193], v[106:109]
	v_mfma_f32_16x16x32_bf16 v[92:95], v[150:153], v[198:201], v[92:95]
	v_mfma_f32_16x16x32_bf16 v[88:91], v[158:161], v[198:201], v[88:91]
	v_mfma_f32_16x16x32_bf16 v[76:79], v[150:153], v[206:209], v[76:79]
	v_mfma_f32_16x16x32_bf16 v[72:75], v[158:161], v[206:209], v[72:75]
	v_mfma_f32_16x16x32_bf16 v[126:129], v[154:157], v[186:189], v[126:129]
	v_mfma_f32_16x16x32_bf16 v[122:125], v[162:165], v[186:189], v[122:125]
	v_mfma_f32_16x16x32_bf16 v[110:113], v[154:157], v[194:197], v[110:113]
	v_mfma_f32_16x16x32_bf16 v[106:109], v[162:165], v[194:197], v[106:109]
	v_mfma_f32_16x16x32_bf16 v[92:95], v[154:157], v[202:205], v[92:95]
	v_mfma_f32_16x16x32_bf16 v[88:91], v[162:165], v[202:205], v[88:91]
	v_mfma_f32_16x16x32_bf16 v[76:79], v[154:157], v[210:213], v[76:79]
	v_mfma_f32_16x16x32_bf16 v[72:75], v[162:165], v[210:213], v[72:75]
	v_mfma_f32_16x16x32_bf16 v[118:121], v[166:169], v[182:185], v[118:121]
	v_mfma_f32_16x16x32_bf16 v[114:117], v[174:177], v[182:185], v[114:117]
	v_mfma_f32_16x16x32_bf16 v[102:105], v[166:169], v[190:193], v[102:105]
	v_mfma_f32_16x16x32_bf16 v[98:101], v[174:177], v[190:193], v[98:101]
	v_mfma_f32_16x16x32_bf16 v[84:87], v[166:169], v[198:201], v[84:87]
	v_mfma_f32_16x16x32_bf16 v[80:83], v[174:177], v[198:201], v[80:83]
	v_mfma_f32_16x16x32_bf16 v[68:71], v[166:169], v[206:209], v[68:71]
	v_mfma_f32_16x16x32_bf16 v[64:67], v[174:177], v[206:209], v[64:67]
	v_mfma_f32_16x16x32_bf16 v[118:121], v[170:173], v[186:189], v[118:121]
	v_mfma_f32_16x16x32_bf16 v[114:117], v[178:181], v[186:189], v[114:117]
	v_mfma_f32_16x16x32_bf16 v[102:105], v[170:173], v[194:197], v[102:105]
	v_mfma_f32_16x16x32_bf16 v[98:101], v[178:181], v[194:197], v[98:101]
	v_mfma_f32_16x16x32_bf16 v[84:87], v[170:173], v[202:205], v[84:87]
	v_mfma_f32_16x16x32_bf16 v[80:83], v[178:181], v[202:205], v[80:83]
	v_mfma_f32_16x16x32_bf16 v[68:71], v[170:173], v[210:213], v[68:71]
	v_mfma_f32_16x16x32_bf16 v[64:67], v[178:181], v[210:213], v[64:67]
	s_barrier
; #define PG8_STAGE(bufoff, gbase, voff) do { _Pragma("unroll") for (int _i = 0; _i < 2; ++_i) \
;         __builtin_amdgcn_global_load_lds((const __attribute__((address_space(1))) unsigned*)((const __attribute__((address_space(1))) char*)(gbase) + (unsigned)lnd_v((int)(voff)[_i])), (LAS unsigned*)(lds + (bufoff) + ldsw + _i * 8192), 16, 0, 0); } while (0)
; #define PG8_LDA(dst, b, h) do { _Pragma("unroll") for (int m = 0; m < 4; ++m) _Pragma("unroll") for (int k = 0; k < 2; ++k) dst[m][k] = *(const LAS bf16x8*)(lds + PG8_SA(b, h) + aoff + m * 2048 + k * 1024); } while (0)
; #define PG8_MMA(ai, bj, At, Bt) do { __builtin_amdgcn_s_setprio(1); _Pragma("unroll") for (int m = 0; m < 4; ++m) _Pragma("unroll") for (int n = 0; n < 2; ++n) _Pragma("unroll") for (int k = 0; k < 2; ++k) \
;         acc[ai][bj][m][n] = __builtin_amdgcn_mfma_f32_16x16x32_bf16(Bt[n][k], At[m][k], acc[ai][bj][m][n], 0, 0, 0); __builtin_amdgcn_s_setprio(0); } while (0)
; #define PG8_WAIT_V(n) asm volatile("s_waitcnt vmcnt(" #n ")" ::: "memory")
; #define PG8_WAIT_L(n) asm volatile("s_waitcnt lgkmcnt(" #n ")" ::: "memory")
; #define PG8_BAR __builtin_amdgcn_s_barrier()
; #define PG8_SCHED __builtin_amdgcn_sched_barrier(0)
; template <class Desc, class Epi>
; __device__ __forceinline__ void gemm_phase(const int wv_, LAS unsigned char* lds, const Desc& d, const Epi& E) {
;     ...
;             PG8_LDA(At, 1, 1); PG8_STAGE(PG8_SB(1, 0), b3, voffB); PG8_STAGE(PG8_SB(1, 1), b3 + hstepB, voffB); PG8_STAGE(PG8_SA(1, 0), a3, sA0);
;             PG8_WAIT_V(8); PG8_WAIT_L(0); PG8_BAR; PG8_MMA(1, 0, At, B0); PG8_MMA(1, 1, At, B1); PG8_BAR; PG8_SCHED;
;         }
	v_mov_b32_e32 v96, v134
	ds_read_b128 v[182:185], v149 offset:49152
	ds_read_b128 v[186:189], v149 offset:50176
	ds_read_b128 v[190:193], v149 offset:51200
	ds_read_b128 v[194:197], v149 offset:52224
	ds_read_b128 v[198:201], v149 offset:53248
	ds_read_b128 v[202:205], v149 offset:54272
	ds_read_b128 v[206:209], v149 offset:55296
	ds_read_b128 v[210:213], v149 offset:56320
	s_add_i32 s63, s63, s54
	v_lshl_add_u64 v[130:131], s[20:21], 0, v[96:97]
	v_lshl_add_u64 v[130:131], v[130:131], 0, s[30:31]
	s_mov_b32 m0, s63
	v_mov_b32_e32 v96, v137
	global_load_lds_dwordx4 v[130:131], off
	s_add_i32 m0, s63, 0x2000
	s_nop 0
	v_lshl_add_u64 v[130:131], s[20:21], 0, v[96:97]
	s_add_u32 s20, s20, 0x40080
	v_lshl_add_u64 v[130:131], v[130:131], 0, s[30:31]
	s_addc_u32 s21, s21, 0
	v_mov_b32_e32 v96, v134
	s_add_i32 s63, s64, s54
	global_load_lds_dwordx4 v[130:131], off
	s_mov_b32 m0, s63
	s_nop 0
	global_load_lds_dwordx4 v96, s[20:21]
	v_mov_b32_e32 v96, v137
	s_add_i32 m0, s63, 0x2000
	s_nop 0
	global_load_lds_dwordx4 v96, s[20:21]
	v_mov_b32_e32 v96, v132
	s_mov_b32 m0, s59
	v_lshl_add_u64 v[130:131], s[4:5], 0, v[96:97]
	v_lshl_add_u64 v[130:131], v[130:131], 0, s[30:31]
	v_mov_b32_e32 v96, v135
	global_load_lds_dwordx4 v[130:131], off
	s_mov_b32 m0, s60
	v_lshl_add_u64 v[130:131], s[4:5], 0, v[96:97]
	v_lshl_add_u64 v[130:131], v[130:131], 0, s[30:31]
	global_load_lds_dwordx4 v[130:131], off
	s_waitcnt vmcnt(8)
	s_waitcnt lgkmcnt(0)
	s_barrier
	v_mfma_f32_16x16x32_bf16 v[60:63], v[150:153], v[182:185], v[60:63]
	v_mfma_f32_16x16x32_bf16 v[56:59], v[158:161], v[182:185], v[56:59]
	v_mfma_f32_16x16x32_bf16 v[44:47], v[150:153], v[190:193], v[44:47]
	v_mfma_f32_16x16x32_bf16 v[32:35], v[158:161], v[190:193], v[32:35]
	v_mfma_f32_16x16x32_bf16 v[16:19], v[150:153], v[198:201], v[16:19]
	v_mfma_f32_16x16x32_bf16 v[8:11], v[158:161], v[198:201], v[8:11]
	v_mfma_f32_16x16x32_bf16 v[4:7], v[150:153], v[206:209], v[4:7]
	v_mfma_f32_16x16x32_bf16 v[0:3], v[158:161], v[206:209], v[0:3]
	v_mfma_f32_16x16x32_bf16 v[60:63], v[154:157], v[186:189], v[60:63]
	v_mfma_f32_16x16x32_bf16 v[56:59], v[162:165], v[186:189], v[56:59]
	v_mfma_f32_16x16x32_bf16 v[44:47], v[154:157], v[194:197], v[44:47]
	v_mfma_f32_16x16x32_bf16 v[32:35], v[162:165], v[194:197], v[32:35]
	v_mfma_f32_16x16x32_bf16 v[16:19], v[154:157], v[202:205], v[16:19]
	v_mfma_f32_16x16x32_bf16 v[8:11], v[162:165], v[202:205], v[8:11]
	v_mfma_f32_16x16x32_bf16 v[4:7], v[154:157], v[210:213], v[4:7]
	v_mfma_f32_16x16x32_bf16 v[0:3], v[162:165], v[210:213], v[0:3]
	v_mfma_f32_16x16x32_bf16 v[52:55], v[166:169], v[182:185], v[52:55]
	v_mfma_f32_16x16x32_bf16 v[48:51], v[174:177], v[182:185], v[48:51]
	v_mfma_f32_16x16x32_bf16 v[28:31], v[166:169], v[190:193], v[28:31]
	v_mfma_f32_16x16x32_bf16 v[12:15], v[174:177], v[190:193], v[12:15]
	v_mfma_f32_16x16x32_bf16 v[36:39], v[166:169], v[198:201], v[36:39]
	v_mfma_f32_16x16x32_bf16 v[40:43], v[174:177], v[198:201], v[40:43]
	v_mfma_f32_16x16x32_bf16 v[20:23], v[166:169], v[206:209], v[20:23]
	v_mfma_f32_16x16x32_bf16 v[24:27], v[174:177], v[206:209], v[24:27]
	v_mfma_f32_16x16x32_bf16 v[52:55], v[170:173], v[186:189], v[52:55]
	v_mfma_f32_16x16x32_bf16 v[48:51], v[178:181], v[186:189], v[48:51]
	v_mfma_f32_16x16x32_bf16 v[28:31], v[170:173], v[194:197], v[28:31]
	v_mfma_f32_16x16x32_bf16 v[12:15], v[178:181], v[194:197], v[12:15]
	v_mfma_f32_16x16x32_bf16 v[36:39], v[170:173], v[202:205], v[36:39]
	v_mfma_f32_16x16x32_bf16 v[40:43], v[178:181], v[202:205], v[40:43]
	v_mfma_f32_16x16x32_bf16 v[20:23], v[170:173], v[210:213], v[20:23]
	v_mfma_f32_16x16x32_bf16 v[24:27], v[178:181], v[210:213], v[24:27]
	s_barrier
	s_add_i32 s45, s45, 2
	s_add_u32 s2, s2, 0x100
	s_addc_u32 s3, s3, 0
	s_add_u32 s29, s29, 0x100
	s_addc_u32 s43, s43, 0
	s_cmp_gt_u32 s45, 13
	s_cbranch_scc0 .LBB0_747
	s_and_b64 vcc, exec, s[40:41]
	s_cbranch_vccz .LBB0_750
	s_barrier

; #define PG8_STAGE(bufoff, gbase, voff) do { _Pragma("unroll") for (int _i = 0; _i < 2; ++_i) \
;         __builtin_amdgcn_global_load_lds((const __attribute__((address_space(1))) unsigned*)((const __attribute__((address_space(1))) char*)(gbase) + (unsigned)lnd_v((int)(voff)[_i])), (LAS unsigned*)(lds + (bufoff) + ldsw + _i * 8192), 16, 0, 0); } while (0)
; #define PG8_LDA(dst, b, h) do { _Pragma("unroll") for (int m = 0; m < 4; ++m) _Pragma("unroll") for (int k = 0; k < 2; ++k) dst[m][k] = *(const LAS bf16x8*)(lds + PG8_SA(b, h) + aoff + m * 2048 + k * 1024); } while (0)
; #define PG8_LDB(dst, b, h) do { _Pragma("unroll") for (int n = 0; n < 2; ++n) _Pragma("unroll") for (int k = 0; k < 2; ++k) dst[n][k] = *(const LAS bf16x8*)(lds + PG8_SB(b, h) + boff + n * 2048 + k * 1024); } while (0)
; #define PG8_WAIT_V(n) asm volatile("s_waitcnt vmcnt(" #n ")" ::: "memory")
; #define PG8_WAIT_L(n) asm volatile("s_waitcnt lgkmcnt(" #n ")" ::: "memory")
; #define PG8_BAR __builtin_amdgcn_s_barrier()
; template <class Desc, class Epi>
; __device__ __forceinline__ void gemm_phase(const int wv_, LAS unsigned char* lds, const Desc& d, const Epi& E) {
;     ...
;         for (int t = 0; t < nt; t += 2) {
;             const bool last = (t == nt - 2);
;             unsigned sA0[2], sA1[2];
;             if constexpr (Desc::GATHER) { sA0[0] = last ? voffAn[0] : voffA[0]; sA0[1] = last ? voffAn[1] : voffA[1]; sA1[0] = last ? voffAn1[0] : voffA1[0]; sA1[1] = last ? voffAn1[1] : voffA1[1]; }
;             else { sA0[0] = voffA[0]; sA0[1] = voffA[1]; sA1[0] = voffA1[0]; sA1[1] = voffA1[1]; }
;             const char* a1 = cA + (size_t)(t + 1) * kstep;
;             const char* a2 = last ? nA : cA + (size_t)(t + 2) * kstep; const char* b2 = last ? nB : cB + (size_t)(t + 2) * kstep;
;             const char* a3 = a2 + kstep; const char* b3 = b2 + kstep;
;             PG8_LDB(B0, 0, 0); PG8_LDB(B1, 0, 1); PG8_SCHED; PG8_LDA(At, 0, 0); PG8_STAGE(PG8_SA(1, 1), a1, voffA1);
;             PG8_WAIT_V(8); PG8_WAIT_L(0); PG8_BAR; PG8_MMA(0, 0, At, B0); PG8_MMA(0, 1, At, B1); PG8_BAR; PG8_SCHED;
;             PG8_LDA(At, 0, 1); PG8_STAGE(PG8_SB(0, 0), b2, voffB); PG8_STAGE(PG8_SB(0, 1), b2 + hstepB, voffB); PG8_STAGE(PG8_SA(0, 0), a2, sA0);
;             PG8_WAIT_V(8); PG8_WAIT_L(0); PG8_BAR; PG8_MMA(1, 0, At, B0); PG8_MMA(1, 1, At, B1); PG8_BAR; PG8_SCHED;
.LBB0_890:
	s_add_u32 s60, s58, s22
	s_addc_u32 s61, s59, 0
	s_add_u32 s23, s60, 0x100
	s_addc_u32 s24, s61, 0
	s_and_b64 s[4:5], s[20:21], exec
	s_cselect_b32 s4, s50, s23
	s_cselect_b32 s5, s51, s24
	s_add_u32 s22, s56, s22
	s_addc_u32 s23, s57, 0
	s_add_u32 s22, s22, 0x100
	s_addc_u32 s23, s23, 0
	s_add_i32 s82, 0, 0x10000
	s_and_b64 s[20:21], s[20:21], exec
	s_cselect_b32 s21, s53, s23
	s_cselect_b32 s20, s52, s22
	s_add_i32 s23, 0, 0x14000
	v_add_u32_e32 v96, s82, v210
	s_add_i32 s84, s82, s68
	ds_read_b128 v[130:133], v96
	ds_read_b128 v[134:137], v96 offset:1024
	ds_read_b128 v[138:141], v96 offset:2048
	ds_read_b128 v[142:145], v96 offset:3072
	v_add_u32_e32 v96, s23, v210
	s_add_i32 m0, s69, 0xc000
	s_add_i32 s85, s69, 0xe000
	s_add_i32 s80, s84, 0x2000
	ds_read_b128 v[146:149], v96
	ds_read_b128 v[150:153], v96 offset:1024
	ds_read_b128 v[154:157], v96 offset:2048
	ds_read_b128 v[158:161], v96 offset:3072
	s_add_u32 s24, s20, 0x10000
	s_addc_u32 s25, s21, 0
	s_add_i32 s78, 0, 0x18000
	s_add_i32 s81, s23, s68
	s_add_i32 s47, s78, s68
	s_add_i32 s79, s81, 0x2000
	s_add_i32 s49, 0, 0x1c000
	s_add_i32 s29, s47, 0x2000
	s_add_u32 s22, s20, 0x10080
	s_addc_u32 s23, s21, 0
	s_add_i32 s83, s49, s68
	s_add_i32 s82, s83, 0x2000
	v_mov_b32_e32 v96, v204
	ds_read_b128 v[162:165], v222
	ds_read_b128 v[166:169], v222 offset:1024
	ds_read_b128 v[170:173], v222 offset:2048
	ds_read_b128 v[174:177], v222 offset:3072
	ds_read_b128 v[178:181], v222 offset:4096
	ds_read_b128 v[182:185], v222 offset:5120
	ds_read_b128 v[188:191], v222 offset:6144
	ds_read_b128 v[192:195], v222 offset:7168
	s_nop 0
	v_lshl_add_u64 v[196:197], s[60:61], 0, v[96:97]
	v_lshl_add_u64 v[196:197], v[196:197], 0, s[30:31]
	v_mov_b32_e32 v96, v207
	global_load_lds_dwordx4 v[196:197], off
	s_mov_b32 m0, s85
	v_lshl_add_u64 v[196:197], s[60:61], 0, v[96:97]
	v_lshl_add_u64 v[196:197], v[196:197], 0, s[30:31]
	global_load_lds_dwordx4 v[196:197], off
	s_waitcnt vmcnt(8)
	s_waitcnt lgkmcnt(0)
	s_barrier
	v_mfma_f32_16x16x32_bf16 v[126:129], v[130:133], v[162:165], v[126:129]
	v_mfma_f32_16x16x32_bf16 v[122:125], v[138:141], v[162:165], v[122:125]
	v_mfma_f32_16x16x32_bf16 v[118:121], v[130:133], v[170:173], v[118:121]
	v_mfma_f32_16x16x32_bf16 v[114:117], v[138:141], v[170:173], v[114:117]
	v_mfma_f32_16x16x32_bf16 v[110:113], v[130:133], v[178:181], v[110:113]
	v_mfma_f32_16x16x32_bf16 v[106:109], v[138:141], v[178:181], v[106:109]
	v_mfma_f32_16x16x32_bf16 v[102:105], v[130:133], v[188:191], v[102:105]
	v_mfma_f32_16x16x32_bf16 v[98:101], v[138:141], v[188:191], v[98:101]
	v_mfma_f32_16x16x32_bf16 v[126:129], v[134:137], v[166:169], v[126:129]
	v_mfma_f32_16x16x32_bf16 v[122:125], v[142:145], v[166:169], v[122:125]
	v_mfma_f32_16x16x32_bf16 v[118:121], v[134:137], v[174:177], v[118:121]
	v_mfma_f32_16x16x32_bf16 v[114:117], v[142:145], v[174:177], v[114:117]
	v_mfma_f32_16x16x32_bf16 v[110:113], v[134:137], v[182:185], v[110:113]
	v_mfma_f32_16x16x32_bf16 v[106:109], v[142:145], v[182:185], v[106:109]
	v_mfma_f32_16x16x32_bf16 v[102:105], v[134:137], v[192:195], v[102:105]
	v_mfma_f32_16x16x32_bf16 v[98:101], v[142:145], v[192:195], v[98:101]
	v_mfma_f32_16x16x32_bf16 v[60:63], v[146:149], v[162:165], v[60:63]
	v_mfma_f32_16x16x32_bf16 v[56:59], v[154:157], v[162:165], v[56:59]
	v_mfma_f32_16x16x32_bf16 v[52:55], v[146:149], v[170:173], v[52:55]
	v_mfma_f32_16x16x32_bf16 v[48:51], v[154:157], v[170:173], v[48:51]
	v_mfma_f32_16x16x32_bf16 v[44:47], v[146:149], v[178:181], v[44:47]
	v_mfma_f32_16x16x32_bf16 v[40:43], v[154:157], v[178:181], v[40:43]
	v_mfma_f32_16x16x32_bf16 v[36:39], v[146:149], v[188:191], v[36:39]
	v_mfma_f32_16x16x32_bf16 v[32:35], v[154:157], v[188:191], v[32:35]
	v_mfma_f32_16x16x32_bf16 v[60:63], v[150:153], v[166:169], v[60:63]
	v_mfma_f32_16x16x32_bf16 v[56:59], v[158:161], v[166:169], v[56:59]
	v_mfma_f32_16x16x32_bf16 v[52:55], v[150:153], v[174:177], v[52:55]
	v_mfma_f32_16x16x32_bf16 v[48:51], v[158:161], v[174:177], v[48:51]
	v_mfma_f32_16x16x32_bf16 v[44:47], v[150:153], v[182:185], v[44:47]
	v_mfma_f32_16x16x32_bf16 v[40:43], v[158:161], v[182:185], v[40:43]
	v_mfma_f32_16x16x32_bf16 v[36:39], v[150:153], v[192:195], v[36:39]
	v_mfma_f32_16x16x32_bf16 v[32:35], v[158:161], v[192:195], v[32:35]
	s_barrier
	v_mov_b32_e32 v96, v205
	s_mov_b32 m0, s84
	ds_read_b128 v[162:165], v222 offset:16384
	ds_read_b128 v[166:169], v222 offset:17408
	ds_read_b128 v[170:173], v222 offset:18432
	ds_read_b128 v[174:177], v222 offset:19456
	ds_read_b128 v[178:181], v222 offset:20480
	ds_read_b128 v[182:185], v222 offset:21504
	ds_read_b128 v[188:191], v222 offset:22528
	ds_read_b128 v[192:195], v222 offset:23552
	s_nop 0
	global_load_lds_dwordx4 v96, s[20:21]
	v_mov_b32_e32 v96, v208
	s_mov_b32 m0, s80
	s_nop 0
	global_load_lds_dwordx4 v96, s[20:21]
	v_mov_b32_e32 v96, v205
	s_mov_b32 m0, s81
	s_nop 0
	global_load_lds_dwordx4 v96, s[24:25]
	v_mov_b32_e32 v96, v208
	s_mov_b32 m0, s79
	s_nop 0
	global_load_lds_dwordx4 v96, s[24:25]
	v_mov_b32_e32 v96, v187
	s_mov_b32 m0, s69
	s_nop 0
	global_load_lds_dwordx4 v96, s[4:5]
	v_mov_b32_e32 v96, v206
	s_mov_b32 m0, s70
	s_nop 0
	global_load_lds_dwordx4 v96, s[4:5]
	s_waitcnt vmcnt(8)
	s_waitcnt lgkmcnt(0)
	s_barrier
; #define PG8_STAGE(bufoff, gbase, voff) do { _Pragma("unroll") for (int _i = 0; _i < 2; ++_i) \
;         __builtin_amdgcn_global_load_lds((const __attribute__((address_space(1))) unsigned*)((const __attribute__((address_space(1))) char*)(gbase) + (unsigned)lnd_v((int)(voff)[_i])), (LAS unsigned*)(lds + (bufoff) + ldsw + _i * 8192), 16, 0, 0); } while (0)
; #define PG8_LDA(dst, b, h) do { _Pragma("unroll") for (int m = 0; m < 4; ++m) _Pragma("unroll") for (int k = 0; k < 2; ++k) dst[m][k] = *(const LAS bf16x8*)(lds + PG8_SA(b, h) + aoff + m * 2048 + k * 1024); } while (0)
; #define PG8_LDB(dst, b, h) do { _Pragma("unroll") for (int n = 0; n < 2; ++n) _Pragma("unroll") for (int k = 0; k < 2; ++k) dst[n][k] = *(const LAS bf16x8*)(lds + PG8_SB(b, h) + boff + n * 2048 + k * 1024); } while (0)
; #define PG8_MMA(ai, bj, At, Bt) do { __builtin_amdgcn_s_setprio(1); _Pragma("unroll") for (int m = 0; m < 4; ++m) _Pragma("unroll") for (int n = 0; n < 2; ++n) _Pragma("unroll") for (int k = 0; k < 2; ++k) \
;         acc[ai][bj][m][n] = __builtin_amdgcn_mfma_f32_16x16x32_bf16(Bt[n][k], At[m][k], acc[ai][bj][m][n], 0, 0, 0); __builtin_amdgcn_s_setprio(0); } while (0)
; #define PG8_WAIT_V(n) asm volatile("s_waitcnt vmcnt(" #n ")" ::: "memory")
; #define PG8_WAIT_L(n) asm volatile("s_waitcnt lgkmcnt(" #n ")" ::: "memory")
; #define PG8_BAR __builtin_amdgcn_s_barrier()
; #define PG8_SCHED __builtin_amdgcn_sched_barrier(0)
; template <class Desc, class Epi>
; __device__ __forceinline__ void gemm_phase(const int wv_, LAS unsigned char* lds, const Desc& d, const Epi& E) {
;     ...
;             PG8_WAIT_V(8); PG8_WAIT_L(0); PG8_BAR; PG8_MMA(1, 0, At, B0); PG8_MMA(1, 1, At, B1); PG8_BAR; PG8_SCHED;
;             PG8_LDB(B0, 1, 0); PG8_LDB(B1, 1, 1); PG8_SCHED; PG8_LDA(At, 1, 0); PG8_STAGE(PG8_SA(0, 1), a2, sA1);
;             PG8_WAIT_V(8); PG8_WAIT_L(0); PG8_BAR; PG8_MMA(0, 0, At, B0); PG8_MMA(0, 1, At, B1); PG8_BAR; PG8_SCHED;
	v_mfma_f32_16x16x32_bf16 v[92:95], v[130:133], v[162:165], v[92:95]
	v_mfma_f32_16x16x32_bf16 v[88:91], v[138:141], v[162:165], v[88:91]
	v_mfma_f32_16x16x32_bf16 v[84:87], v[130:133], v[170:173], v[84:87]
	v_mfma_f32_16x16x32_bf16 v[80:83], v[138:141], v[170:173], v[80:83]
	v_mfma_f32_16x16x32_bf16 v[76:79], v[130:133], v[178:181], v[76:79]
	v_mfma_f32_16x16x32_bf16 v[72:75], v[138:141], v[178:181], v[72:75]
	v_mfma_f32_16x16x32_bf16 v[68:71], v[130:133], v[188:191], v[68:71]
	v_mfma_f32_16x16x32_bf16 v[64:67], v[138:141], v[188:191], v[64:67]
	v_mfma_f32_16x16x32_bf16 v[92:95], v[134:137], v[166:169], v[92:95]
	v_mfma_f32_16x16x32_bf16 v[88:91], v[142:145], v[166:169], v[88:91]
	v_mfma_f32_16x16x32_bf16 v[84:87], v[134:137], v[174:177], v[84:87]
	v_mfma_f32_16x16x32_bf16 v[80:83], v[142:145], v[174:177], v[80:83]
	v_mfma_f32_16x16x32_bf16 v[76:79], v[134:137], v[182:185], v[76:79]
	v_mfma_f32_16x16x32_bf16 v[72:75], v[142:145], v[182:185], v[72:75]
	v_mfma_f32_16x16x32_bf16 v[68:71], v[134:137], v[192:195], v[68:71]
	v_mfma_f32_16x16x32_bf16 v[64:67], v[142:145], v[192:195], v[64:67]
	v_mfma_f32_16x16x32_bf16 v[28:31], v[146:149], v[162:165], v[28:31]
	v_mfma_f32_16x16x32_bf16 v[24:27], v[154:157], v[162:165], v[24:27]
	v_mfma_f32_16x16x32_bf16 v[12:15], v[146:149], v[170:173], v[12:15]
	v_mfma_f32_16x16x32_bf16 v[8:11], v[154:157], v[170:173], v[8:11]
	v_mfma_f32_16x16x32_bf16 v[20:23], v[146:149], v[178:181], v[20:23]
	v_mfma_f32_16x16x32_bf16 v[16:19], v[154:157], v[178:181], v[16:19]
	v_mfma_f32_16x16x32_bf16 v[4:7], v[146:149], v[188:191], v[4:7]
	v_mfma_f32_16x16x32_bf16 v[0:3], v[154:157], v[188:191], v[0:3]
	v_mfma_f32_16x16x32_bf16 v[28:31], v[150:153], v[166:169], v[28:31]
	v_mfma_f32_16x16x32_bf16 v[24:27], v[158:161], v[166:169], v[24:27]
	v_mfma_f32_16x16x32_bf16 v[12:15], v[150:153], v[174:177], v[12:15]
	v_mfma_f32_16x16x32_bf16 v[8:11], v[158:161], v[174:177], v[8:11]
	v_mfma_f32_16x16x32_bf16 v[20:23], v[150:153], v[182:185], v[20:23]
	v_mfma_f32_16x16x32_bf16 v[16:19], v[158:161], v[182:185], v[16:19]
	v_mfma_f32_16x16x32_bf16 v[4:7], v[150:153], v[192:195], v[4:7]
	v_mfma_f32_16x16x32_bf16 v[0:3], v[158:161], v[192:195], v[0:3]
	s_barrier
	v_add_u32_e32 v96, s78, v210
	ds_read_b128 v[130:133], v96
	ds_read_b128 v[134:137], v96 offset:1024
	ds_read_b128 v[138:141], v96 offset:2048
	ds_read_b128 v[142:145], v96 offset:3072
	v_add_u32_e32 v96, s49, v210
	ds_read_b128 v[146:149], v96
	ds_read_b128 v[150:153], v96 offset:1024
	ds_read_b128 v[154:157], v96 offset:2048
	ds_read_b128 v[158:161], v96 offset:3072
	v_mov_b32_e32 v96, v204
	s_mov_b32 m0, s71
	ds_read_b128 v[162:165], v222 offset:32768
	ds_read_b128 v[166:169], v222 offset:33792
	ds_read_b128 v[170:173], v222 offset:34816
	ds_read_b128 v[174:177], v222 offset:35840
	ds_read_b128 v[178:181], v222 offset:36864
	ds_read_b128 v[182:185], v222 offset:37888
	ds_read_b128 v[188:191], v222 offset:38912
	ds_read_b128 v[192:195], v222 offset:39936
	s_nop 0
	global_load_lds_dwordx4 v96, s[4:5]
	v_mov_b32_e32 v96, v207
	s_mov_b32 m0, s72
	s_nop 0
	global_load_lds_dwordx4 v96, s[4:5]
	s_waitcnt vmcnt(8)
	s_waitcnt lgkmcnt(0)
	s_barrier
	v_mfma_f32_16x16x32_bf16 v[126:129], v[130:133], v[162:165], v[126:129]
	v_mfma_f32_16x16x32_bf16 v[122:125], v[138:141], v[162:165], v[122:125]
	v_mfma_f32_16x16x32_bf16 v[118:121], v[130:133], v[170:173], v[118:121]
	v_mfma_f32_16x16x32_bf16 v[114:117], v[138:141], v[170:173], v[114:117]
	v_mfma_f32_16x16x32_bf16 v[110:113], v[130:133], v[178:181], v[110:113]
	v_mfma_f32_16x16x32_bf16 v[106:109], v[138:141], v[178:181], v[106:109]
	v_mfma_f32_16x16x32_bf16 v[102:105], v[130:133], v[188:191], v[102:105]
	v_mfma_f32_16x16x32_bf16 v[98:101], v[138:141], v[188:191], v[98:101]
	v_mfma_f32_16x16x32_bf16 v[126:129], v[134:137], v[166:169], v[126:129]
	v_mfma_f32_16x16x32_bf16 v[122:125], v[142:145], v[166:169], v[122:125]
	v_mfma_f32_16x16x32_bf16 v[118:121], v[134:137], v[174:177], v[118:121]
	v_mfma_f32_16x16x32_bf16 v[114:117], v[142:145], v[174:177], v[114:117]
	v_mfma_f32_16x16x32_bf16 v[110:113], v[134:137], v[182:185], v[110:113]
	v_mfma_f32_16x16x32_bf16 v[106:109], v[142:145], v[182:185], v[106:109]
	v_mfma_f32_16x16x32_bf16 v[102:105], v[134:137], v[192:195], v[102:105]
	v_mfma_f32_16x16x32_bf16 v[98:101], v[142:145], v[192:195], v[98:101]
	v_mfma_f32_16x16x32_bf16 v[60:63], v[146:149], v[162:165], v[60:63]
	v_mfma_f32_16x16x32_bf16 v[56:59], v[154:157], v[162:165], v[56:59]
	v_mfma_f32_16x16x32_bf16 v[52:55], v[146:149], v[170:173], v[52:55]
	v_mfma_f32_16x16x32_bf16 v[48:51], v[154:157], v[170:173], v[48:51]
	v_mfma_f32_16x16x32_bf16 v[44:47], v[146:149], v[178:181], v[44:47]
	v_mfma_f32_16x16x32_bf16 v[40:43], v[154:157], v[178:181], v[40:43]
	v_mfma_f32_16x16x32_bf16 v[36:39], v[146:149], v[188:191], v[36:39]
	v_mfma_f32_16x16x32_bf16 v[32:35], v[154:157], v[188:191], v[32:35]
	v_mfma_f32_16x16x32_bf16 v[60:63], v[150:153], v[166:169], v[60:63]
	v_mfma_f32_16x16x32_bf16 v[56:59], v[158:161], v[166:169], v[56:59]
	v_mfma_f32_16x16x32_bf16 v[52:55], v[150:153], v[174:177], v[52:55]
	v_mfma_f32_16x16x32_bf16 v[48:51], v[158:161], v[174:177], v[48:51]
	v_mfma_f32_16x16x32_bf16 v[44:47], v[150:153], v[182:185], v[44:47]
	v_mfma_f32_16x16x32_bf16 v[40:43], v[158:161], v[182:185], v[40:43]
	v_mfma_f32_16x16x32_bf16 v[36:39], v[150:153], v[192:195], v[36:39]
	v_mfma_f32_16x16x32_bf16 v[32:35], v[158:161], v[192:195], v[32:35]
	s_barrier
; #define PG8_STAGE(bufoff, gbase, voff) do { _Pragma("unroll") for (int _i = 0; _i < 2; ++_i) \
;         __builtin_amdgcn_global_load_lds((const __attribute__((address_space(1))) unsigned*)((const __attribute__((address_space(1))) char*)(gbase) + (unsigned)lnd_v((int)(voff)[_i])), (LAS unsigned*)(lds + (bufoff) + ldsw + _i * 8192), 16, 0, 0); } while (0)
; #define PG8_LDA(dst, b, h) do { _Pragma("unroll") for (int m = 0; m < 4; ++m) _Pragma("unroll") for (int k = 0; k < 2; ++k) dst[m][k] = *(const LAS bf16x8*)(lds + PG8_SA(b, h) + aoff + m * 2048 + k * 1024); } while (0)
; #define PG8_MMA(ai, bj, At, Bt) do { __builtin_amdgcn_s_setprio(1); _Pragma("unroll") for (int m = 0; m < 4; ++m) _Pragma("unroll") for (int n = 0; n < 2; ++n) _Pragma("unroll") for (int k = 0; k < 2; ++k) \
;         acc[ai][bj][m][n] = __builtin_amdgcn_mfma_f32_16x16x32_bf16(Bt[n][k], At[m][k], acc[ai][bj][m][n], 0, 0, 0); __builtin_amdgcn_s_setprio(0); } while (0)
; #define PG8_WAIT_V(n) asm volatile("s_waitcnt vmcnt(" #n ")" ::: "memory")
; #define PG8_WAIT_L(n) asm volatile("s_waitcnt lgkmcnt(" #n ")" ::: "memory")
; #define PG8_BAR __builtin_amdgcn_s_barrier()
; #define PG8_SCHED __builtin_amdgcn_sched_barrier(0)
; template <class Desc, class Epi>
; __device__ __forceinline__ void gemm_phase(const int wv_, LAS unsigned char* lds, const Desc& d, const Epi& E) {
;     ...
;             PG8_LDA(At, 1, 1); PG8_STAGE(PG8_SB(1, 0), b3, voffB); PG8_STAGE(PG8_SB(1, 1), b3 + hstepB, voffB); PG8_STAGE(PG8_SA(1, 0), a3, sA0);
;             PG8_WAIT_V(8); PG8_WAIT_L(0); PG8_BAR; PG8_MMA(1, 0, At, B0); PG8_MMA(1, 1, At, B1); PG8_BAR; PG8_SCHED;
;         }
	v_mov_b32_e32 v96, v205
	ds_read_b128 v[162:165], v222 offset:49152
	ds_read_b128 v[166:169], v222 offset:50176
	ds_read_b128 v[170:173], v222 offset:51200
	ds_read_b128 v[174:177], v222 offset:52224
	ds_read_b128 v[178:181], v222 offset:53248
	ds_read_b128 v[182:185], v222 offset:54272
	ds_read_b128 v[188:191], v222 offset:55296
	ds_read_b128 v[192:195], v222 offset:56320
	s_mov_b32 m0, s47
	v_lshl_add_u64 v[196:197], s[20:21], 0, v[96:97]
	v_lshl_add_u64 v[196:197], v[196:197], 0, s[30:31]
	v_mov_b32_e32 v96, v208
	global_load_lds_dwordx4 v[196:197], off
	s_mov_b32 m0, s29
	v_lshl_add_u64 v[196:197], s[20:21], 0, v[96:97]
	v_lshl_add_u64 v[196:197], v[196:197], 0, s[30:31]
	v_mov_b32_e32 v96, v205
	global_load_lds_dwordx4 v[196:197], off
	s_mov_b32 m0, s83
	s_nop 0
	global_load_lds_dwordx4 v96, s[22:23]
	v_mov_b32_e32 v96, v208
	s_mov_b32 m0, s82
	s_nop 0
	global_load_lds_dwordx4 v96, s[22:23]
	v_mov_b32_e32 v96, v187
	s_mov_b32 m0, s74
	v_lshl_add_u64 v[196:197], s[4:5], 0, v[96:97]
	v_lshl_add_u64 v[196:197], v[196:197], 0, s[30:31]
	v_mov_b32_e32 v96, v206
	global_load_lds_dwordx4 v[196:197], off
	s_mov_b32 m0, s75
	v_lshl_add_u64 v[196:197], s[4:5], 0, v[96:97]
	v_lshl_add_u64 v[196:197], v[196:197], 0, s[30:31]
	global_load_lds_dwordx4 v[196:197], off
	s_waitcnt vmcnt(8)
	s_waitcnt lgkmcnt(0)
	s_barrier
	v_mfma_f32_16x16x32_bf16 v[92:95], v[130:133], v[162:165], v[92:95]
	v_mfma_f32_16x16x32_bf16 v[88:91], v[138:141], v[162:165], v[88:91]
	v_mfma_f32_16x16x32_bf16 v[84:87], v[130:133], v[170:173], v[84:87]
	v_mfma_f32_16x16x32_bf16 v[80:83], v[138:141], v[170:173], v[80:83]
	v_mfma_f32_16x16x32_bf16 v[76:79], v[130:133], v[178:181], v[76:79]
	v_mfma_f32_16x16x32_bf16 v[72:75], v[138:141], v[178:181], v[72:75]
	v_mfma_f32_16x16x32_bf16 v[68:71], v[130:133], v[188:191], v[68:71]
	v_mfma_f32_16x16x32_bf16 v[64:67], v[138:141], v[188:191], v[64:67]
	v_mfma_f32_16x16x32_bf16 v[92:95], v[134:137], v[166:169], v[92:95]
	v_mfma_f32_16x16x32_bf16 v[88:91], v[142:145], v[166:169], v[88:91]
	v_mfma_f32_16x16x32_bf16 v[84:87], v[134:137], v[174:177], v[84:87]
	v_mfma_f32_16x16x32_bf16 v[80:83], v[142:145], v[174:177], v[80:83]
	v_mfma_f32_16x16x32_bf16 v[76:79], v[134:137], v[182:185], v[76:79]
	v_mfma_f32_16x16x32_bf16 v[72:75], v[142:145], v[182:185], v[72:75]
	v_mfma_f32_16x16x32_bf16 v[68:71], v[134:137], v[192:195], v[68:71]
	v_mfma_f32_16x16x32_bf16 v[64:67], v[142:145], v[192:195], v[64:67]
	v_mfma_f32_16x16x32_bf16 v[28:31], v[146:149], v[162:165], v[28:31]
	v_mfma_f32_16x16x32_bf16 v[24:27], v[154:157], v[162:165], v[24:27]
	v_mfma_f32_16x16x32_bf16 v[12:15], v[146:149], v[170:173], v[12:15]
	v_mfma_f32_16x16x32_bf16 v[8:11], v[154:157], v[170:173], v[8:11]
	v_mfma_f32_16x16x32_bf16 v[20:23], v[146:149], v[178:181], v[20:23]
	v_mfma_f32_16x16x32_bf16 v[16:19], v[154:157], v[178:181], v[16:19]
	v_mfma_f32_16x16x32_bf16 v[4:7], v[146:149], v[188:191], v[4:7]
	v_mfma_f32_16x16x32_bf16 v[0:3], v[154:157], v[188:191], v[0:3]
	v_mfma_f32_16x16x32_bf16 v[28:31], v[150:153], v[166:169], v[28:31]
	v_mfma_f32_16x16x32_bf16 v[24:27], v[158:161], v[166:169], v[24:27]
	v_mfma_f32_16x16x32_bf16 v[12:15], v[150:153], v[174:177], v[12:15]
	v_mfma_f32_16x16x32_bf16 v[8:11], v[158:161], v[174:177], v[8:11]
	v_mfma_f32_16x16x32_bf16 v[20:23], v[150:153], v[182:185], v[20:23]
	v_mfma_f32_16x16x32_bf16 v[16:19], v[158:161], v[182:185], v[16:19]
	v_mfma_f32_16x16x32_bf16 v[4:7], v[150:153], v[192:195], v[4:7]
	v_mfma_f32_16x16x32_bf16 v[0:3], v[158:161], v[192:195], v[0:3]
	s_barrier
	s_movk_i32 s22, 0x100
	s_andn2_b64 vcc, exec, s[2:3]
	s_mov_b64 s[20:21], -1
	s_mov_b64 s[2:3], 0
	s_cbranch_vccz .LBB0_890
	s_and_b64 vcc, exec, s[44:45]
	s_cbranch_vccz .LBB0_893
	s_barrier

; #define PG8_STAGE(bufoff, gbase, voff) do { _Pragma("unroll") for (int _i = 0; _i < 2; ++_i) \
;         __builtin_amdgcn_global_load_lds((const __attribute__((address_space(1))) unsigned*)((const __attribute__((address_space(1))) char*)(gbase) + (unsigned)lnd_v((int)(voff)[_i])), (LAS unsigned*)(lds + (bufoff) + ldsw + _i * 8192), 16, 0, 0); } while (0)
; #define PG8_LDA(dst, b, h) do { _Pragma("unroll") for (int m = 0; m < 4; ++m) _Pragma("unroll") for (int k = 0; k < 2; ++k) dst[m][k] = *(const LAS bf16x8*)(lds + PG8_SA(b, h) + aoff + m * 2048 + k * 1024); } while (0)
; #define PG8_LDB(dst, b, h) do { _Pragma("unroll") for (int n = 0; n < 2; ++n) _Pragma("unroll") for (int k = 0; k < 2; ++k) dst[n][k] = *(const LAS bf16x8*)(lds + PG8_SB(b, h) + boff + n * 2048 + k * 1024); } while (0)
; #define PG8_WAIT_V(n) asm volatile("s_waitcnt vmcnt(" #n ")" ::: "memory")
; #define PG8_WAIT_L(n) asm volatile("s_waitcnt lgkmcnt(" #n ")" ::: "memory")
; #define PG8_BAR __builtin_amdgcn_s_barrier()
; template <class Desc, class Epi>
; __device__ __forceinline__ void gemm_phase(const int wv_, LAS unsigned char* lds, const Desc& d, const Epi& E) {
;     ...
;         for (int t = 0; t < nt; t += 2) {
;             const bool last = (t == nt - 2);
;             unsigned sA0[2], sA1[2];
;             if constexpr (Desc::GATHER) { sA0[0] = last ? voffAn[0] : voffA[0]; sA0[1] = last ? voffAn[1] : voffA[1]; sA1[0] = last ? voffAn1[0] : voffA1[0]; sA1[1] = last ? voffAn1[1] : voffA1[1]; }
;             else { sA0[0] = voffA[0]; sA0[1] = voffA[1]; sA1[0] = voffA1[0]; sA1[1] = voffA1[1]; }
;             const char* a1 = cA + (size_t)(t + 1) * kstep;
;             const char* a2 = last ? nA : cA + (size_t)(t + 2) * kstep; const char* b2 = last ? nB : cB + (size_t)(t + 2) * kstep;
;             const char* a3 = a2 + kstep; const char* b3 = b2 + kstep;
;             PG8_LDB(B0, 0, 0); PG8_LDB(B1, 0, 1); PG8_SCHED; PG8_LDA(At, 0, 0); PG8_STAGE(PG8_SA(1, 1), a1, voffA1);
;             PG8_WAIT_V(8); PG8_WAIT_L(0); PG8_BAR; PG8_MMA(0, 0, At, B0); PG8_MMA(0, 1, At, B1); PG8_BAR; PG8_SCHED;
;             PG8_LDA(At, 0, 1); PG8_STAGE(PG8_SB(0, 0), b2, voffB); PG8_STAGE(PG8_SB(0, 1), b2 + hstepB, voffB); PG8_STAGE(PG8_SA(0, 0), a2, sA0);
;             PG8_WAIT_V(8); PG8_WAIT_L(0); PG8_BAR; PG8_MMA(1, 0, At, B0); PG8_MMA(1, 1, At, B1); PG8_BAR; PG8_SCHED;
.LBB0_917:
	s_add_u32 s54, s52, s22
	s_addc_u32 s55, s53, 0
	s_add_u32 s23, s54, 0x100
	s_addc_u32 s24, s55, 0
	s_and_b64 s[4:5], s[20:21], exec
	s_cselect_b32 s4, s44, s23
	s_cselect_b32 s5, s45, s24
	s_add_u32 s22, s50, s22
	s_addc_u32 s23, s51, 0
	s_add_u32 s22, s22, 0x100
	s_addc_u32 s23, s23, 0
	s_add_i32 s80, 0, 0x10000
	s_and_b64 s[20:21], s[20:21], exec
	s_cselect_b32 s21, s47, s23
	s_cselect_b32 s20, s46, s22
	s_add_i32 s23, 0, 0x14000
	v_add_u32_e32 v96, s80, v139
	s_add_i32 s82, s80, s60
	ds_read_b128 v[150:153], v96
	ds_read_b128 v[154:157], v96 offset:1024
	ds_read_b128 v[158:161], v96 offset:2048
	ds_read_b128 v[162:165], v96 offset:3072
	v_add_u32_e32 v96, s23, v139
	s_add_i32 m0, s61, 0xc000
	s_add_i32 s83, s61, 0xe000
	s_add_i32 s78, s82, 0x2000
	ds_read_b128 v[166:169], v96
	ds_read_b128 v[170:173], v96 offset:1024
	ds_read_b128 v[174:177], v96 offset:2048
	ds_read_b128 v[178:181], v96 offset:3072
	s_add_u32 s24, s20, 0x40000
	s_addc_u32 s25, s21, 0
	s_add_i32 s76, 0, 0x18000
	s_add_i32 s79, s23, s60
	s_add_i32 s74, s76, s60
	s_add_i32 s77, s79, 0x2000
	s_add_i32 s75, 0, 0x1c000
	s_add_i32 s29, s74, 0x2000
	s_add_u32 s22, s20, 0x40080
	s_addc_u32 s23, s21, 0
	s_add_i32 s81, s75, s60
	s_add_i32 s80, s81, 0x2000
	v_mov_b32_e32 v96, v133
	ds_read_b128 v[182:185], v149
	ds_read_b128 v[186:189], v149 offset:1024
	ds_read_b128 v[190:193], v149 offset:2048
	ds_read_b128 v[194:197], v149 offset:3072
	ds_read_b128 v[198:201], v149 offset:4096
	ds_read_b128 v[202:205], v149 offset:5120
	ds_read_b128 v[206:209], v149 offset:6144
	ds_read_b128 v[210:213], v149 offset:7168
	s_nop 0
	v_lshl_add_u64 v[130:131], s[54:55], 0, v[96:97]
	v_lshl_add_u64 v[130:131], v[130:131], 0, s[30:31]
	v_mov_b32_e32 v96, v136
	global_load_lds_dwordx4 v[130:131], off
	s_mov_b32 m0, s83
	v_lshl_add_u64 v[130:131], s[54:55], 0, v[96:97]
	v_lshl_add_u64 v[130:131], v[130:131], 0, s[30:31]
	global_load_lds_dwordx4 v[130:131], off
	s_waitcnt vmcnt(8)
	s_waitcnt lgkmcnt(0)
	s_barrier
	v_mfma_f32_16x16x32_bf16 v[126:129], v[150:153], v[182:185], v[126:129]
	v_mfma_f32_16x16x32_bf16 v[122:125], v[158:161], v[182:185], v[122:125]
	v_mfma_f32_16x16x32_bf16 v[110:113], v[150:153], v[190:193], v[110:113]
	v_mfma_f32_16x16x32_bf16 v[106:109], v[158:161], v[190:193], v[106:109]
	v_mfma_f32_16x16x32_bf16 v[92:95], v[150:153], v[198:201], v[92:95]
	v_mfma_f32_16x16x32_bf16 v[88:91], v[158:161], v[198:201], v[88:91]
	v_mfma_f32_16x16x32_bf16 v[76:79], v[150:153], v[206:209], v[76:79]
	v_mfma_f32_16x16x32_bf16 v[72:75], v[158:161], v[206:209], v[72:75]
	v_mfma_f32_16x16x32_bf16 v[126:129], v[154:157], v[186:189], v[126:129]
	v_mfma_f32_16x16x32_bf16 v[122:125], v[162:165], v[186:189], v[122:125]
	v_mfma_f32_16x16x32_bf16 v[110:113], v[154:157], v[194:197], v[110:113]
	v_mfma_f32_16x16x32_bf16 v[106:109], v[162:165], v[194:197], v[106:109]
	v_mfma_f32_16x16x32_bf16 v[92:95], v[154:157], v[202:205], v[92:95]
	v_mfma_f32_16x16x32_bf16 v[88:91], v[162:165], v[202:205], v[88:91]
	v_mfma_f32_16x16x32_bf16 v[76:79], v[154:157], v[210:213], v[76:79]
	v_mfma_f32_16x16x32_bf16 v[72:75], v[162:165], v[210:213], v[72:75]
	v_mfma_f32_16x16x32_bf16 v[118:121], v[166:169], v[182:185], v[118:121]
	v_mfma_f32_16x16x32_bf16 v[114:117], v[174:177], v[182:185], v[114:117]
	v_mfma_f32_16x16x32_bf16 v[102:105], v[166:169], v[190:193], v[102:105]
	v_mfma_f32_16x16x32_bf16 v[98:101], v[174:177], v[190:193], v[98:101]
	v_mfma_f32_16x16x32_bf16 v[84:87], v[166:169], v[198:201], v[84:87]
	v_mfma_f32_16x16x32_bf16 v[80:83], v[174:177], v[198:201], v[80:83]
	v_mfma_f32_16x16x32_bf16 v[68:71], v[166:169], v[206:209], v[68:71]
	v_mfma_f32_16x16x32_bf16 v[64:67], v[174:177], v[206:209], v[64:67]
	v_mfma_f32_16x16x32_bf16 v[118:121], v[170:173], v[186:189], v[118:121]
	v_mfma_f32_16x16x32_bf16 v[114:117], v[178:181], v[186:189], v[114:117]
	v_mfma_f32_16x16x32_bf16 v[102:105], v[170:173], v[194:197], v[102:105]
	v_mfma_f32_16x16x32_bf16 v[98:101], v[178:181], v[194:197], v[98:101]
	v_mfma_f32_16x16x32_bf16 v[84:87], v[170:173], v[202:205], v[84:87]
	v_mfma_f32_16x16x32_bf16 v[80:83], v[178:181], v[202:205], v[80:83]
	v_mfma_f32_16x16x32_bf16 v[68:71], v[170:173], v[210:213], v[68:71]
	v_mfma_f32_16x16x32_bf16 v[64:67], v[178:181], v[210:213], v[64:67]
	s_barrier
	v_mov_b32_e32 v96, v134
	s_mov_b32 m0, s82
	ds_read_b128 v[182:185], v149 offset:16384
	ds_read_b128 v[186:189], v149 offset:17408
	ds_read_b128 v[190:193], v149 offset:18432
	ds_read_b128 v[194:197], v149 offset:19456
	ds_read_b128 v[198:201], v149 offset:20480
	ds_read_b128 v[202:205], v149 offset:21504
	ds_read_b128 v[206:209], v149 offset:22528
	ds_read_b128 v[210:213], v149 offset:23552
	s_nop 0
	global_load_lds_dwordx4 v96, s[20:21]
	v_mov_b32_e32 v96, v137
	s_mov_b32 m0, s78
	s_nop 0
	global_load_lds_dwordx4 v96, s[20:21]
	v_mov_b32_e32 v96, v134
	s_mov_b32 m0, s79
	s_nop 0
	global_load_lds_dwordx4 v96, s[24:25]
	v_mov_b32_e32 v96, v137
	s_mov_b32 m0, s77
	s_nop 0
	global_load_lds_dwordx4 v96, s[24:25]
	v_mov_b32_e32 v96, v132
	s_mov_b32 m0, s61
	s_nop 0
	global_load_lds_dwordx4 v96, s[4:5]
	v_mov_b32_e32 v96, v135
	s_mov_b32 m0, s63
	s_nop 0
	global_load_lds_dwordx4 v96, s[4:5]
	s_waitcnt vmcnt(8)
	s_waitcnt lgkmcnt(0)
	s_barrier
; #define PG8_STAGE(bufoff, gbase, voff) do { _Pragma("unroll") for (int _i = 0; _i < 2; ++_i) \
;         __builtin_amdgcn_global_load_lds((const __attribute__((address_space(1))) unsigned*)((const __attribute__((address_space(1))) char*)(gbase) + (unsigned)lnd_v((int)(voff)[_i])), (LAS unsigned*)(lds + (bufoff) + ldsw + _i * 8192), 16, 0, 0); } while (0)
; #define PG8_LDA(dst, b, h) do { _Pragma("unroll") for (int m = 0; m < 4; ++m) _Pragma("unroll") for (int k = 0; k < 2; ++k) dst[m][k] = *(const LAS bf16x8*)(lds + PG8_SA(b, h) + aoff + m * 2048 + k * 1024); } while (0)
; #define PG8_LDB(dst, b, h) do { _Pragma("unroll") for (int n = 0; n < 2; ++n) _Pragma("unroll") for (int k = 0; k < 2; ++k) dst[n][k] = *(const LAS bf16x8*)(lds + PG8_SB(b, h) + boff + n * 2048 + k * 1024); } while (0)
; #define PG8_MMA(ai, bj, At, Bt) do { __builtin_amdgcn_s_setprio(1); _Pragma("unroll") for (int m = 0; m < 4; ++m) _Pragma("unroll") for (int n = 0; n < 2; ++n) _Pragma("unroll") for (int k = 0; k < 2; ++k) \
;         acc[ai][bj][m][n] = __builtin_amdgcn_mfma_f32_16x16x32_bf16(Bt[n][k], At[m][k], acc[ai][bj][m][n], 0, 0, 0); __builtin_amdgcn_s_setprio(0); } while (0)
; #define PG8_WAIT_V(n) asm volatile("s_waitcnt vmcnt(" #n ")" ::: "memory")
; #define PG8_WAIT_L(n) asm volatile("s_waitcnt lgkmcnt(" #n ")" ::: "memory")
; #define PG8_BAR __builtin_amdgcn_s_barrier()
; #define PG8_SCHED __builtin_amdgcn_sched_barrier(0)
; template <class Desc, class Epi>
; __device__ __forceinline__ void gemm_phase(const int wv_, LAS unsigned char* lds, const Desc& d, const Epi& E) {
;     ...
;             PG8_WAIT_V(8); PG8_WAIT_L(0); PG8_BAR; PG8_MMA(1, 0, At, B0); PG8_MMA(1, 1, At, B1); PG8_BAR; PG8_SCHED;
;             PG8_LDB(B0, 1, 0); PG8_LDB(B1, 1, 1); PG8_SCHED; PG8_LDA(At, 1, 0); PG8_STAGE(PG8_SA(0, 1), a2, sA1);
;             PG8_WAIT_V(8); PG8_WAIT_L(0); PG8_BAR; PG8_MMA(0, 0, At, B0); PG8_MMA(0, 1, At, B1); PG8_BAR; PG8_SCHED;
	v_mfma_f32_16x16x32_bf16 v[60:63], v[150:153], v[182:185], v[60:63]
	v_mfma_f32_16x16x32_bf16 v[56:59], v[158:161], v[182:185], v[56:59]
	v_mfma_f32_16x16x32_bf16 v[44:47], v[150:153], v[190:193], v[44:47]
	v_mfma_f32_16x16x32_bf16 v[32:35], v[158:161], v[190:193], v[32:35]
	v_mfma_f32_16x16x32_bf16 v[16:19], v[150:153], v[198:201], v[16:19]
	v_mfma_f32_16x16x32_bf16 v[8:11], v[158:161], v[198:201], v[8:11]
	v_mfma_f32_16x16x32_bf16 v[4:7], v[150:153], v[206:209], v[4:7]
	v_mfma_f32_16x16x32_bf16 v[0:3], v[158:161], v[206:209], v[0:3]
	v_mfma_f32_16x16x32_bf16 v[60:63], v[154:157], v[186:189], v[60:63]
	v_mfma_f32_16x16x32_bf16 v[56:59], v[162:165], v[186:189], v[56:59]
	v_mfma_f32_16x16x32_bf16 v[44:47], v[154:157], v[194:197], v[44:47]
	v_mfma_f32_16x16x32_bf16 v[32:35], v[162:165], v[194:197], v[32:35]
	v_mfma_f32_16x16x32_bf16 v[16:19], v[154:157], v[202:205], v[16:19]
	v_mfma_f32_16x16x32_bf16 v[8:11], v[162:165], v[202:205], v[8:11]
	v_mfma_f32_16x16x32_bf16 v[4:7], v[154:157], v[210:213], v[4:7]
	v_mfma_f32_16x16x32_bf16 v[0:3], v[162:165], v[210:213], v[0:3]
	v_mfma_f32_16x16x32_bf16 v[52:55], v[166:169], v[182:185], v[52:55]
	v_mfma_f32_16x16x32_bf16 v[48:51], v[174:177], v[182:185], v[48:51]
	v_mfma_f32_16x16x32_bf16 v[28:31], v[166:169], v[190:193], v[28:31]
	v_mfma_f32_16x16x32_bf16 v[12:15], v[174:177], v[190:193], v[12:15]
	v_mfma_f32_16x16x32_bf16 v[36:39], v[166:169], v[198:201], v[36:39]
	v_mfma_f32_16x16x32_bf16 v[40:43], v[174:177], v[198:201], v[40:43]
	v_mfma_f32_16x16x32_bf16 v[20:23], v[166:169], v[206:209], v[20:23]
	v_mfma_f32_16x16x32_bf16 v[24:27], v[174:177], v[206:209], v[24:27]
	v_mfma_f32_16x16x32_bf16 v[52:55], v[170:173], v[186:189], v[52:55]
	v_mfma_f32_16x16x32_bf16 v[48:51], v[178:181], v[186:189], v[48:51]
	v_mfma_f32_16x16x32_bf16 v[28:31], v[170:173], v[194:197], v[28:31]
	v_mfma_f32_16x16x32_bf16 v[12:15], v[178:181], v[194:197], v[12:15]
	v_mfma_f32_16x16x32_bf16 v[36:39], v[170:173], v[202:205], v[36:39]
	v_mfma_f32_16x16x32_bf16 v[40:43], v[178:181], v[202:205], v[40:43]
	v_mfma_f32_16x16x32_bf16 v[20:23], v[170:173], v[210:213], v[20:23]
	v_mfma_f32_16x16x32_bf16 v[24:27], v[178:181], v[210:213], v[24:27]
	s_barrier
	v_add_u32_e32 v96, s76, v139
	ds_read_b128 v[150:153], v96
	ds_read_b128 v[154:157], v96 offset:1024
	ds_read_b128 v[158:161], v96 offset:2048
	ds_read_b128 v[162:165], v96 offset:3072
	v_add_u32_e32 v96, s75, v139
	ds_read_b128 v[166:169], v96
	ds_read_b128 v[170:173], v96 offset:1024
	ds_read_b128 v[174:177], v96 offset:2048
	ds_read_b128 v[178:181], v96 offset:3072
	v_mov_b32_e32 v96, v133
	s_mov_b32 m0, s64
	ds_read_b128 v[182:185], v149 offset:32768
	ds_read_b128 v[186:189], v149 offset:33792
	ds_read_b128 v[190:193], v149 offset:34816
	ds_read_b128 v[194:197], v149 offset:35840
	ds_read_b128 v[198:201], v149 offset:36864
	ds_read_b128 v[202:205], v149 offset:37888
	ds_read_b128 v[206:209], v149 offset:38912
	ds_read_b128 v[210:213], v149 offset:39936
	s_nop 0
	global_load_lds_dwordx4 v96, s[4:5]
	v_mov_b32_e32 v96, v136
	s_mov_b32 m0, s65
	s_nop 0
	global_load_lds_dwordx4 v96, s[4:5]
	s_waitcnt vmcnt(8)
	s_waitcnt lgkmcnt(0)
	s_barrier
	v_mfma_f32_16x16x32_bf16 v[126:129], v[150:153], v[182:185], v[126:129]
	v_mfma_f32_16x16x32_bf16 v[122:125], v[158:161], v[182:185], v[122:125]
	v_mfma_f32_16x16x32_bf16 v[110:113], v[150:153], v[190:193], v[110:113]
	v_mfma_f32_16x16x32_bf16 v[106:109], v[158:161], v[190:193], v[106:109]
	v_mfma_f32_16x16x32_bf16 v[92:95], v[150:153], v[198:201], v[92:95]
	v_mfma_f32_16x16x32_bf16 v[88:91], v[158:161], v[198:201], v[88:91]
	v_mfma_f32_16x16x32_bf16 v[76:79], v[150:153], v[206:209], v[76:79]
	v_mfma_f32_16x16x32_bf16 v[72:75], v[158:161], v[206:209], v[72:75]
	v_mfma_f32_16x16x32_bf16 v[126:129], v[154:157], v[186:189], v[126:129]
	v_mfma_f32_16x16x32_bf16 v[122:125], v[162:165], v[186:189], v[122:125]
	v_mfma_f32_16x16x32_bf16 v[110:113], v[154:157], v[194:197], v[110:113]
	v_mfma_f32_16x16x32_bf16 v[106:109], v[162:165], v[194:197], v[106:109]
	v_mfma_f32_16x16x32_bf16 v[92:95], v[154:157], v[202:205], v[92:95]
	v_mfma_f32_16x16x32_bf16 v[88:91], v[162:165], v[202:205], v[88:91]
	v_mfma_f32_16x16x32_bf16 v[76:79], v[154:157], v[210:213], v[76:79]
	v_mfma_f32_16x16x32_bf16 v[72:75], v[162:165], v[210:213], v[72:75]
	v_mfma_f32_16x16x32_bf16 v[118:121], v[166:169], v[182:185], v[118:121]
	v_mfma_f32_16x16x32_bf16 v[114:117], v[174:177], v[182:185], v[114:117]
	v_mfma_f32_16x16x32_bf16 v[102:105], v[166:169], v[190:193], v[102:105]
	v_mfma_f32_16x16x32_bf16 v[98:101], v[174:177], v[190:193], v[98:101]
	v_mfma_f32_16x16x32_bf16 v[84:87], v[166:169], v[198:201], v[84:87]
	v_mfma_f32_16x16x32_bf16 v[80:83], v[174:177], v[198:201], v[80:83]
	v_mfma_f32_16x16x32_bf16 v[68:71], v[166:169], v[206:209], v[68:71]
	v_mfma_f32_16x16x32_bf16 v[64:67], v[174:177], v[206:209], v[64:67]
	v_mfma_f32_16x16x32_bf16 v[118:121], v[170:173], v[186:189], v[118:121]
	v_mfma_f32_16x16x32_bf16 v[114:117], v[178:181], v[186:189], v[114:117]
	v_mfma_f32_16x16x32_bf16 v[102:105], v[170:173], v[194:197], v[102:105]
	v_mfma_f32_16x16x32_bf16 v[98:101], v[178:181], v[194:197], v[98:101]
	v_mfma_f32_16x16x32_bf16 v[84:87], v[170:173], v[202:205], v[84:87]
	v_mfma_f32_16x16x32_bf16 v[80:83], v[178:181], v[202:205], v[80:83]
	v_mfma_f32_16x16x32_bf16 v[68:71], v[170:173], v[210:213], v[68:71]
	v_mfma_f32_16x16x32_bf16 v[64:67], v[178:181], v[210:213], v[64:67]
	s_barrier
; #define PG8_STAGE(bufoff, gbase, voff) do { _Pragma("unroll") for (int _i = 0; _i < 2; ++_i) \
;         __builtin_amdgcn_global_load_lds((const __attribute__((address_space(1))) unsigned*)((const __attribute__((address_space(1))) char*)(gbase) + (unsigned)lnd_v((int)(voff)[_i])), (LAS unsigned*)(lds + (bufoff) + ldsw + _i * 8192), 16, 0, 0); } while (0)
; #define PG8_LDA(dst, b, h) do { _Pragma("unroll") for (int m = 0; m < 4; ++m) _Pragma("unroll") for (int k = 0; k < 2; ++k) dst[m][k] = *(const LAS bf16x8*)(lds + PG8_SA(b, h) + aoff + m * 2048 + k * 1024); } while (0)
; #define PG8_MMA(ai, bj, At, Bt) do { __builtin_amdgcn_s_setprio(1); _Pragma("unroll") for (int m = 0; m < 4; ++m) _Pragma("unroll") for (int n = 0; n < 2; ++n) _Pragma("unroll") for (int k = 0; k < 2; ++k) \
;         acc[ai][bj][m][n] = __builtin_amdgcn_mfma_f32_16x16x32_bf16(Bt[n][k], At[m][k], acc[ai][bj][m][n], 0, 0, 0); __builtin_amdgcn_s_setprio(0); } while (0)
; #define PG8_WAIT_V(n) asm volatile("s_waitcnt vmcnt(" #n ")" ::: "memory")
; #define PG8_WAIT_L(n) asm volatile("s_waitcnt lgkmcnt(" #n ")" ::: "memory")
; #define PG8_BAR __builtin_amdgcn_s_barrier()
; #define PG8_SCHED __builtin_amdgcn_sched_barrier(0)
; template <class Desc, class Epi>
; __device__ __forceinline__ void gemm_phase(const int wv_, LAS unsigned char* lds, const Desc& d, const Epi& E) {
;     ...
;             PG8_LDA(At, 1, 1); PG8_STAGE(PG8_SB(1, 0), b3, voffB); PG8_STAGE(PG8_SB(1, 1), b3 + hstepB, voffB); PG8_STAGE(PG8_SA(1, 0), a3, sA0);
;             PG8_WAIT_V(8); PG8_WAIT_L(0); PG8_BAR; PG8_MMA(1, 0, At, B0); PG8_MMA(1, 1, At, B1); PG8_BAR; PG8_SCHED;
;         }
	v_mov_b32_e32 v96, v134
	ds_read_b128 v[182:185], v149 offset:49152
	ds_read_b128 v[186:189], v149 offset:50176
	ds_read_b128 v[190:193], v149 offset:51200
	ds_read_b128 v[194:197], v149 offset:52224
	ds_read_b128 v[198:201], v149 offset:53248
	ds_read_b128 v[202:205], v149 offset:54272
	ds_read_b128 v[206:209], v149 offset:55296
	ds_read_b128 v[210:213], v149 offset:56320
	s_mov_b32 m0, s74
	v_lshl_add_u64 v[130:131], s[20:21], 0, v[96:97]
	v_lshl_add_u64 v[130:131], v[130:131], 0, s[30:31]
	v_mov_b32_e32 v96, v137
	global_load_lds_dwordx4 v[130:131], off
	s_mov_b32 m0, s29
	v_lshl_add_u64 v[130:131], s[20:21], 0, v[96:97]
	v_lshl_add_u64 v[130:131], v[130:131], 0, s[30:31]
	v_mov_b32_e32 v96, v134
	global_load_lds_dwordx4 v[130:131], off
	s_mov_b32 m0, s81
	s_nop 0
	global_load_lds_dwordx4 v96, s[22:23]
	v_mov_b32_e32 v96, v137
	s_mov_b32 m0, s80
	s_nop 0
	global_load_lds_dwordx4 v96, s[22:23]
	v_mov_b32_e32 v96, v132
	s_mov_b32 m0, s68
	v_lshl_add_u64 v[130:131], s[4:5], 0, v[96:97]
	v_lshl_add_u64 v[130:131], v[130:131], 0, s[30:31]
	v_mov_b32_e32 v96, v135
	global_load_lds_dwordx4 v[130:131], off
	s_mov_b32 m0, s69
	v_lshl_add_u64 v[130:131], s[4:5], 0, v[96:97]
	v_lshl_add_u64 v[130:131], v[130:131], 0, s[30:31]
	global_load_lds_dwordx4 v[130:131], off
	s_waitcnt vmcnt(8)
	s_waitcnt lgkmcnt(0)
	s_barrier
	v_mfma_f32_16x16x32_bf16 v[60:63], v[150:153], v[182:185], v[60:63]
	v_mfma_f32_16x16x32_bf16 v[56:59], v[158:161], v[182:185], v[56:59]
	v_mfma_f32_16x16x32_bf16 v[44:47], v[150:153], v[190:193], v[44:47]
	v_mfma_f32_16x16x32_bf16 v[32:35], v[158:161], v[190:193], v[32:35]
	v_mfma_f32_16x16x32_bf16 v[16:19], v[150:153], v[198:201], v[16:19]
	v_mfma_f32_16x16x32_bf16 v[8:11], v[158:161], v[198:201], v[8:11]
	v_mfma_f32_16x16x32_bf16 v[4:7], v[150:153], v[206:209], v[4:7]
	v_mfma_f32_16x16x32_bf16 v[0:3], v[158:161], v[206:209], v[0:3]
	v_mfma_f32_16x16x32_bf16 v[60:63], v[154:157], v[186:189], v[60:63]
	v_mfma_f32_16x16x32_bf16 v[56:59], v[162:165], v[186:189], v[56:59]
	v_mfma_f32_16x16x32_bf16 v[44:47], v[154:157], v[194:197], v[44:47]
	v_mfma_f32_16x16x32_bf16 v[32:35], v[162:165], v[194:197], v[32:35]
	v_mfma_f32_16x16x32_bf16 v[16:19], v[154:157], v[202:205], v[16:19]
	v_mfma_f32_16x16x32_bf16 v[8:11], v[162:165], v[202:205], v[8:11]
	v_mfma_f32_16x16x32_bf16 v[4:7], v[154:157], v[210:213], v[4:7]
	v_mfma_f32_16x16x32_bf16 v[0:3], v[162:165], v[210:213], v[0:3]
	v_mfma_f32_16x16x32_bf16 v[52:55], v[166:169], v[182:185], v[52:55]
	v_mfma_f32_16x16x32_bf16 v[48:51], v[174:177], v[182:185], v[48:51]
	v_mfma_f32_16x16x32_bf16 v[28:31], v[166:169], v[190:193], v[28:31]
	v_mfma_f32_16x16x32_bf16 v[12:15], v[174:177], v[190:193], v[12:15]
	v_mfma_f32_16x16x32_bf16 v[36:39], v[166:169], v[198:201], v[36:39]
	v_mfma_f32_16x16x32_bf16 v[40:43], v[174:177], v[198:201], v[40:43]
	v_mfma_f32_16x16x32_bf16 v[20:23], v[166:169], v[206:209], v[20:23]
	v_mfma_f32_16x16x32_bf16 v[24:27], v[174:177], v[206:209], v[24:27]
	v_mfma_f32_16x16x32_bf16 v[52:55], v[170:173], v[186:189], v[52:55]
	v_mfma_f32_16x16x32_bf16 v[48:51], v[178:181], v[186:189], v[48:51]
	v_mfma_f32_16x16x32_bf16 v[28:31], v[170:173], v[194:197], v[28:31]
	v_mfma_f32_16x16x32_bf16 v[12:15], v[178:181], v[194:197], v[12:15]
	v_mfma_f32_16x16x32_bf16 v[36:39], v[170:173], v[202:205], v[36:39]
	v_mfma_f32_16x16x32_bf16 v[40:43], v[178:181], v[202:205], v[40:43]
	v_mfma_f32_16x16x32_bf16 v[20:23], v[170:173], v[210:213], v[20:23]
	v_mfma_f32_16x16x32_bf16 v[24:27], v[178:181], v[210:213], v[24:27]
	s_barrier
	s_movk_i32 s22, 0x100
	s_andn2_b64 vcc, exec, s[2:3]
	s_mov_b64 s[20:21], -1
	s_mov_b64 s[2:3], 0
	s_cbranch_vccz .LBB0_917
	s_and_b64 vcc, exec, s[42:43]
	s_cbranch_vccz .LBB0_920
	s_barrier

; #define PG8_STAGE(bufoff, gbase, voff) do { _Pragma("unroll") for (int _i = 0; _i < 2; ++_i) \
;         __builtin_amdgcn_global_load_lds((const __attribute__((address_space(1))) unsigned*)((const __attribute__((address_space(1))) char*)(gbase) + (unsigned)lnd_v((int)(voff)[_i])), (LAS unsigned*)(lds + (bufoff) + ldsw + _i * 8192), 16, 0, 0); } while (0)
; #define PG8_LDA(dst, b, h) do { _Pragma("unroll") for (int m = 0; m < 4; ++m) _Pragma("unroll") for (int k = 0; k < 2; ++k) dst[m][k] = *(const LAS bf16x8*)(lds + PG8_SA(b, h) + aoff + m * 2048 + k * 1024); } while (0)
; #define PG8_LDB(dst, b, h) do { _Pragma("unroll") for (int n = 0; n < 2; ++n) _Pragma("unroll") for (int k = 0; k < 2; ++k) dst[n][k] = *(const LAS bf16x8*)(lds + PG8_SB(b, h) + boff + n * 2048 + k * 1024); } while (0)
; #define PG8_WAIT_V(n) asm volatile("s_waitcnt vmcnt(" #n ")" ::: "memory")
; #define PG8_WAIT_L(n) asm volatile("s_waitcnt lgkmcnt(" #n ")" ::: "memory")
; #define PG8_BAR __builtin_amdgcn_s_barrier()
; template <class Desc, class Epi>
; __device__ __forceinline__ void gemm_phase(const int wv_, LAS unsigned char* lds, const Desc& d, const Epi& E) {
;     ...
;         for (int t = 0; t < nt; t += 2) {
;             const bool last = (t == nt - 2);
;             unsigned sA0[2], sA1[2];
;             if constexpr (Desc::GATHER) { sA0[0] = last ? voffAn[0] : voffA[0]; sA0[1] = last ? voffAn[1] : voffA[1]; sA1[0] = last ? voffAn1[0] : voffA1[0]; sA1[1] = last ? voffAn1[1] : voffA1[1]; }
;             else { sA0[0] = voffA[0]; sA0[1] = voffA[1]; sA1[0] = voffA1[0]; sA1[1] = voffA1[1]; }
;             const char* a1 = cA + (size_t)(t + 1) * kstep;
;             const char* a2 = last ? nA : cA + (size_t)(t + 2) * kstep; const char* b2 = last ? nB : cB + (size_t)(t + 2) * kstep;
;             const char* a3 = a2 + kstep; const char* b3 = b2 + kstep;
;             PG8_LDB(B0, 0, 0); PG8_LDB(B1, 0, 1); PG8_SCHED; PG8_LDA(At, 0, 0); PG8_STAGE(PG8_SA(1, 1), a1, voffA1);
;             PG8_WAIT_V(8); PG8_WAIT_L(0); PG8_BAR; PG8_MMA(0, 0, At, B0); PG8_MMA(0, 1, At, B1); PG8_BAR; PG8_SCHED;
;             PG8_LDA(At, 0, 1); PG8_STAGE(PG8_SB(0, 0), b2, voffB); PG8_STAGE(PG8_SB(0, 1), b2 + hstepB, voffB); PG8_STAGE(PG8_SA(0, 0), a2, sA0);
;             PG8_WAIT_V(8); PG8_WAIT_L(0); PG8_BAR; PG8_MMA(1, 0, At, B0); PG8_MMA(1, 1, At, B1); PG8_BAR; PG8_SCHED;
.LBB0_937:
	s_add_u32 s52, s50, s22
	s_addc_u32 s53, s51, 0
	s_add_u32 s23, s52, 0x100
	s_addc_u32 s24, s53, 0
	s_and_b64 s[4:5], s[20:21], exec
	s_cselect_b32 s4, s42, s23
	s_cselect_b32 s5, s43, s24
	s_add_u32 s22, s48, s22
	s_addc_u32 s23, s49, 0
	s_add_u32 s22, s22, 0x100
	s_addc_u32 s23, s23, 0
	s_add_i32 s77, 0, 0x10000
	s_and_b64 s[20:21], s[20:21], exec
	s_cselect_b32 s21, s45, s23
	s_cselect_b32 s20, s44, s22
	s_add_i32 s23, 0, 0x14000
	v_add_u32_e32 v96, s77, v139
	s_add_i32 s79, s77, s59
	ds_read_b128 v[150:153], v96
	ds_read_b128 v[154:157], v96 offset:1024
	ds_read_b128 v[158:161], v96 offset:2048
	ds_read_b128 v[162:165], v96 offset:3072
	v_add_u32_e32 v96, s23, v139
	s_add_i32 m0, s60, 0xc000
	s_add_i32 s80, s60, 0xe000
	s_add_i32 s75, s79, 0x2000
	ds_read_b128 v[166:169], v96
	ds_read_b128 v[170:173], v96 offset:1024
	ds_read_b128 v[174:177], v96 offset:2048
	ds_read_b128 v[178:181], v96 offset:3072
	s_add_u32 s24, s20, 0x40000
	s_addc_u32 s25, s21, 0
	s_add_i32 s73, 0, 0x18000
	s_add_i32 s76, s23, s59
	s_add_i32 s71, s73, s59
	s_add_i32 s74, s76, 0x2000
	s_add_i32 s72, 0, 0x1c000
	s_add_i32 s29, s71, 0x2000
	s_add_u32 s22, s20, 0x40080
	s_addc_u32 s23, s21, 0
	s_add_i32 s78, s72, s59
	s_add_i32 s77, s78, 0x2000
	v_mov_b32_e32 v96, v133
	ds_read_b128 v[182:185], v149
	ds_read_b128 v[186:189], v149 offset:1024
	ds_read_b128 v[190:193], v149 offset:2048
	ds_read_b128 v[194:197], v149 offset:3072
	ds_read_b128 v[198:201], v149 offset:4096
	ds_read_b128 v[202:205], v149 offset:5120
	ds_read_b128 v[206:209], v149 offset:6144
	ds_read_b128 v[210:213], v149 offset:7168
	s_nop 0
	v_lshl_add_u64 v[130:131], s[52:53], 0, v[96:97]
	v_lshl_add_u64 v[130:131], v[130:131], 0, s[30:31]
	v_mov_b32_e32 v96, v136
	global_load_lds_dwordx4 v[130:131], off
	s_mov_b32 m0, s80
	v_lshl_add_u64 v[130:131], s[52:53], 0, v[96:97]
	v_lshl_add_u64 v[130:131], v[130:131], 0, s[30:31]
	global_load_lds_dwordx4 v[130:131], off
	s_waitcnt vmcnt(8)
	s_waitcnt lgkmcnt(0)
	s_barrier
	v_mfma_f32_16x16x32_bf16 v[126:129], v[150:153], v[182:185], v[126:129]
	v_mfma_f32_16x16x32_bf16 v[122:125], v[158:161], v[182:185], v[122:125]
	v_mfma_f32_16x16x32_bf16 v[110:113], v[150:153], v[190:193], v[110:113]
	v_mfma_f32_16x16x32_bf16 v[106:109], v[158:161], v[190:193], v[106:109]
	v_mfma_f32_16x16x32_bf16 v[92:95], v[150:153], v[198:201], v[92:95]
	v_mfma_f32_16x16x32_bf16 v[88:91], v[158:161], v[198:201], v[88:91]
	v_mfma_f32_16x16x32_bf16 v[76:79], v[150:153], v[206:209], v[76:79]
	v_mfma_f32_16x16x32_bf16 v[72:75], v[158:161], v[206:209], v[72:75]
	v_mfma_f32_16x16x32_bf16 v[126:129], v[154:157], v[186:189], v[126:129]
	v_mfma_f32_16x16x32_bf16 v[122:125], v[162:165], v[186:189], v[122:125]
	v_mfma_f32_16x16x32_bf16 v[110:113], v[154:157], v[194:197], v[110:113]
	v_mfma_f32_16x16x32_bf16 v[106:109], v[162:165], v[194:197], v[106:109]
	v_mfma_f32_16x16x32_bf16 v[92:95], v[154:157], v[202:205], v[92:95]
	v_mfma_f32_16x16x32_bf16 v[88:91], v[162:165], v[202:205], v[88:91]
	v_mfma_f32_16x16x32_bf16 v[76:79], v[154:157], v[210:213], v[76:79]
	v_mfma_f32_16x16x32_bf16 v[72:75], v[162:165], v[210:213], v[72:75]
	v_mfma_f32_16x16x32_bf16 v[118:121], v[166:169], v[182:185], v[118:121]
	v_mfma_f32_16x16x32_bf16 v[114:117], v[174:177], v[182:185], v[114:117]
	v_mfma_f32_16x16x32_bf16 v[102:105], v[166:169], v[190:193], v[102:105]
	v_mfma_f32_16x16x32_bf16 v[98:101], v[174:177], v[190:193], v[98:101]
	v_mfma_f32_16x16x32_bf16 v[84:87], v[166:169], v[198:201], v[84:87]
	v_mfma_f32_16x16x32_bf16 v[80:83], v[174:177], v[198:201], v[80:83]
	v_mfma_f32_16x16x32_bf16 v[68:71], v[166:169], v[206:209], v[68:71]
	v_mfma_f32_16x16x32_bf16 v[64:67], v[174:177], v[206:209], v[64:67]
	v_mfma_f32_16x16x32_bf16 v[118:121], v[170:173], v[186:189], v[118:121]
	v_mfma_f32_16x16x32_bf16 v[114:117], v[178:181], v[186:189], v[114:117]
	v_mfma_f32_16x16x32_bf16 v[102:105], v[170:173], v[194:197], v[102:105]
	v_mfma_f32_16x16x32_bf16 v[98:101], v[178:181], v[194:197], v[98:101]
	v_mfma_f32_16x16x32_bf16 v[84:87], v[170:173], v[202:205], v[84:87]
	v_mfma_f32_16x16x32_bf16 v[80:83], v[178:181], v[202:205], v[80:83]
	v_mfma_f32_16x16x32_bf16 v[68:71], v[170:173], v[210:213], v[68:71]
	v_mfma_f32_16x16x32_bf16 v[64:67], v[178:181], v[210:213], v[64:67]
	s_barrier
	v_mov_b32_e32 v96, v134
	s_mov_b32 m0, s79
	ds_read_b128 v[182:185], v149 offset:16384
	ds_read_b128 v[186:189], v149 offset:17408
	ds_read_b128 v[190:193], v149 offset:18432
	ds_read_b128 v[194:197], v149 offset:19456
	ds_read_b128 v[198:201], v149 offset:20480
	ds_read_b128 v[202:205], v149 offset:21504
	ds_read_b128 v[206:209], v149 offset:22528
	ds_read_b128 v[210:213], v149 offset:23552
	s_nop 0
	global_load_lds_dwordx4 v96, s[20:21]
	v_mov_b32_e32 v96, v137
	s_mov_b32 m0, s75
	s_nop 0
	global_load_lds_dwordx4 v96, s[20:21]
	v_mov_b32_e32 v96, v134
	s_mov_b32 m0, s76
	s_nop 0
	global_load_lds_dwordx4 v96, s[24:25]
	v_mov_b32_e32 v96, v137
	s_mov_b32 m0, s74
	s_nop 0
	global_load_lds_dwordx4 v96, s[24:25]
	v_mov_b32_e32 v96, v132
	s_mov_b32 m0, s60
	s_nop 0
	global_load_lds_dwordx4 v96, s[4:5]
	v_mov_b32_e32 v96, v135
	s_mov_b32 m0, s61
	s_nop 0
	global_load_lds_dwordx4 v96, s[4:5]
	s_waitcnt vmcnt(8)
	s_waitcnt lgkmcnt(0)
	s_barrier
; #define PG8_STAGE(bufoff, gbase, voff) do { _Pragma("unroll") for (int _i = 0; _i < 2; ++_i) \
;         __builtin_amdgcn_global_load_lds((const __attribute__((address_space(1))) unsigned*)((const __attribute__((address_space(1))) char*)(gbase) + (unsigned)lnd_v((int)(voff)[_i])), (LAS unsigned*)(lds + (bufoff) + ldsw + _i * 8192), 16, 0, 0); } while (0)
; #define PG8_LDA(dst, b, h) do { _Pragma("unroll") for (int m = 0; m < 4; ++m) _Pragma("unroll") for (int k = 0; k < 2; ++k) dst[m][k] = *(const LAS bf16x8*)(lds + PG8_SA(b, h) + aoff + m * 2048 + k * 1024); } while (0)
; #define PG8_LDB(dst, b, h) do { _Pragma("unroll") for (int n = 0; n < 2; ++n) _Pragma("unroll") for (int k = 0; k < 2; ++k) dst[n][k] = *(const LAS bf16x8*)(lds + PG8_SB(b, h) + boff + n * 2048 + k * 1024); } while (0)
; #define PG8_MMA(ai, bj, At, Bt) do { __builtin_amdgcn_s_setprio(1); _Pragma("unroll") for (int m = 0; m < 4; ++m) _Pragma("unroll") for (int n = 0; n < 2; ++n) _Pragma("unroll") for (int k = 0; k < 2; ++k) \
;         acc[ai][bj][m][n] = __builtin_amdgcn_mfma_f32_16x16x32_bf16(Bt[n][k], At[m][k], acc[ai][bj][m][n], 0, 0, 0); __builtin_amdgcn_s_setprio(0); } while (0)
; #define PG8_WAIT_V(n) asm volatile("s_waitcnt vmcnt(" #n ")" ::: "memory")
; #define PG8_WAIT_L(n) asm volatile("s_waitcnt lgkmcnt(" #n ")" ::: "memory")
; #define PG8_BAR __builtin_amdgcn_s_barrier()
; #define PG8_SCHED __builtin_amdgcn_sched_barrier(0)
; template <class Desc, class Epi>
; __device__ __forceinline__ void gemm_phase(const int wv_, LAS unsigned char* lds, const Desc& d, const Epi& E) {
;     ...
;             PG8_WAIT_V(8); PG8_WAIT_L(0); PG8_BAR; PG8_MMA(1, 0, At, B0); PG8_MMA(1, 1, At, B1); PG8_BAR; PG8_SCHED;
;             PG8_LDB(B0, 1, 0); PG8_LDB(B1, 1, 1); PG8_SCHED; PG8_LDA(At, 1, 0); PG8_STAGE(PG8_SA(0, 1), a2, sA1);
;             PG8_WAIT_V(8); PG8_WAIT_L(0); PG8_BAR; PG8_MMA(0, 0, At, B0); PG8_MMA(0, 1, At, B1); PG8_BAR; PG8_SCHED;
	v_mfma_f32_16x16x32_bf16 v[60:63], v[150:153], v[182:185], v[60:63]
	v_mfma_f32_16x16x32_bf16 v[56:59], v[158:161], v[182:185], v[56:59]
	v_mfma_f32_16x16x32_bf16 v[44:47], v[150:153], v[190:193], v[44:47]
	v_mfma_f32_16x16x32_bf16 v[32:35], v[158:161], v[190:193], v[32:35]
	v_mfma_f32_16x16x32_bf16 v[16:19], v[150:153], v[198:201], v[16:19]
	v_mfma_f32_16x16x32_bf16 v[8:11], v[158:161], v[198:201], v[8:11]
	v_mfma_f32_16x16x32_bf16 v[4:7], v[150:153], v[206:209], v[4:7]
	v_mfma_f32_16x16x32_bf16 v[0:3], v[158:161], v[206:209], v[0:3]
	v_mfma_f32_16x16x32_bf16 v[60:63], v[154:157], v[186:189], v[60:63]
	v_mfma_f32_16x16x32_bf16 v[56:59], v[162:165], v[186:189], v[56:59]
	v_mfma_f32_16x16x32_bf16 v[44:47], v[154:157], v[194:197], v[44:47]
	v_mfma_f32_16x16x32_bf16 v[32:35], v[162:165], v[194:197], v[32:35]
	v_mfma_f32_16x16x32_bf16 v[16:19], v[154:157], v[202:205], v[16:19]
	v_mfma_f32_16x16x32_bf16 v[8:11], v[162:165], v[202:205], v[8:11]
	v_mfma_f32_16x16x32_bf16 v[4:7], v[154:157], v[210:213], v[4:7]
	v_mfma_f32_16x16x32_bf16 v[0:3], v[162:165], v[210:213], v[0:3]
	v_mfma_f32_16x16x32_bf16 v[52:55], v[166:169], v[182:185], v[52:55]
	v_mfma_f32_16x16x32_bf16 v[48:51], v[174:177], v[182:185], v[48:51]
	v_mfma_f32_16x16x32_bf16 v[28:31], v[166:169], v[190:193], v[28:31]
	v_mfma_f32_16x16x32_bf16 v[12:15], v[174:177], v[190:193], v[12:15]
	v_mfma_f32_16x16x32_bf16 v[36:39], v[166:169], v[198:201], v[36:39]
	v_mfma_f32_16x16x32_bf16 v[40:43], v[174:177], v[198:201], v[40:43]
	v_mfma_f32_16x16x32_bf16 v[20:23], v[166:169], v[206:209], v[20:23]
	v_mfma_f32_16x16x32_bf16 v[24:27], v[174:177], v[206:209], v[24:27]
	v_mfma_f32_16x16x32_bf16 v[52:55], v[170:173], v[186:189], v[52:55]
	v_mfma_f32_16x16x32_bf16 v[48:51], v[178:181], v[186:189], v[48:51]
	v_mfma_f32_16x16x32_bf16 v[28:31], v[170:173], v[194:197], v[28:31]
	v_mfma_f32_16x16x32_bf16 v[12:15], v[178:181], v[194:197], v[12:15]
	v_mfma_f32_16x16x32_bf16 v[36:39], v[170:173], v[202:205], v[36:39]
	v_mfma_f32_16x16x32_bf16 v[40:43], v[178:181], v[202:205], v[40:43]
	v_mfma_f32_16x16x32_bf16 v[20:23], v[170:173], v[210:213], v[20:23]
	v_mfma_f32_16x16x32_bf16 v[24:27], v[178:181], v[210:213], v[24:27]
	s_barrier
	v_add_u32_e32 v96, s73, v139
	ds_read_b128 v[150:153], v96
	ds_read_b128 v[154:157], v96 offset:1024
	ds_read_b128 v[158:161], v96 offset:2048
	ds_read_b128 v[162:165], v96 offset:3072
	v_add_u32_e32 v96, s72, v139
	ds_read_b128 v[166:169], v96
	ds_read_b128 v[170:173], v96 offset:1024
	ds_read_b128 v[174:177], v96 offset:2048
	ds_read_b128 v[178:181], v96 offset:3072
	v_mov_b32_e32 v96, v133
	s_mov_b32 m0, s63
	ds_read_b128 v[182:185], v149 offset:32768
	ds_read_b128 v[186:189], v149 offset:33792
	ds_read_b128 v[190:193], v149 offset:34816
	ds_read_b128 v[194:197], v149 offset:35840
	ds_read_b128 v[198:201], v149 offset:36864
	ds_read_b128 v[202:205], v149 offset:37888
	ds_read_b128 v[206:209], v149 offset:38912
	ds_read_b128 v[210:213], v149 offset:39936
	s_nop 0
	global_load_lds_dwordx4 v96, s[4:5]
	v_mov_b32_e32 v96, v136
	s_mov_b32 m0, s64
	s_nop 0
	global_load_lds_dwordx4 v96, s[4:5]
	s_waitcnt vmcnt(8)
	s_waitcnt lgkmcnt(0)
	s_barrier
	v_mfma_f32_16x16x32_bf16 v[126:129], v[150:153], v[182:185], v[126:129]
	v_mfma_f32_16x16x32_bf16 v[122:125], v[158:161], v[182:185], v[122:125]
	v_mfma_f32_16x16x32_bf16 v[110:113], v[150:153], v[190:193], v[110:113]
	v_mfma_f32_16x16x32_bf16 v[106:109], v[158:161], v[190:193], v[106:109]
	v_mfma_f32_16x16x32_bf16 v[92:95], v[150:153], v[198:201], v[92:95]
	v_mfma_f32_16x16x32_bf16 v[88:91], v[158:161], v[198:201], v[88:91]
	v_mfma_f32_16x16x32_bf16 v[76:79], v[150:153], v[206:209], v[76:79]
	v_mfma_f32_16x16x32_bf16 v[72:75], v[158:161], v[206:209], v[72:75]
	v_mfma_f32_16x16x32_bf16 v[126:129], v[154:157], v[186:189], v[126:129]
	v_mfma_f32_16x16x32_bf16 v[122:125], v[162:165], v[186:189], v[122:125]
	v_mfma_f32_16x16x32_bf16 v[110:113], v[154:157], v[194:197], v[110:113]
	v_mfma_f32_16x16x32_bf16 v[106:109], v[162:165], v[194:197], v[106:109]
	v_mfma_f32_16x16x32_bf16 v[92:95], v[154:157], v[202:205], v[92:95]
	v_mfma_f32_16x16x32_bf16 v[88:91], v[162:165], v[202:205], v[88:91]
	v_mfma_f32_16x16x32_bf16 v[76:79], v[154:157], v[210:213], v[76:79]
	v_mfma_f32_16x16x32_bf16 v[72:75], v[162:165], v[210:213], v[72:75]
	v_mfma_f32_16x16x32_bf16 v[118:121], v[166:169], v[182:185], v[118:121]
	v_mfma_f32_16x16x32_bf16 v[114:117], v[174:177], v[182:185], v[114:117]
	v_mfma_f32_16x16x32_bf16 v[102:105], v[166:169], v[190:193], v[102:105]
	v_mfma_f32_16x16x32_bf16 v[98:101], v[174:177], v[190:193], v[98:101]
	v_mfma_f32_16x16x32_bf16 v[84:87], v[166:169], v[198:201], v[84:87]
	v_mfma_f32_16x16x32_bf16 v[80:83], v[174:177], v[198:201], v[80:83]
	v_mfma_f32_16x16x32_bf16 v[68:71], v[166:169], v[206:209], v[68:71]
	v_mfma_f32_16x16x32_bf16 v[64:67], v[174:177], v[206:209], v[64:67]
	v_mfma_f32_16x16x32_bf16 v[118:121], v[170:173], v[186:189], v[118:121]
	v_mfma_f32_16x16x32_bf16 v[114:117], v[178:181], v[186:189], v[114:117]
	v_mfma_f32_16x16x32_bf16 v[102:105], v[170:173], v[194:197], v[102:105]
	v_mfma_f32_16x16x32_bf16 v[98:101], v[178:181], v[194:197], v[98:101]
	v_mfma_f32_16x16x32_bf16 v[84:87], v[170:173], v[202:205], v[84:87]
	v_mfma_f32_16x16x32_bf16 v[80:83], v[178:181], v[202:205], v[80:83]
	v_mfma_f32_16x16x32_bf16 v[68:71], v[170:173], v[210:213], v[68:71]
	v_mfma_f32_16x16x32_bf16 v[64:67], v[178:181], v[210:213], v[64:67]
	s_barrier
; #define PG8_STAGE(bufoff, gbase, voff) do { _Pragma("unroll") for (int _i = 0; _i < 2; ++_i) \
;         __builtin_amdgcn_global_load_lds((const __attribute__((address_space(1))) unsigned*)((const __attribute__((address_space(1))) char*)(gbase) + (unsigned)lnd_v((int)(voff)[_i])), (LAS unsigned*)(lds + (bufoff) + ldsw + _i * 8192), 16, 0, 0); } while (0)
; #define PG8_LDA(dst, b, h) do { _Pragma("unroll") for (int m = 0; m < 4; ++m) _Pragma("unroll") for (int k = 0; k < 2; ++k) dst[m][k] = *(const LAS bf16x8*)(lds + PG8_SA(b, h) + aoff + m * 2048 + k * 1024); } while (0)
; #define PG8_MMA(ai, bj, At, Bt) do { __builtin_amdgcn_s_setprio(1); _Pragma("unroll") for (int m = 0; m < 4; ++m) _Pragma("unroll") for (int n = 0; n < 2; ++n) _Pragma("unroll") for (int k = 0; k < 2; ++k) \
;         acc[ai][bj][m][n] = __builtin_amdgcn_mfma_f32_16x16x32_bf16(Bt[n][k], At[m][k], acc[ai][bj][m][n], 0, 0, 0); __builtin_amdgcn_s_setprio(0); } while (0)
; #define PG8_WAIT_V(n) asm volatile("s_waitcnt vmcnt(" #n ")" ::: "memory")
; #define PG8_WAIT_L(n) asm volatile("s_waitcnt lgkmcnt(" #n ")" ::: "memory")
; #define PG8_BAR __builtin_amdgcn_s_barrier()
; #define PG8_SCHED __builtin_amdgcn_sched_barrier(0)
; template <class Desc, class Epi>
; __device__ __forceinline__ void gemm_phase(const int wv_, LAS unsigned char* lds, const Desc& d, const Epi& E) {
;     ...
;             PG8_LDA(At, 1, 1); PG8_STAGE(PG8_SB(1, 0), b3, voffB); PG8_STAGE(PG8_SB(1, 1), b3 + hstepB, voffB); PG8_STAGE(PG8_SA(1, 0), a3, sA0);
;             PG8_WAIT_V(8); PG8_WAIT_L(0); PG8_BAR; PG8_MMA(1, 0, At, B0); PG8_MMA(1, 1, At, B1); PG8_BAR; PG8_SCHED;
;         }
;         if (wr == 0) PG8_BAR;
	v_mov_b32_e32 v96, v134
	ds_read_b128 v[182:185], v149 offset:49152
	ds_read_b128 v[186:189], v149 offset:50176
	ds_read_b128 v[190:193], v149 offset:51200
	ds_read_b128 v[194:197], v149 offset:52224
	ds_read_b128 v[198:201], v149 offset:53248
	ds_read_b128 v[202:205], v149 offset:54272
	ds_read_b128 v[206:209], v149 offset:55296
	ds_read_b128 v[210:213], v149 offset:56320
	s_mov_b32 m0, s71
	v_lshl_add_u64 v[130:131], s[20:21], 0, v[96:97]
	v_lshl_add_u64 v[130:131], v[130:131], 0, s[30:31]
	v_mov_b32_e32 v96, v137
	global_load_lds_dwordx4 v[130:131], off
	s_mov_b32 m0, s29
	v_lshl_add_u64 v[130:131], s[20:21], 0, v[96:97]
	v_lshl_add_u64 v[130:131], v[130:131], 0, s[30:31]
	v_mov_b32_e32 v96, v134
	global_load_lds_dwordx4 v[130:131], off
	s_mov_b32 m0, s78
	s_nop 0
	global_load_lds_dwordx4 v96, s[22:23]
	v_mov_b32_e32 v96, v137
	s_mov_b32 m0, s77
	s_nop 0
	global_load_lds_dwordx4 v96, s[22:23]
	v_mov_b32_e32 v96, v132
	s_mov_b32 m0, s65
	v_lshl_add_u64 v[130:131], s[4:5], 0, v[96:97]
	v_lshl_add_u64 v[130:131], v[130:131], 0, s[30:31]
	v_mov_b32_e32 v96, v135
	global_load_lds_dwordx4 v[130:131], off
	s_mov_b32 m0, s66
	v_lshl_add_u64 v[130:131], s[4:5], 0, v[96:97]
	v_lshl_add_u64 v[130:131], v[130:131], 0, s[30:31]
	global_load_lds_dwordx4 v[130:131], off
	s_waitcnt vmcnt(8)
	s_waitcnt lgkmcnt(0)
	s_barrier
	v_mfma_f32_16x16x32_bf16 v[60:63], v[150:153], v[182:185], v[60:63]
	v_mfma_f32_16x16x32_bf16 v[56:59], v[158:161], v[182:185], v[56:59]
	v_mfma_f32_16x16x32_bf16 v[44:47], v[150:153], v[190:193], v[44:47]
	v_mfma_f32_16x16x32_bf16 v[32:35], v[158:161], v[190:193], v[32:35]
	v_mfma_f32_16x16x32_bf16 v[16:19], v[150:153], v[198:201], v[16:19]
	v_mfma_f32_16x16x32_bf16 v[8:11], v[158:161], v[198:201], v[8:11]
	v_mfma_f32_16x16x32_bf16 v[4:7], v[150:153], v[206:209], v[4:7]
	v_mfma_f32_16x16x32_bf16 v[0:3], v[158:161], v[206:209], v[0:3]
	v_mfma_f32_16x16x32_bf16 v[60:63], v[154:157], v[186:189], v[60:63]
	v_mfma_f32_16x16x32_bf16 v[56:59], v[162:165], v[186:189], v[56:59]
	v_mfma_f32_16x16x32_bf16 v[44:47], v[154:157], v[194:197], v[44:47]
	v_mfma_f32_16x16x32_bf16 v[32:35], v[162:165], v[194:197], v[32:35]
	v_mfma_f32_16x16x32_bf16 v[16:19], v[154:157], v[202:205], v[16:19]
	v_mfma_f32_16x16x32_bf16 v[8:11], v[162:165], v[202:205], v[8:11]
	v_mfma_f32_16x16x32_bf16 v[4:7], v[154:157], v[210:213], v[4:7]
	v_mfma_f32_16x16x32_bf16 v[0:3], v[162:165], v[210:213], v[0:3]
	v_mfma_f32_16x16x32_bf16 v[52:55], v[166:169], v[182:185], v[52:55]
	v_mfma_f32_16x16x32_bf16 v[48:51], v[174:177], v[182:185], v[48:51]
	v_mfma_f32_16x16x32_bf16 v[28:31], v[166:169], v[190:193], v[28:31]
	v_mfma_f32_16x16x32_bf16 v[12:15], v[174:177], v[190:193], v[12:15]
	v_mfma_f32_16x16x32_bf16 v[36:39], v[166:169], v[198:201], v[36:39]
	v_mfma_f32_16x16x32_bf16 v[40:43], v[174:177], v[198:201], v[40:43]
	v_mfma_f32_16x16x32_bf16 v[20:23], v[166:169], v[206:209], v[20:23]
	v_mfma_f32_16x16x32_bf16 v[24:27], v[174:177], v[206:209], v[24:27]
	v_mfma_f32_16x16x32_bf16 v[52:55], v[170:173], v[186:189], v[52:55]
	v_mfma_f32_16x16x32_bf16 v[48:51], v[178:181], v[186:189], v[48:51]
	v_mfma_f32_16x16x32_bf16 v[28:31], v[170:173], v[194:197], v[28:31]
	v_mfma_f32_16x16x32_bf16 v[12:15], v[178:181], v[194:197], v[12:15]
	v_mfma_f32_16x16x32_bf16 v[36:39], v[170:173], v[202:205], v[36:39]
	v_mfma_f32_16x16x32_bf16 v[40:43], v[178:181], v[202:205], v[40:43]
	v_mfma_f32_16x16x32_bf16 v[20:23], v[170:173], v[210:213], v[20:23]
	v_mfma_f32_16x16x32_bf16 v[24:27], v[178:181], v[210:213], v[24:27]
	s_barrier
	s_movk_i32 s22, 0x100
	s_andn2_b64 vcc, exec, s[2:3]
	s_mov_b64 s[20:21], -1
	s_mov_b64 s[2:3], 0
	s_cbranch_vccz .LBB0_937
	s_and_b64 vcc, exec, s[40:41]
	s_cbranch_vccz .LBB0_940
	s_barrier

; #define PG8_STAGE(bufoff, gbase, voff) do { _Pragma("unroll") for (int _i = 0; _i < 2; ++_i) \
;         __builtin_amdgcn_global_load_lds((const __attribute__((address_space(1))) unsigned*)((const __attribute__((address_space(1))) char*)(gbase) + (unsigned)lnd_v((int)(voff)[_i])), (LAS unsigned*)(lds + (bufoff) + ldsw + _i * 8192), 16, 0, 0); } while (0)
; #define PG8_LDA(dst, b, h) do { _Pragma("unroll") for (int m = 0; m < 4; ++m) _Pragma("unroll") for (int k = 0; k < 2; ++k) dst[m][k] = *(const LAS bf16x8*)(lds + PG8_SA(b, h) + aoff + m * 2048 + k * 1024); } while (0)
; #define PG8_LDB(dst, b, h) do { _Pragma("unroll") for (int n = 0; n < 2; ++n) _Pragma("unroll") for (int k = 0; k < 2; ++k) dst[n][k] = *(const LAS bf16x8*)(lds + PG8_SB(b, h) + boff + n * 2048 + k * 1024); } while (0)
; #define PG8_WAIT_V(n) asm volatile("s_waitcnt vmcnt(" #n ")" ::: "memory")
; #define PG8_WAIT_L(n) asm volatile("s_waitcnt lgkmcnt(" #n ")" ::: "memory")
; #define PG8_BAR __builtin_amdgcn_s_barrier()
; #define PG8_SCHED __builtin_amdgcn_sched_barrier(0)
; template <class Desc, class Epi>
; __device__ __forceinline__ void gemm_phase(const int wv_, LAS unsigned char* lds, const Desc& d, const Epi& E) {
;     ...
;             const bool last = (t == nt - 2);
;             unsigned sA0[2], sA1[2];
;             if constexpr (Desc::GATHER) { sA0[0] = last ? voffAn[0] : voffA[0]; sA0[1] = last ? voffAn[1] : voffA[1]; sA1[0] = last ? voffAn1[0] : voffA1[0]; sA1[1] = last ? voffAn1[1] : voffA1[1]; }
;             else { sA0[0] = voffA[0]; sA0[1] = voffA[1]; sA1[0] = voffA1[0]; sA1[1] = voffA1[1]; }
;             const char* a1 = cA + (size_t)(t + 1) * kstep;
;             const char* a2 = last ? nA : cA + (size_t)(t + 2) * kstep; const char* b2 = last ? nB : cB + (size_t)(t + 2) * kstep;
;             const char* a3 = a2 + kstep; const char* b3 = b2 + kstep;
;             PG8_LDB(B0, 0, 0); PG8_LDB(B1, 0, 1); PG8_SCHED; PG8_LDA(At, 0, 0); PG8_STAGE(PG8_SA(1, 1), a1, voffA1);
;             PG8_WAIT_V(8); PG8_WAIT_L(0); PG8_BAR; PG8_MMA(0, 0, At, B0); PG8_MMA(0, 1, At, B1); PG8_BAR; PG8_SCHED;
;             PG8_LDA(At, 0, 1); PG8_STAGE(PG8_SB(0, 0), b2, voffB); PG8_STAGE(PG8_SB(0, 1), b2 + hstepB, voffB); PG8_STAGE(PG8_SA(0, 0), a2, sA0);
;             PG8_WAIT_V(8); PG8_WAIT_L(0); PG8_BAR; PG8_MMA(1, 0, At, B0); PG8_MMA(1, 1, At, B1); PG8_BAR; PG8_SCHED;
.LBB0_1075:
	s_add_u32 s4, s2, 0x80
	s_addc_u32 s5, s3, 0
	s_add_i32 s47, 0, 0x10000
	s_cmp_eq_u32 s29, 12
	s_cselect_b32 s5, s51, s5
	s_cselect_b32 s4, s50, s4
	v_add_u32_e32 v96, s47, v226
	s_cselect_b32 s21, s53, s26
	s_cselect_b32 s20, s52, s1
	s_add_i32 s49, 0, 0x14000
	ds_read_b128 v[118:121], v96
	ds_read_b128 v[126:129], v96 offset:1024
	ds_read_b128 v[130:133], v96 offset:2048
	ds_read_b128 v[134:137], v96 offset:3072
	v_add_u32_e32 v96, s49, v226
	ds_read_b128 v[142:145], v96
	ds_read_b128 v[150:153], v96 offset:1024
	ds_read_b128 v[154:157], v96 offset:2048
	ds_read_b128 v[158:161], v96 offset:3072
	v_mov_b32_e32 v96, v220
	ds_read_b128 v[162:165], v231
	ds_read_b128 v[166:169], v231 offset:1024
	ds_read_b128 v[170:173], v231 offset:2048
	ds_read_b128 v[174:177], v231 offset:3072
	ds_read_b128 v[178:181], v231 offset:4096
	ds_read_b128 v[182:185], v231 offset:5120
	ds_read_b128 v[186:189], v231 offset:6144
	ds_read_b128 v[190:193], v231 offset:7168
	s_add_i32 m0, s60, 0xc000
	s_nop 0
	global_load_lds_dwordx4 v96, s[2:3]
	v_mov_b32_e32 v96, v223
	s_add_i32 m0, s60, 0xe000
	s_nop 0
	global_load_lds_dwordx4 v96, s[2:3]
	s_waitcnt vmcnt(8)
	s_waitcnt lgkmcnt(0)
	s_barrier
	v_mfma_f32_16x16x32_bf16 v[146:149], v[118:121], v[162:165], v[146:149]
	v_mfma_f32_16x16x32_bf16 v[138:141], v[130:133], v[162:165], v[138:141]
	v_mfma_f32_16x16x32_bf16 v[110:113], v[118:121], v[170:173], v[110:113]
	v_mfma_f32_16x16x32_bf16 v[106:109], v[130:133], v[170:173], v[106:109]
	v_mfma_f32_16x16x32_bf16 v[92:95], v[118:121], v[178:181], v[92:95]
	v_mfma_f32_16x16x32_bf16 v[88:91], v[130:133], v[178:181], v[88:91]
	v_mfma_f32_16x16x32_bf16 v[76:79], v[118:121], v[186:189], v[76:79]
	v_mfma_f32_16x16x32_bf16 v[72:75], v[130:133], v[186:189], v[72:75]
	v_mfma_f32_16x16x32_bf16 v[146:149], v[126:129], v[166:169], v[146:149]
	v_mfma_f32_16x16x32_bf16 v[138:141], v[134:137], v[166:169], v[138:141]
	v_mfma_f32_16x16x32_bf16 v[110:113], v[126:129], v[174:177], v[110:113]
	v_mfma_f32_16x16x32_bf16 v[106:109], v[134:137], v[174:177], v[106:109]
	v_mfma_f32_16x16x32_bf16 v[92:95], v[126:129], v[182:185], v[92:95]
	v_mfma_f32_16x16x32_bf16 v[88:91], v[134:137], v[182:185], v[88:91]
	v_mfma_f32_16x16x32_bf16 v[76:79], v[126:129], v[190:193], v[76:79]
	v_mfma_f32_16x16x32_bf16 v[72:75], v[134:137], v[190:193], v[72:75]
	v_mfma_f32_16x16x32_bf16 v[122:125], v[142:145], v[162:165], v[122:125]
	v_mfma_f32_16x16x32_bf16 v[114:117], v[154:157], v[162:165], v[114:117]
	v_mfma_f32_16x16x32_bf16 v[102:105], v[142:145], v[170:173], v[102:105]
	v_mfma_f32_16x16x32_bf16 v[98:101], v[154:157], v[170:173], v[98:101]
	v_mfma_f32_16x16x32_bf16 v[84:87], v[142:145], v[178:181], v[84:87]
	v_mfma_f32_16x16x32_bf16 v[80:83], v[154:157], v[178:181], v[80:83]
	v_mfma_f32_16x16x32_bf16 v[68:71], v[142:145], v[186:189], v[68:71]
	v_mfma_f32_16x16x32_bf16 v[64:67], v[154:157], v[186:189], v[64:67]
	v_mfma_f32_16x16x32_bf16 v[122:125], v[150:153], v[166:169], v[122:125]
	v_mfma_f32_16x16x32_bf16 v[114:117], v[158:161], v[166:169], v[114:117]
	v_mfma_f32_16x16x32_bf16 v[102:105], v[150:153], v[174:177], v[102:105]
	v_mfma_f32_16x16x32_bf16 v[98:101], v[158:161], v[174:177], v[98:101]
	v_mfma_f32_16x16x32_bf16 v[84:87], v[150:153], v[182:185], v[84:87]
	v_mfma_f32_16x16x32_bf16 v[80:83], v[158:161], v[182:185], v[80:83]
	v_mfma_f32_16x16x32_bf16 v[68:71], v[150:153], v[190:193], v[68:71]
	v_mfma_f32_16x16x32_bf16 v[64:67], v[158:161], v[190:193], v[64:67]
	s_barrier
	v_mov_b32_e32 v96, v221
	s_add_i32 s47, s47, s59
	ds_read_b128 v[162:165], v231 offset:16384
	ds_read_b128 v[166:169], v231 offset:17408
	ds_read_b128 v[170:173], v231 offset:18432
	ds_read_b128 v[174:177], v231 offset:19456
	ds_read_b128 v[178:181], v231 offset:20480
	ds_read_b128 v[182:185], v231 offset:21504
	ds_read_b128 v[186:189], v231 offset:22528
	ds_read_b128 v[190:193], v231 offset:23552
	s_mov_b32 m0, s47
	s_nop 0
	global_load_lds_dwordx4 v96, s[20:21]
	v_mov_b32_e32 v96, v224
	s_add_i32 m0, s47, 0x2000
	s_add_u32 s70, s20, 0x40000
	global_load_lds_dwordx4 v96, s[20:21]
	s_addc_u32 s71, s21, 0
	v_mov_b32_e32 v96, v221
	s_add_i32 s47, s49, s59
	s_mov_b32 m0, s47
	s_nop 0
	global_load_lds_dwordx4 v96, s[70:71]
	v_mov_b32_e32 v96, v224
	s_add_i32 m0, s47, 0x2000
	s_nop 0
	global_load_lds_dwordx4 v96, s[70:71]
	v_mov_b32_e32 v96, v219
	s_mov_b32 m0, s60
	s_nop 0
	global_load_lds_dwordx4 v96, s[4:5]
	v_mov_b32_e32 v96, v222
	s_mov_b32 m0, s62
	s_nop 0
	global_load_lds_dwordx4 v96, s[4:5]
	s_waitcnt vmcnt(8)
	s_waitcnt lgkmcnt(0)
	s_barrier
	v_mfma_f32_16x16x32_bf16 v[60:63], v[118:121], v[162:165], v[60:63]
	v_mfma_f32_16x16x32_bf16 v[56:59], v[130:133], v[162:165], v[56:59]
	v_mfma_f32_16x16x32_bf16 v[44:47], v[118:121], v[170:173], v[44:47]
	v_mfma_f32_16x16x32_bf16 v[40:43], v[130:133], v[170:173], v[40:43]
	v_mfma_f32_16x16x32_bf16 v[20:23], v[118:121], v[178:181], v[20:23]
	v_mfma_f32_16x16x32_bf16 v[16:19], v[130:133], v[178:181], v[16:19]
	v_mfma_f32_16x16x32_bf16 v[4:7], v[118:121], v[186:189], v[4:7]
	v_mfma_f32_16x16x32_bf16 v[0:3], v[130:133], v[186:189], v[0:3]
	v_mfma_f32_16x16x32_bf16 v[60:63], v[126:129], v[166:169], v[60:63]
	v_mfma_f32_16x16x32_bf16 v[56:59], v[134:137], v[166:169], v[56:59]
	v_mfma_f32_16x16x32_bf16 v[44:47], v[126:129], v[174:177], v[44:47]
	v_mfma_f32_16x16x32_bf16 v[40:43], v[134:137], v[174:177], v[40:43]
	v_mfma_f32_16x16x32_bf16 v[20:23], v[126:129], v[182:185], v[20:23]
	v_mfma_f32_16x16x32_bf16 v[16:19], v[134:137], v[182:185], v[16:19]
	v_mfma_f32_16x16x32_bf16 v[4:7], v[126:129], v[190:193], v[4:7]
	v_mfma_f32_16x16x32_bf16 v[0:3], v[134:137], v[190:193], v[0:3]
	v_mfma_f32_16x16x32_bf16 v[52:55], v[142:145], v[162:165], v[52:55]
	v_mfma_f32_16x16x32_bf16 v[48:51], v[154:157], v[162:165], v[48:51]
	v_mfma_f32_16x16x32_bf16 v[36:39], v[142:145], v[170:173], v[36:39]
	v_mfma_f32_16x16x32_bf16 v[32:35], v[154:157], v[170:173], v[32:35]
	v_mfma_f32_16x16x32_bf16 v[28:31], v[142:145], v[178:181], v[28:31]
	v_mfma_f32_16x16x32_bf16 v[24:27], v[154:157], v[178:181], v[24:27]
	v_mfma_f32_16x16x32_bf16 v[12:15], v[142:145], v[186:189], v[12:15]
	v_mfma_f32_16x16x32_bf16 v[8:11], v[154:157], v[186:189], v[8:11]
	v_mfma_f32_16x16x32_bf16 v[52:55], v[150:153], v[166:169], v[52:55]
	v_mfma_f32_16x16x32_bf16 v[48:51], v[158:161], v[166:169], v[48:51]
	v_mfma_f32_16x16x32_bf16 v[36:39], v[150:153], v[174:177], v[36:39]
	v_mfma_f32_16x16x32_bf16 v[32:35], v[158:161], v[174:177], v[32:35]
	v_mfma_f32_16x16x32_bf16 v[28:31], v[150:153], v[182:185], v[28:31]
	v_mfma_f32_16x16x32_bf16 v[24:27], v[158:161], v[182:185], v[24:27]
	v_mfma_f32_16x16x32_bf16 v[12:15], v[150:153], v[190:193], v[12:15]
	v_mfma_f32_16x16x32_bf16 v[8:11], v[158:161], v[190:193], v[8:11]
	s_barrier
; #define PG8_STAGE(bufoff, gbase, voff) do { _Pragma("unroll") for (int _i = 0; _i < 2; ++_i) \
;         __builtin_amdgcn_global_load_lds((const __attribute__((address_space(1))) unsigned*)((const __attribute__((address_space(1))) char*)(gbase) + (unsigned)lnd_v((int)(voff)[_i])), (LAS unsigned*)(lds + (bufoff) + ldsw + _i * 8192), 16, 0, 0); } while (0)
; #define PG8_LDA(dst, b, h) do { _Pragma("unroll") for (int m = 0; m < 4; ++m) _Pragma("unroll") for (int k = 0; k < 2; ++k) dst[m][k] = *(const LAS bf16x8*)(lds + PG8_SA(b, h) + aoff + m * 2048 + k * 1024); } while (0)
; #define PG8_LDB(dst, b, h) do { _Pragma("unroll") for (int n = 0; n < 2; ++n) _Pragma("unroll") for (int k = 0; k < 2; ++k) dst[n][k] = *(const LAS bf16x8*)(lds + PG8_SB(b, h) + boff + n * 2048 + k * 1024); } while (0)
; #define PG8_MMA(ai, bj, At, Bt) do { __builtin_amdgcn_s_setprio(1); _Pragma("unroll") for (int m = 0; m < 4; ++m) _Pragma("unroll") for (int n = 0; n < 2; ++n) _Pragma("unroll") for (int k = 0; k < 2; ++k) \
;         acc[ai][bj][m][n] = __builtin_amdgcn_mfma_f32_16x16x32_bf16(Bt[n][k], At[m][k], acc[ai][bj][m][n], 0, 0, 0); __builtin_amdgcn_s_setprio(0); } while (0)
; #define PG8_WAIT_V(n) asm volatile("s_waitcnt vmcnt(" #n ")" ::: "memory")
; #define PG8_WAIT_L(n) asm volatile("s_waitcnt lgkmcnt(" #n ")" ::: "memory")
; #define PG8_BAR __builtin_amdgcn_s_barrier()
; #define PG8_SCHED __builtin_amdgcn_sched_barrier(0)
; template <class Desc, class Epi>
; __device__ __forceinline__ void gemm_phase(const int wv_, LAS unsigned char* lds, const Desc& d, const Epi& E) {
;     ...
;             PG8_LDB(B0, 1, 0); PG8_LDB(B1, 1, 1); PG8_SCHED; PG8_LDA(At, 1, 0); PG8_STAGE(PG8_SA(0, 1), a2, sA1);
;             PG8_WAIT_V(8); PG8_WAIT_L(0); PG8_BAR; PG8_MMA(0, 0, At, B0); PG8_MMA(0, 1, At, B1); PG8_BAR; PG8_SCHED;
	s_add_i32 s47, 0, 0x18000
	v_add_u32_e32 v96, s47, v226
	s_add_i32 s49, 0, 0x1c000
	ds_read_b128 v[118:121], v96
	ds_read_b128 v[126:129], v96 offset:1024
	ds_read_b128 v[130:133], v96 offset:2048
	ds_read_b128 v[134:137], v96 offset:3072
	v_add_u32_e32 v96, s49, v226
	ds_read_b128 v[142:145], v96
	ds_read_b128 v[150:153], v96 offset:1024
	ds_read_b128 v[154:157], v96 offset:2048
	ds_read_b128 v[158:161], v96 offset:3072
	v_mov_b32_e32 v96, v220
	s_mov_b32 m0, s63
	ds_read_b128 v[162:165], v231 offset:32768
	ds_read_b128 v[166:169], v231 offset:33792
	ds_read_b128 v[170:173], v231 offset:34816
	ds_read_b128 v[174:177], v231 offset:35840
	ds_read_b128 v[178:181], v231 offset:36864
	ds_read_b128 v[182:185], v231 offset:37888
	ds_read_b128 v[186:189], v231 offset:38912
	ds_read_b128 v[190:193], v231 offset:39936
	s_nop 0
	global_load_lds_dwordx4 v96, s[4:5]
	v_mov_b32_e32 v96, v223
	s_mov_b32 m0, s64
	s_nop 0
	global_load_lds_dwordx4 v96, s[4:5]
	s_waitcnt vmcnt(8)
	s_waitcnt lgkmcnt(0)
	s_barrier
	v_mfma_f32_16x16x32_bf16 v[146:149], v[118:121], v[162:165], v[146:149]
	v_mfma_f32_16x16x32_bf16 v[138:141], v[130:133], v[162:165], v[138:141]
	v_mfma_f32_16x16x32_bf16 v[110:113], v[118:121], v[170:173], v[110:113]
	v_mfma_f32_16x16x32_bf16 v[106:109], v[130:133], v[170:173], v[106:109]
	v_mfma_f32_16x16x32_bf16 v[92:95], v[118:121], v[178:181], v[92:95]
	v_mfma_f32_16x16x32_bf16 v[88:91], v[130:133], v[178:181], v[88:91]
	v_mfma_f32_16x16x32_bf16 v[76:79], v[118:121], v[186:189], v[76:79]
	v_mfma_f32_16x16x32_bf16 v[72:75], v[130:133], v[186:189], v[72:75]
	v_mfma_f32_16x16x32_bf16 v[146:149], v[126:129], v[166:169], v[146:149]
	v_mfma_f32_16x16x32_bf16 v[138:141], v[134:137], v[166:169], v[138:141]
	v_mfma_f32_16x16x32_bf16 v[110:113], v[126:129], v[174:177], v[110:113]
	v_mfma_f32_16x16x32_bf16 v[106:109], v[134:137], v[174:177], v[106:109]
	v_mfma_f32_16x16x32_bf16 v[92:95], v[126:129], v[182:185], v[92:95]
	v_mfma_f32_16x16x32_bf16 v[88:91], v[134:137], v[182:185], v[88:91]
	v_mfma_f32_16x16x32_bf16 v[76:79], v[126:129], v[190:193], v[76:79]
	v_mfma_f32_16x16x32_bf16 v[72:75], v[134:137], v[190:193], v[72:75]
	v_mfma_f32_16x16x32_bf16 v[122:125], v[142:145], v[162:165], v[122:125]
	v_mfma_f32_16x16x32_bf16 v[114:117], v[154:157], v[162:165], v[114:117]
	v_mfma_f32_16x16x32_bf16 v[102:105], v[142:145], v[170:173], v[102:105]
	v_mfma_f32_16x16x32_bf16 v[98:101], v[154:157], v[170:173], v[98:101]
	v_mfma_f32_16x16x32_bf16 v[84:87], v[142:145], v[178:181], v[84:87]
	v_mfma_f32_16x16x32_bf16 v[80:83], v[154:157], v[178:181], v[80:83]
	v_mfma_f32_16x16x32_bf16 v[68:71], v[142:145], v[186:189], v[68:71]
	v_mfma_f32_16x16x32_bf16 v[64:67], v[154:157], v[186:189], v[64:67]
	v_mfma_f32_16x16x32_bf16 v[122:125], v[150:153], v[166:169], v[122:125]
	v_mfma_f32_16x16x32_bf16 v[114:117], v[158:161], v[166:169], v[114:117]
	v_mfma_f32_16x16x32_bf16 v[102:105], v[150:153], v[174:177], v[102:105]
	v_mfma_f32_16x16x32_bf16 v[98:101], v[158:161], v[174:177], v[98:101]
	v_mfma_f32_16x16x32_bf16 v[84:87], v[150:153], v[182:185], v[84:87]
	v_mfma_f32_16x16x32_bf16 v[80:83], v[158:161], v[182:185], v[80:83]
	v_mfma_f32_16x16x32_bf16 v[68:71], v[150:153], v[190:193], v[68:71]
	v_mfma_f32_16x16x32_bf16 v[64:67], v[158:161], v[190:193], v[64:67]
	s_barrier
; #define PG8_STAGE(bufoff, gbase, voff) do { _Pragma("unroll") for (int _i = 0; _i < 2; ++_i) \
;         __builtin_amdgcn_global_load_lds((const __attribute__((address_space(1))) unsigned*)((const __attribute__((address_space(1))) char*)(gbase) + (unsigned)lnd_v((int)(voff)[_i])), (LAS unsigned*)(lds + (bufoff) + ldsw + _i * 8192), 16, 0, 0); } while (0)
; #define PG8_LDA(dst, b, h) do { _Pragma("unroll") for (int m = 0; m < 4; ++m) _Pragma("unroll") for (int k = 0; k < 2; ++k) dst[m][k] = *(const LAS bf16x8*)(lds + PG8_SA(b, h) + aoff + m * 2048 + k * 1024); } while (0)
; #define PG8_MMA(ai, bj, At, Bt) do { __builtin_amdgcn_s_setprio(1); _Pragma("unroll") for (int m = 0; m < 4; ++m) _Pragma("unroll") for (int n = 0; n < 2; ++n) _Pragma("unroll") for (int k = 0; k < 2; ++k) \
;         acc[ai][bj][m][n] = __builtin_amdgcn_mfma_f32_16x16x32_bf16(Bt[n][k], At[m][k], acc[ai][bj][m][n], 0, 0, 0); __builtin_amdgcn_s_setprio(0); } while (0)
; #define PG8_WAIT_V(n) asm volatile("s_waitcnt vmcnt(" #n ")" ::: "memory")
; #define PG8_WAIT_L(n) asm volatile("s_waitcnt lgkmcnt(" #n ")" ::: "memory")
; #define PG8_BAR __builtin_amdgcn_s_barrier()
; #define PG8_SCHED __builtin_amdgcn_sched_barrier(0)
; template <class Desc, class Epi>
; __device__ __forceinline__ void gemm_phase(const int wv_, LAS unsigned char* lds, const Desc& d, const Epi& E) {
;     ...
;             PG8_LDA(At, 1, 1); PG8_STAGE(PG8_SB(1, 0), b3, voffB); PG8_STAGE(PG8_SB(1, 1), b3 + hstepB, voffB); PG8_STAGE(PG8_SA(1, 0), a3, sA0);
;             PG8_WAIT_V(8); PG8_WAIT_L(0); PG8_BAR; PG8_MMA(1, 0, At, B0); PG8_MMA(1, 1, At, B1); PG8_BAR; PG8_SCHED;
;         }
;         if (wr == 0) PG8_BAR;
	v_mov_b32_e32 v96, v221
	ds_read_b128 v[162:165], v231 offset:49152
	ds_read_b128 v[166:169], v231 offset:50176
	ds_read_b128 v[170:173], v231 offset:51200
	ds_read_b128 v[174:177], v231 offset:52224
	ds_read_b128 v[178:181], v231 offset:53248
	ds_read_b128 v[182:185], v231 offset:54272
	ds_read_b128 v[186:189], v231 offset:55296
	ds_read_b128 v[190:193], v231 offset:56320
	s_add_i32 s47, s47, s59
	v_lshl_add_u64 v[194:195], s[20:21], 0, v[96:97]
	v_lshl_add_u64 v[194:195], v[194:195], 0, s[30:31]
	s_mov_b32 m0, s47
	v_mov_b32_e32 v96, v224
	global_load_lds_dwordx4 v[194:195], off
	s_add_i32 m0, s47, 0x2000
	s_nop 0
	v_lshl_add_u64 v[194:195], s[20:21], 0, v[96:97]
	s_add_u32 s20, s20, 0x40080
	v_lshl_add_u64 v[194:195], v[194:195], 0, s[30:31]
	s_addc_u32 s21, s21, 0
	v_mov_b32_e32 v96, v221
	s_add_i32 s47, s49, s59
	global_load_lds_dwordx4 v[194:195], off
	s_mov_b32 m0, s47
	s_nop 0
	global_load_lds_dwordx4 v96, s[20:21]
	v_mov_b32_e32 v96, v224
	s_add_i32 m0, s47, 0x2000
	s_nop 0
	global_load_lds_dwordx4 v96, s[20:21]
	v_mov_b32_e32 v96, v219
	s_mov_b32 m0, s66
	v_lshl_add_u64 v[194:195], s[4:5], 0, v[96:97]
	v_lshl_add_u64 v[194:195], v[194:195], 0, s[30:31]
	v_mov_b32_e32 v96, v222
	global_load_lds_dwordx4 v[194:195], off
	s_mov_b32 m0, s67
	v_lshl_add_u64 v[194:195], s[4:5], 0, v[96:97]
	v_lshl_add_u64 v[194:195], v[194:195], 0, s[30:31]
	global_load_lds_dwordx4 v[194:195], off
	s_waitcnt vmcnt(8)
	s_waitcnt lgkmcnt(0)
	s_barrier
	v_mfma_f32_16x16x32_bf16 v[60:63], v[118:121], v[162:165], v[60:63]
	v_mfma_f32_16x16x32_bf16 v[56:59], v[130:133], v[162:165], v[56:59]
	v_mfma_f32_16x16x32_bf16 v[44:47], v[118:121], v[170:173], v[44:47]
	v_mfma_f32_16x16x32_bf16 v[40:43], v[130:133], v[170:173], v[40:43]
	v_mfma_f32_16x16x32_bf16 v[20:23], v[118:121], v[178:181], v[20:23]
	v_mfma_f32_16x16x32_bf16 v[16:19], v[130:133], v[178:181], v[16:19]
	v_mfma_f32_16x16x32_bf16 v[4:7], v[118:121], v[186:189], v[4:7]
	v_mfma_f32_16x16x32_bf16 v[0:3], v[130:133], v[186:189], v[0:3]
	v_mfma_f32_16x16x32_bf16 v[60:63], v[126:129], v[166:169], v[60:63]
	v_mfma_f32_16x16x32_bf16 v[56:59], v[134:137], v[166:169], v[56:59]
	v_mfma_f32_16x16x32_bf16 v[44:47], v[126:129], v[174:177], v[44:47]
	v_mfma_f32_16x16x32_bf16 v[40:43], v[134:137], v[174:177], v[40:43]
	v_mfma_f32_16x16x32_bf16 v[20:23], v[126:129], v[182:185], v[20:23]
	v_mfma_f32_16x16x32_bf16 v[16:19], v[134:137], v[182:185], v[16:19]
	v_mfma_f32_16x16x32_bf16 v[4:7], v[126:129], v[190:193], v[4:7]
	v_mfma_f32_16x16x32_bf16 v[0:3], v[134:137], v[190:193], v[0:3]
	v_mfma_f32_16x16x32_bf16 v[52:55], v[142:145], v[162:165], v[52:55]
	v_mfma_f32_16x16x32_bf16 v[48:51], v[154:157], v[162:165], v[48:51]
	v_mfma_f32_16x16x32_bf16 v[36:39], v[142:145], v[170:173], v[36:39]
	v_mfma_f32_16x16x32_bf16 v[32:35], v[154:157], v[170:173], v[32:35]
	v_mfma_f32_16x16x32_bf16 v[28:31], v[142:145], v[178:181], v[28:31]
	v_mfma_f32_16x16x32_bf16 v[24:27], v[154:157], v[178:181], v[24:27]
	v_mfma_f32_16x16x32_bf16 v[12:15], v[142:145], v[186:189], v[12:15]
	v_mfma_f32_16x16x32_bf16 v[8:11], v[154:157], v[186:189], v[8:11]
	v_mfma_f32_16x16x32_bf16 v[52:55], v[150:153], v[166:169], v[52:55]
	v_mfma_f32_16x16x32_bf16 v[48:51], v[158:161], v[166:169], v[48:51]
	v_mfma_f32_16x16x32_bf16 v[36:39], v[150:153], v[174:177], v[36:39]
	v_mfma_f32_16x16x32_bf16 v[32:35], v[158:161], v[174:177], v[32:35]
	v_mfma_f32_16x16x32_bf16 v[28:31], v[150:153], v[182:185], v[28:31]
	v_mfma_f32_16x16x32_bf16 v[24:27], v[158:161], v[182:185], v[24:27]
	v_mfma_f32_16x16x32_bf16 v[12:15], v[150:153], v[190:193], v[12:15]
	v_mfma_f32_16x16x32_bf16 v[8:11], v[158:161], v[190:193], v[8:11]
	s_barrier
	s_add_i32 s29, s29, 2
	s_add_u32 s2, s2, 0x100
	s_addc_u32 s3, s3, 0
	s_add_u32 s1, s1, 0x100
	s_addc_u32 s26, s26, 0
	s_cmp_gt_u32 s29, 13
	s_cbranch_scc0 .LBB0_1075
	s_and_b64 vcc, exec, s[44:45]
	s_cbranch_vccz .LBB0_1078
	s_barrier

; #define PG8_STAGE(bufoff, gbase, voff) do { _Pragma("unroll") for (int _i = 0; _i < 2; ++_i) \
;         __builtin_amdgcn_global_load_lds((const __attribute__((address_space(1))) unsigned*)((const __attribute__((address_space(1))) char*)(gbase) + (unsigned)lnd_v((int)(voff)[_i])), (LAS unsigned*)(lds + (bufoff) + ldsw + _i * 8192), 16, 0, 0); } while (0)
; #define PG8_LDA(dst, b, h) do { _Pragma("unroll") for (int m = 0; m < 4; ++m) _Pragma("unroll") for (int k = 0; k < 2; ++k) dst[m][k] = *(const LAS bf16x8*)(lds + PG8_SA(b, h) + aoff + m * 2048 + k * 1024); } while (0)
; #define PG8_LDB(dst, b, h) do { _Pragma("unroll") for (int n = 0; n < 2; ++n) _Pragma("unroll") for (int k = 0; k < 2; ++k) dst[n][k] = *(const LAS bf16x8*)(lds + PG8_SB(b, h) + boff + n * 2048 + k * 1024); } while (0)
; #define PG8_WAIT_V(n) asm volatile("s_waitcnt vmcnt(" #n ")" ::: "memory")
; #define PG8_WAIT_L(n) asm volatile("s_waitcnt lgkmcnt(" #n ")" ::: "memory")
; #define PG8_BAR __builtin_amdgcn_s_barrier()
; #define PG8_SCHED __builtin_amdgcn_sched_barrier(0)
; template <class Desc, class Epi>
; __device__ __forceinline__ void gemm_phase(const int wv_, LAS unsigned char* lds, const Desc& d, const Epi& E) {
;     ...
;             const bool last = (t == nt - 2);
;             unsigned sA0[2], sA1[2];
;             if constexpr (Desc::GATHER) { sA0[0] = last ? voffAn[0] : voffA[0]; sA0[1] = last ? voffAn[1] : voffA[1]; sA1[0] = last ? voffAn1[0] : voffA1[0]; sA1[1] = last ? voffAn1[1] : voffA1[1]; }
;             else { sA0[0] = voffA[0]; sA0[1] = voffA[1]; sA1[0] = voffA1[0]; sA1[1] = voffA1[1]; }
;             const char* a1 = cA + (size_t)(t + 1) * kstep;
;             const char* a2 = last ? nA : cA + (size_t)(t + 2) * kstep; const char* b2 = last ? nB : cB + (size_t)(t + 2) * kstep;
;             const char* a3 = a2 + kstep; const char* b3 = b2 + kstep;
;             PG8_LDB(B0, 0, 0); PG8_LDB(B1, 0, 1); PG8_SCHED; PG8_LDA(At, 0, 0); PG8_STAGE(PG8_SA(1, 1), a1, voffA1);
;             PG8_WAIT_V(8); PG8_WAIT_L(0); PG8_BAR; PG8_MMA(0, 0, At, B0); PG8_MMA(0, 1, At, B1); PG8_BAR; PG8_SCHED;
;             PG8_LDA(At, 0, 1); PG8_STAGE(PG8_SB(0, 0), b2, voffB); PG8_STAGE(PG8_SB(0, 1), b2 + hstepB, voffB); PG8_STAGE(PG8_SA(0, 0), a2, sA0);
;             PG8_WAIT_V(8); PG8_WAIT_L(0); PG8_BAR; PG8_MMA(1, 0, At, B0); PG8_MMA(1, 1, At, B1); PG8_BAR; PG8_SCHED;
.LBB0_1161:
	s_add_u32 s4, s2, 0x80
	s_addc_u32 s5, s3, 0
	s_add_i32 s65, 0, 0x10000
	s_cmp_eq_u32 s45, 12
	s_cselect_b32 s5, s47, s5
	s_cselect_b32 s4, s46, s4
	v_add_u32_e32 v96, s65, v197
	s_cselect_b32 s21, s49, s29
	s_cselect_b32 s20, s48, s1
	s_add_i32 s68, 0, 0x14000
	ds_read_b128 v[130:133], v96
	ds_read_b128 v[134:137], v96 offset:1024
	ds_read_b128 v[138:141], v96 offset:2048
	ds_read_b128 v[142:145], v96 offset:3072
	v_add_u32_e32 v96, s68, v197
	ds_read_b128 v[146:149], v96
	ds_read_b128 v[150:153], v96 offset:1024
	ds_read_b128 v[154:157], v96 offset:2048
	ds_read_b128 v[158:161], v96 offset:3072
	v_mov_b32_e32 v96, v191
	ds_read_b128 v[162:165], v228
	ds_read_b128 v[166:169], v228 offset:1024
	ds_read_b128 v[170:173], v228 offset:2048
	ds_read_b128 v[174:177], v228 offset:3072
	ds_read_b128 v[178:181], v228 offset:4096
	ds_read_b128 v[182:185], v228 offset:5120
	ds_read_b128 v[186:189], v228 offset:6144
	ds_read_b128 v[230:233], v228 offset:7168
	s_add_i32 m0, s55, 0xc000
	s_nop 0
	global_load_lds_dwordx4 v96, s[2:3]
	v_mov_b32_e32 v96, v194
	s_add_i32 m0, s55, 0xe000
	s_nop 0
	global_load_lds_dwordx4 v96, s[2:3]
	s_waitcnt vmcnt(8)
	s_waitcnt lgkmcnt(0)
	s_barrier
	v_mfma_f32_16x16x32_bf16 v[126:129], v[130:133], v[162:165], v[126:129]
	v_mfma_f32_16x16x32_bf16 v[122:125], v[138:141], v[162:165], v[122:125]
	v_mfma_f32_16x16x32_bf16 v[114:117], v[130:133], v[170:173], v[114:117]
	v_mfma_f32_16x16x32_bf16 v[106:109], v[138:141], v[170:173], v[106:109]
	v_mfma_f32_16x16x32_bf16 v[98:101], v[130:133], v[178:181], v[98:101]
	v_mfma_f32_16x16x32_bf16 v[88:91], v[138:141], v[178:181], v[88:91]
	v_mfma_f32_16x16x32_bf16 v[80:83], v[130:133], v[186:189], v[80:83]
	v_mfma_f32_16x16x32_bf16 v[72:75], v[138:141], v[186:189], v[72:75]
	v_mfma_f32_16x16x32_bf16 v[126:129], v[134:137], v[166:169], v[126:129]
	v_mfma_f32_16x16x32_bf16 v[122:125], v[142:145], v[166:169], v[122:125]
	v_mfma_f32_16x16x32_bf16 v[114:117], v[134:137], v[174:177], v[114:117]
	v_mfma_f32_16x16x32_bf16 v[106:109], v[142:145], v[174:177], v[106:109]
	v_mfma_f32_16x16x32_bf16 v[98:101], v[134:137], v[182:185], v[98:101]
	v_mfma_f32_16x16x32_bf16 v[88:91], v[142:145], v[182:185], v[88:91]
	v_mfma_f32_16x16x32_bf16 v[80:83], v[134:137], v[230:233], v[80:83]
	v_mfma_f32_16x16x32_bf16 v[72:75], v[142:145], v[230:233], v[72:75]
	v_mfma_f32_16x16x32_bf16 v[118:121], v[146:149], v[162:165], v[118:121]
	v_mfma_f32_16x16x32_bf16 v[110:113], v[154:157], v[162:165], v[110:113]
	v_mfma_f32_16x16x32_bf16 v[102:105], v[146:149], v[170:173], v[102:105]
	v_mfma_f32_16x16x32_bf16 v[92:95], v[154:157], v[170:173], v[92:95]
	v_mfma_f32_16x16x32_bf16 v[84:87], v[146:149], v[178:181], v[84:87]
	v_mfma_f32_16x16x32_bf16 v[76:79], v[154:157], v[178:181], v[76:79]
	v_mfma_f32_16x16x32_bf16 v[68:71], v[146:149], v[186:189], v[68:71]
	v_mfma_f32_16x16x32_bf16 v[64:67], v[154:157], v[186:189], v[64:67]
	v_mfma_f32_16x16x32_bf16 v[118:121], v[150:153], v[166:169], v[118:121]
	v_mfma_f32_16x16x32_bf16 v[110:113], v[158:161], v[166:169], v[110:113]
	v_mfma_f32_16x16x32_bf16 v[102:105], v[150:153], v[174:177], v[102:105]
	v_mfma_f32_16x16x32_bf16 v[92:95], v[158:161], v[174:177], v[92:95]
	v_mfma_f32_16x16x32_bf16 v[84:87], v[150:153], v[182:185], v[84:87]
	v_mfma_f32_16x16x32_bf16 v[76:79], v[158:161], v[182:185], v[76:79]
	v_mfma_f32_16x16x32_bf16 v[68:71], v[150:153], v[230:233], v[68:71]
	v_mfma_f32_16x16x32_bf16 v[64:67], v[158:161], v[230:233], v[64:67]
	s_barrier
	v_mov_b32_e32 v96, v192
	s_add_i32 s65, s65, s54
	ds_read_b128 v[162:165], v228 offset:16384
	ds_read_b128 v[166:169], v228 offset:17408
	ds_read_b128 v[170:173], v228 offset:18432
	ds_read_b128 v[174:177], v228 offset:19456
	ds_read_b128 v[178:181], v228 offset:20480
	ds_read_b128 v[182:185], v228 offset:21504
	ds_read_b128 v[186:189], v228 offset:22528
	ds_read_b128 v[230:233], v228 offset:23552
	s_mov_b32 m0, s65
	s_nop 0
	global_load_lds_dwordx4 v96, s[20:21]
	v_mov_b32_e32 v96, v195
	s_add_i32 m0, s65, 0x2000
	s_add_u32 s66, s20, 0x40000
	global_load_lds_dwordx4 v96, s[20:21]
	s_addc_u32 s67, s21, 0
	v_mov_b32_e32 v96, v192
	s_add_i32 s65, s68, s54
	s_mov_b32 m0, s65
	s_nop 0
	global_load_lds_dwordx4 v96, s[66:67]
	v_mov_b32_e32 v96, v195
	s_add_i32 m0, s65, 0x2000
	s_nop 0
	global_load_lds_dwordx4 v96, s[66:67]
	v_mov_b32_e32 v96, v190
	s_mov_b32 m0, s55
	s_nop 0
	global_load_lds_dwordx4 v96, s[4:5]
	v_mov_b32_e32 v96, v193
	s_mov_b32 m0, s56
	s_nop 0
	global_load_lds_dwordx4 v96, s[4:5]
	s_waitcnt vmcnt(8)
	s_waitcnt lgkmcnt(0)
	s_barrier
	v_mfma_f32_16x16x32_bf16 v[60:63], v[130:133], v[162:165], v[60:63]
	v_mfma_f32_16x16x32_bf16 v[56:59], v[138:141], v[162:165], v[56:59]
	v_mfma_f32_16x16x32_bf16 v[40:43], v[130:133], v[170:173], v[40:43]
	v_mfma_f32_16x16x32_bf16 v[32:35], v[138:141], v[170:173], v[32:35]
	v_mfma_f32_16x16x32_bf16 v[16:19], v[130:133], v[178:181], v[16:19]
	v_mfma_f32_16x16x32_bf16 v[8:11], v[138:141], v[178:181], v[8:11]
	v_mfma_f32_16x16x32_bf16 v[4:7], v[130:133], v[186:189], v[4:7]
	v_mfma_f32_16x16x32_bf16 v[0:3], v[138:141], v[186:189], v[0:3]
	v_mfma_f32_16x16x32_bf16 v[60:63], v[134:137], v[166:169], v[60:63]
	v_mfma_f32_16x16x32_bf16 v[56:59], v[142:145], v[166:169], v[56:59]
	v_mfma_f32_16x16x32_bf16 v[40:43], v[134:137], v[174:177], v[40:43]
	v_mfma_f32_16x16x32_bf16 v[32:35], v[142:145], v[174:177], v[32:35]
	v_mfma_f32_16x16x32_bf16 v[16:19], v[134:137], v[182:185], v[16:19]
	v_mfma_f32_16x16x32_bf16 v[8:11], v[142:145], v[182:185], v[8:11]
	v_mfma_f32_16x16x32_bf16 v[4:7], v[134:137], v[230:233], v[4:7]
	v_mfma_f32_16x16x32_bf16 v[0:3], v[142:145], v[230:233], v[0:3]
	v_mfma_f32_16x16x32_bf16 v[44:47], v[146:149], v[162:165], v[44:47]
	v_mfma_f32_16x16x32_bf16 v[36:39], v[154:157], v[162:165], v[36:39]
	v_mfma_f32_16x16x32_bf16 v[20:23], v[146:149], v[170:173], v[20:23]
	v_mfma_f32_16x16x32_bf16 v[12:15], v[154:157], v[170:173], v[12:15]
	v_mfma_f32_16x16x32_bf16 v[52:55], v[146:149], v[178:181], v[52:55]
	v_mfma_f32_16x16x32_bf16 v[48:51], v[154:157], v[178:181], v[48:51]
	v_mfma_f32_16x16x32_bf16 v[28:31], v[146:149], v[186:189], v[28:31]
	v_mfma_f32_16x16x32_bf16 v[24:27], v[154:157], v[186:189], v[24:27]
	v_mfma_f32_16x16x32_bf16 v[44:47], v[150:153], v[166:169], v[44:47]
	v_mfma_f32_16x16x32_bf16 v[36:39], v[158:161], v[166:169], v[36:39]
	v_mfma_f32_16x16x32_bf16 v[20:23], v[150:153], v[174:177], v[20:23]
	v_mfma_f32_16x16x32_bf16 v[12:15], v[158:161], v[174:177], v[12:15]
	v_mfma_f32_16x16x32_bf16 v[52:55], v[150:153], v[182:185], v[52:55]
	v_mfma_f32_16x16x32_bf16 v[48:51], v[158:161], v[182:185], v[48:51]
	v_mfma_f32_16x16x32_bf16 v[28:31], v[150:153], v[230:233], v[28:31]
	v_mfma_f32_16x16x32_bf16 v[24:27], v[158:161], v[230:233], v[24:27]
	s_barrier
; #define PG8_STAGE(bufoff, gbase, voff) do { _Pragma("unroll") for (int _i = 0; _i < 2; ++_i) \
;         __builtin_amdgcn_global_load_lds((const __attribute__((address_space(1))) unsigned*)((const __attribute__((address_space(1))) char*)(gbase) + (unsigned)lnd_v((int)(voff)[_i])), (LAS unsigned*)(lds + (bufoff) + ldsw + _i * 8192), 16, 0, 0); } while (0)
; #define PG8_LDA(dst, b, h) do { _Pragma("unroll") for (int m = 0; m < 4; ++m) _Pragma("unroll") for (int k = 0; k < 2; ++k) dst[m][k] = *(const LAS bf16x8*)(lds + PG8_SA(b, h) + aoff + m * 2048 + k * 1024); } while (0)
; #define PG8_LDB(dst, b, h) do { _Pragma("unroll") for (int n = 0; n < 2; ++n) _Pragma("unroll") for (int k = 0; k < 2; ++k) dst[n][k] = *(const LAS bf16x8*)(lds + PG8_SB(b, h) + boff + n * 2048 + k * 1024); } while (0)
; #define PG8_MMA(ai, bj, At, Bt) do { __builtin_amdgcn_s_setprio(1); _Pragma("unroll") for (int m = 0; m < 4; ++m) _Pragma("unroll") for (int n = 0; n < 2; ++n) _Pragma("unroll") for (int k = 0; k < 2; ++k) \
;         acc[ai][bj][m][n] = __builtin_amdgcn_mfma_f32_16x16x32_bf16(Bt[n][k], At[m][k], acc[ai][bj][m][n], 0, 0, 0); __builtin_amdgcn_s_setprio(0); } while (0)
; #define PG8_WAIT_V(n) asm volatile("s_waitcnt vmcnt(" #n ")" ::: "memory")
; #define PG8_WAIT_L(n) asm volatile("s_waitcnt lgkmcnt(" #n ")" ::: "memory")
; #define PG8_BAR __builtin_amdgcn_s_barrier()
; #define PG8_SCHED __builtin_amdgcn_sched_barrier(0)
; template <class Desc, class Epi>
; __device__ __forceinline__ void gemm_phase(const int wv_, LAS unsigned char* lds, const Desc& d, const Epi& E) {
;     ...
;             PG8_LDB(B0, 1, 0); PG8_LDB(B1, 1, 1); PG8_SCHED; PG8_LDA(At, 1, 0); PG8_STAGE(PG8_SA(0, 1), a2, sA1);
;             PG8_WAIT_V(8); PG8_WAIT_L(0); PG8_BAR; PG8_MMA(0, 0, At, B0); PG8_MMA(0, 1, At, B1); PG8_BAR; PG8_SCHED;
	s_add_i32 s65, 0, 0x18000
	v_add_u32_e32 v96, s65, v197
	s_add_i32 s66, 0, 0x1c000
	ds_read_b128 v[130:133], v96
	ds_read_b128 v[134:137], v96 offset:1024
	ds_read_b128 v[138:141], v96 offset:2048
	ds_read_b128 v[142:145], v96 offset:3072
	v_add_u32_e32 v96, s66, v197
	ds_read_b128 v[146:149], v96
	ds_read_b128 v[150:153], v96 offset:1024
	ds_read_b128 v[154:157], v96 offset:2048
	ds_read_b128 v[158:161], v96 offset:3072
	v_mov_b32_e32 v96, v191
	s_mov_b32 m0, s57
	ds_read_b128 v[162:165], v228 offset:32768
	ds_read_b128 v[166:169], v228 offset:33792
	ds_read_b128 v[170:173], v228 offset:34816
	ds_read_b128 v[174:177], v228 offset:35840
	ds_read_b128 v[178:181], v228 offset:36864
	ds_read_b128 v[182:185], v228 offset:37888
	ds_read_b128 v[186:189], v228 offset:38912
	ds_read_b128 v[230:233], v228 offset:39936
	s_nop 0
	global_load_lds_dwordx4 v96, s[4:5]
	v_mov_b32_e32 v96, v194
	s_mov_b32 m0, s58
	s_nop 0
	global_load_lds_dwordx4 v96, s[4:5]
	s_waitcnt vmcnt(8)
	s_waitcnt lgkmcnt(0)
	s_barrier
	v_mfma_f32_16x16x32_bf16 v[126:129], v[130:133], v[162:165], v[126:129]
	v_mfma_f32_16x16x32_bf16 v[122:125], v[138:141], v[162:165], v[122:125]
	v_mfma_f32_16x16x32_bf16 v[114:117], v[130:133], v[170:173], v[114:117]
	v_mfma_f32_16x16x32_bf16 v[106:109], v[138:141], v[170:173], v[106:109]
	v_mfma_f32_16x16x32_bf16 v[98:101], v[130:133], v[178:181], v[98:101]
	v_mfma_f32_16x16x32_bf16 v[88:91], v[138:141], v[178:181], v[88:91]
	v_mfma_f32_16x16x32_bf16 v[80:83], v[130:133], v[186:189], v[80:83]
	v_mfma_f32_16x16x32_bf16 v[72:75], v[138:141], v[186:189], v[72:75]
	v_mfma_f32_16x16x32_bf16 v[126:129], v[134:137], v[166:169], v[126:129]
	v_mfma_f32_16x16x32_bf16 v[122:125], v[142:145], v[166:169], v[122:125]
	v_mfma_f32_16x16x32_bf16 v[114:117], v[134:137], v[174:177], v[114:117]
	v_mfma_f32_16x16x32_bf16 v[106:109], v[142:145], v[174:177], v[106:109]
	v_mfma_f32_16x16x32_bf16 v[98:101], v[134:137], v[182:185], v[98:101]
	v_mfma_f32_16x16x32_bf16 v[88:91], v[142:145], v[182:185], v[88:91]
	v_mfma_f32_16x16x32_bf16 v[80:83], v[134:137], v[230:233], v[80:83]
	v_mfma_f32_16x16x32_bf16 v[72:75], v[142:145], v[230:233], v[72:75]
	v_mfma_f32_16x16x32_bf16 v[118:121], v[146:149], v[162:165], v[118:121]
	v_mfma_f32_16x16x32_bf16 v[110:113], v[154:157], v[162:165], v[110:113]
	v_mfma_f32_16x16x32_bf16 v[102:105], v[146:149], v[170:173], v[102:105]
	v_mfma_f32_16x16x32_bf16 v[92:95], v[154:157], v[170:173], v[92:95]
	v_mfma_f32_16x16x32_bf16 v[84:87], v[146:149], v[178:181], v[84:87]
	v_mfma_f32_16x16x32_bf16 v[76:79], v[154:157], v[178:181], v[76:79]
	v_mfma_f32_16x16x32_bf16 v[68:71], v[146:149], v[186:189], v[68:71]
	v_mfma_f32_16x16x32_bf16 v[64:67], v[154:157], v[186:189], v[64:67]
	v_mfma_f32_16x16x32_bf16 v[118:121], v[150:153], v[166:169], v[118:121]
	v_mfma_f32_16x16x32_bf16 v[110:113], v[158:161], v[166:169], v[110:113]
	v_mfma_f32_16x16x32_bf16 v[102:105], v[150:153], v[174:177], v[102:105]
	v_mfma_f32_16x16x32_bf16 v[92:95], v[158:161], v[174:177], v[92:95]
	v_mfma_f32_16x16x32_bf16 v[84:87], v[150:153], v[182:185], v[84:87]
	v_mfma_f32_16x16x32_bf16 v[76:79], v[158:161], v[182:185], v[76:79]
	v_mfma_f32_16x16x32_bf16 v[68:71], v[150:153], v[230:233], v[68:71]
	v_mfma_f32_16x16x32_bf16 v[64:67], v[158:161], v[230:233], v[64:67]
	s_barrier
; #define PG8_STAGE(bufoff, gbase, voff) do { _Pragma("unroll") for (int _i = 0; _i < 2; ++_i) \
;         __builtin_amdgcn_global_load_lds((const __attribute__((address_space(1))) unsigned*)((const __attribute__((address_space(1))) char*)(gbase) + (unsigned)lnd_v((int)(voff)[_i])), (LAS unsigned*)(lds + (bufoff) + ldsw + _i * 8192), 16, 0, 0); } while (0)
; #define PG8_LDA(dst, b, h) do { _Pragma("unroll") for (int m = 0; m < 4; ++m) _Pragma("unroll") for (int k = 0; k < 2; ++k) dst[m][k] = *(const LAS bf16x8*)(lds + PG8_SA(b, h) + aoff + m * 2048 + k * 1024); } while (0)
; #define PG8_MMA(ai, bj, At, Bt) do { __builtin_amdgcn_s_setprio(1); _Pragma("unroll") for (int m = 0; m < 4; ++m) _Pragma("unroll") for (int n = 0; n < 2; ++n) _Pragma("unroll") for (int k = 0; k < 2; ++k) \
;         acc[ai][bj][m][n] = __builtin_amdgcn_mfma_f32_16x16x32_bf16(Bt[n][k], At[m][k], acc[ai][bj][m][n], 0, 0, 0); __builtin_amdgcn_s_setprio(0); } while (0)
; #define PG8_WAIT_V(n) asm volatile("s_waitcnt vmcnt(" #n ")" ::: "memory")
; #define PG8_WAIT_L(n) asm volatile("s_waitcnt lgkmcnt(" #n ")" ::: "memory")
; #define PG8_BAR __builtin_amdgcn_s_barrier()
; #define PG8_SCHED __builtin_amdgcn_sched_barrier(0)
; template <class Desc, class Epi>
; __device__ __forceinline__ void gemm_phase(const int wv_, LAS unsigned char* lds, const Desc& d, const Epi& E) {
;     ...
;             PG8_LDA(At, 1, 1); PG8_STAGE(PG8_SB(1, 0), b3, voffB); PG8_STAGE(PG8_SB(1, 1), b3 + hstepB, voffB); PG8_STAGE(PG8_SA(1, 0), a3, sA0);
;             PG8_WAIT_V(8); PG8_WAIT_L(0); PG8_BAR; PG8_MMA(1, 0, At, B0); PG8_MMA(1, 1, At, B1); PG8_BAR; PG8_SCHED;
;         }
;         if (wr == 0) PG8_BAR;
	v_mov_b32_e32 v96, v192
	ds_read_b128 v[162:165], v228 offset:49152
	ds_read_b128 v[166:169], v228 offset:50176
	ds_read_b128 v[170:173], v228 offset:51200
	ds_read_b128 v[174:177], v228 offset:52224
	ds_read_b128 v[178:181], v228 offset:53248
	ds_read_b128 v[182:185], v228 offset:54272
	ds_read_b128 v[186:189], v228 offset:55296
	ds_read_b128 v[230:233], v228 offset:56320
	s_add_i32 s65, s65, s54
	v_lshl_add_u64 v[234:235], s[20:21], 0, v[96:97]
	v_lshl_add_u64 v[234:235], v[234:235], 0, s[30:31]
	s_mov_b32 m0, s65
	v_mov_b32_e32 v96, v195
	global_load_lds_dwordx4 v[234:235], off
	s_add_i32 m0, s65, 0x2000
	s_nop 0
	v_lshl_add_u64 v[234:235], s[20:21], 0, v[96:97]
	s_add_u32 s20, s20, 0x40080
	v_lshl_add_u64 v[234:235], v[234:235], 0, s[30:31]
	s_addc_u32 s21, s21, 0
	v_mov_b32_e32 v96, v192
	s_add_i32 s65, s66, s54
	global_load_lds_dwordx4 v[234:235], off
	s_mov_b32 m0, s65
	s_nop 0
	global_load_lds_dwordx4 v96, s[20:21]
	v_mov_b32_e32 v96, v195
	s_add_i32 m0, s65, 0x2000
	s_nop 0
	global_load_lds_dwordx4 v96, s[20:21]
	v_mov_b32_e32 v96, v190
	s_mov_b32 m0, s59
	v_lshl_add_u64 v[234:235], s[4:5], 0, v[96:97]
	v_lshl_add_u64 v[234:235], v[234:235], 0, s[30:31]
	v_mov_b32_e32 v96, v193
	global_load_lds_dwordx4 v[234:235], off
	s_mov_b32 m0, s60
	v_lshl_add_u64 v[234:235], s[4:5], 0, v[96:97]
	v_lshl_add_u64 v[234:235], v[234:235], 0, s[30:31]
	global_load_lds_dwordx4 v[234:235], off
	s_waitcnt vmcnt(8)
	s_waitcnt lgkmcnt(0)
	s_barrier
	v_mfma_f32_16x16x32_bf16 v[60:63], v[130:133], v[162:165], v[60:63]
	v_mfma_f32_16x16x32_bf16 v[56:59], v[138:141], v[162:165], v[56:59]
	v_mfma_f32_16x16x32_bf16 v[40:43], v[130:133], v[170:173], v[40:43]
	v_mfma_f32_16x16x32_bf16 v[32:35], v[138:141], v[170:173], v[32:35]
	v_mfma_f32_16x16x32_bf16 v[16:19], v[130:133], v[178:181], v[16:19]
	v_mfma_f32_16x16x32_bf16 v[8:11], v[138:141], v[178:181], v[8:11]
	v_mfma_f32_16x16x32_bf16 v[4:7], v[130:133], v[186:189], v[4:7]
	v_mfma_f32_16x16x32_bf16 v[0:3], v[138:141], v[186:189], v[0:3]
	v_mfma_f32_16x16x32_bf16 v[60:63], v[134:137], v[166:169], v[60:63]
	v_mfma_f32_16x16x32_bf16 v[56:59], v[142:145], v[166:169], v[56:59]
	v_mfma_f32_16x16x32_bf16 v[40:43], v[134:137], v[174:177], v[40:43]
	v_mfma_f32_16x16x32_bf16 v[32:35], v[142:145], v[174:177], v[32:35]
	v_mfma_f32_16x16x32_bf16 v[16:19], v[134:137], v[182:185], v[16:19]
	v_mfma_f32_16x16x32_bf16 v[8:11], v[142:145], v[182:185], v[8:11]
	v_mfma_f32_16x16x32_bf16 v[4:7], v[134:137], v[230:233], v[4:7]
	v_mfma_f32_16x16x32_bf16 v[0:3], v[142:145], v[230:233], v[0:3]
	v_mfma_f32_16x16x32_bf16 v[44:47], v[146:149], v[162:165], v[44:47]
	v_mfma_f32_16x16x32_bf16 v[36:39], v[154:157], v[162:165], v[36:39]
	v_mfma_f32_16x16x32_bf16 v[20:23], v[146:149], v[170:173], v[20:23]
	v_mfma_f32_16x16x32_bf16 v[12:15], v[154:157], v[170:173], v[12:15]
	v_mfma_f32_16x16x32_bf16 v[52:55], v[146:149], v[178:181], v[52:55]
	v_mfma_f32_16x16x32_bf16 v[48:51], v[154:157], v[178:181], v[48:51]
	v_mfma_f32_16x16x32_bf16 v[28:31], v[146:149], v[186:189], v[28:31]
	v_mfma_f32_16x16x32_bf16 v[24:27], v[154:157], v[186:189], v[24:27]
	v_mfma_f32_16x16x32_bf16 v[44:47], v[150:153], v[166:169], v[44:47]
	v_mfma_f32_16x16x32_bf16 v[36:39], v[158:161], v[166:169], v[36:39]
	v_mfma_f32_16x16x32_bf16 v[20:23], v[150:153], v[174:177], v[20:23]
	v_mfma_f32_16x16x32_bf16 v[12:15], v[158:161], v[174:177], v[12:15]
	v_mfma_f32_16x16x32_bf16 v[52:55], v[150:153], v[182:185], v[52:55]
	v_mfma_f32_16x16x32_bf16 v[48:51], v[158:161], v[182:185], v[48:51]
	v_mfma_f32_16x16x32_bf16 v[28:31], v[150:153], v[230:233], v[28:31]
	v_mfma_f32_16x16x32_bf16 v[24:27], v[158:161], v[230:233], v[24:27]
	s_barrier
	s_add_i32 s45, s45, 2
	s_add_u32 s2, s2, 0x100
	s_addc_u32 s3, s3, 0
	s_add_u32 s1, s1, 0x100
	s_addc_u32 s29, s29, 0
	s_cmp_gt_u32 s45, 13
	s_cbranch_scc0 .LBB0_1161
	s_and_b64 vcc, exec, s[42:43]
	s_cbranch_vccz .LBB0_1164
	s_barrier

; #define PG8_STAGE(bufoff, gbase, voff) do { _Pragma("unroll") for (int _i = 0; _i < 2; ++_i) \
;         __builtin_amdgcn_global_load_lds((const __attribute__((address_space(1))) unsigned*)((const __attribute__((address_space(1))) char*)(gbase) + (unsigned)lnd_v((int)(voff)[_i])), (LAS unsigned*)(lds + (bufoff) + ldsw + _i * 8192), 16, 0, 0); } while (0)
; #define PG8_LDA(dst, b, h) do { _Pragma("unroll") for (int m = 0; m < 4; ++m) _Pragma("unroll") for (int k = 0; k < 2; ++k) dst[m][k] = *(const LAS bf16x8*)(lds + PG8_SA(b, h) + aoff + m * 2048 + k * 1024); } while (0)
; #define PG8_LDB(dst, b, h) do { _Pragma("unroll") for (int n = 0; n < 2; ++n) _Pragma("unroll") for (int k = 0; k < 2; ++k) dst[n][k] = *(const LAS bf16x8*)(lds + PG8_SB(b, h) + boff + n * 2048 + k * 1024); } while (0)
; #define PG8_MMA(ai, bj, At, Bt) do { __builtin_amdgcn_s_setprio(1); _Pragma("unroll") for (int m = 0; m < 4; ++m) _Pragma("unroll") for (int n = 0; n < 2; ++n) _Pragma("unroll") for (int k = 0; k < 2; ++k) \
;         acc[ai][bj][m][n] = __builtin_amdgcn_mfma_f32_16x16x32_bf16(Bt[n][k], At[m][k], acc[ai][bj][m][n], 0, 0, 0); __builtin_amdgcn_s_setprio(0); } while (0)
; template <class Desc, class Epi>
; __device__ __forceinline__ void gemm_phase(const int wv_, LAS unsigned char* lds, const Desc& d, const Epi& E) {
;     ...
;             const bool last = (t == nt - 2);
;             unsigned sA0[2], sA1[2];
;             if constexpr (Desc::GATHER) { sA0[0] = last ? voffAn[0] : voffA[0]; sA0[1] = last ? voffAn[1] : voffA[1]; sA1[0] = last ? voffAn1[0] : voffA1[0]; sA1[1] = last ? voffAn1[1] : voffA1[1]; }
;             else { sA0[0] = voffA[0]; sA0[1] = voffA[1]; sA1[0] = voffA1[0]; sA1[1] = voffA1[1]; }
;             const char* a1 = cA + (size_t)(t + 1) * kstep;
;             const char* a2 = last ? nA : cA + (size_t)(t + 2) * kstep; const char* b2 = last ? nB : cB + (size_t)(t + 2) * kstep;
;             const char* a3 = a2 + kstep; const char* b3 = b2 + kstep;
;             PG8_LDB(B0, 0, 0); PG8_LDB(B1, 0, 1); PG8_SCHED; PG8_LDA(At, 0, 0); PG8_STAGE(PG8_SA(1, 1), a1, voffA1);
;             PG8_WAIT_V(8); PG8_WAIT_L(0); PG8_BAR; PG8_MMA(0, 0, At, B0); PG8_MMA(0, 1, At, B1); PG8_BAR; PG8_SCHED;
;             PG8_LDA(At, 0, 1); PG8_STAGE(PG8_SB(0, 0), b2, voffB); PG8_STAGE(PG8_SB(0, 1), b2 + hstepB, voffB); PG8_STAGE(PG8_SA(0, 0), a2, sA0);
.LBB0_1262:
	s_add_u32 s4, s2, 0x80
	s_addc_u32 s5, s3, 0
	s_add_i32 s62, 0, 0x10000
	s_cmp_eq_u32 s61, 12
	s_cselect_b32 s5, s45, s5
	s_cselect_b32 s4, s44, s4
	v_add_u32_e32 v96, s62, v213
	s_cselect_b32 s21, s47, s43
	s_cselect_b32 s20, s46, s29
	s_add_i32 s64, 0, 0x14000
	ds_read_b128 v[130:133], v96
	ds_read_b128 v[134:137], v96 offset:1024
	ds_read_b128 v[138:141], v96 offset:2048
	ds_read_b128 v[142:145], v96 offset:3072
	v_add_u32_e32 v96, s64, v213
	ds_read_b128 v[146:149], v96
	ds_read_b128 v[150:153], v96 offset:1024
	ds_read_b128 v[154:157], v96 offset:2048
	ds_read_b128 v[158:161], v96 offset:3072
	v_mov_b32_e32 v96, v207
	ds_read_b128 v[162:165], v221
	ds_read_b128 v[166:169], v221 offset:1024
	ds_read_b128 v[170:173], v221 offset:2048
	ds_read_b128 v[174:177], v221 offset:3072
	ds_read_b128 v[178:181], v221 offset:4096
	ds_read_b128 v[182:185], v221 offset:5120
	ds_read_b128 v[186:189], v221 offset:6144
	ds_read_b128 v[190:193], v221 offset:7168
	s_add_i32 m0, s53, 0xc000
	s_nop 0
	global_load_lds_dwordx4 v96, s[2:3]
	v_mov_b32_e32 v96, v210
	s_add_i32 m0, s53, 0xe000
	s_nop 0
	global_load_lds_dwordx4 v96, s[2:3]
	s_waitcnt vmcnt(8)
	s_waitcnt lgkmcnt(0)
	s_barrier
	v_mfma_f32_16x16x32_bf16 v[126:129], v[130:133], v[162:165], v[126:129]
	v_mfma_f32_16x16x32_bf16 v[122:125], v[138:141], v[162:165], v[122:125]
	v_mfma_f32_16x16x32_bf16 v[110:113], v[130:133], v[170:173], v[110:113]
	v_mfma_f32_16x16x32_bf16 v[106:109], v[138:141], v[170:173], v[106:109]
	v_mfma_f32_16x16x32_bf16 v[92:95], v[130:133], v[178:181], v[92:95]
	v_mfma_f32_16x16x32_bf16 v[88:91], v[138:141], v[178:181], v[88:91]
	v_mfma_f32_16x16x32_bf16 v[76:79], v[130:133], v[186:189], v[76:79]
	v_mfma_f32_16x16x32_bf16 v[72:75], v[138:141], v[186:189], v[72:75]
	v_mfma_f32_16x16x32_bf16 v[126:129], v[134:137], v[166:169], v[126:129]
	v_mfma_f32_16x16x32_bf16 v[122:125], v[142:145], v[166:169], v[122:125]
	v_mfma_f32_16x16x32_bf16 v[110:113], v[134:137], v[174:177], v[110:113]
	v_mfma_f32_16x16x32_bf16 v[106:109], v[142:145], v[174:177], v[106:109]
	v_mfma_f32_16x16x32_bf16 v[92:95], v[134:137], v[182:185], v[92:95]
	v_mfma_f32_16x16x32_bf16 v[88:91], v[142:145], v[182:185], v[88:91]
	v_mfma_f32_16x16x32_bf16 v[76:79], v[134:137], v[190:193], v[76:79]
	v_mfma_f32_16x16x32_bf16 v[72:75], v[142:145], v[190:193], v[72:75]
	v_mfma_f32_16x16x32_bf16 v[118:121], v[146:149], v[162:165], v[118:121]
	v_mfma_f32_16x16x32_bf16 v[114:117], v[154:157], v[162:165], v[114:117]
	v_mfma_f32_16x16x32_bf16 v[102:105], v[146:149], v[170:173], v[102:105]
	v_mfma_f32_16x16x32_bf16 v[98:101], v[154:157], v[170:173], v[98:101]
	v_mfma_f32_16x16x32_bf16 v[84:87], v[146:149], v[178:181], v[84:87]
	v_mfma_f32_16x16x32_bf16 v[80:83], v[154:157], v[178:181], v[80:83]
	v_mfma_f32_16x16x32_bf16 v[68:71], v[146:149], v[186:189], v[68:71]
	v_mfma_f32_16x16x32_bf16 v[64:67], v[154:157], v[186:189], v[64:67]
	v_mfma_f32_16x16x32_bf16 v[118:121], v[150:153], v[166:169], v[118:121]
	v_mfma_f32_16x16x32_bf16 v[114:117], v[158:161], v[166:169], v[114:117]
	v_mfma_f32_16x16x32_bf16 v[102:105], v[150:153], v[174:177], v[102:105]
	v_mfma_f32_16x16x32_bf16 v[98:101], v[158:161], v[174:177], v[98:101]
	v_mfma_f32_16x16x32_bf16 v[84:87], v[150:153], v[182:185], v[84:87]
	v_mfma_f32_16x16x32_bf16 v[80:83], v[158:161], v[182:185], v[80:83]
	v_mfma_f32_16x16x32_bf16 v[68:71], v[150:153], v[190:193], v[68:71]
	v_mfma_f32_16x16x32_bf16 v[64:67], v[158:161], v[190:193], v[64:67]
	s_barrier
	v_mov_b32_e32 v96, v208
	s_add_i32 s62, s62, s52
	ds_read_b128 v[162:165], v221 offset:16384
	ds_read_b128 v[166:169], v221 offset:17408
	ds_read_b128 v[170:173], v221 offset:18432
	ds_read_b128 v[174:177], v221 offset:19456
	ds_read_b128 v[178:181], v221 offset:20480
	ds_read_b128 v[182:185], v221 offset:21504
	ds_read_b128 v[186:189], v221 offset:22528
	ds_read_b128 v[190:193], v221 offset:23552
	s_mov_b32 m0, s62
	s_nop 0
	global_load_lds_dwordx4 v96, s[20:21]
	v_mov_b32_e32 v96, v211
	s_add_i32 m0, s62, 0x2000
	s_add_u32 s62, s20, 0x40000
	global_load_lds_dwordx4 v96, s[20:21]
	s_addc_u32 s63, s21, 0
	v_mov_b32_e32 v96, v208
	s_add_i32 s64, s64, s52
	s_mov_b32 m0, s64
	s_nop 0
	global_load_lds_dwordx4 v96, s[62:63]
	v_mov_b32_e32 v96, v211
	s_add_i32 m0, s64, 0x2000
	s_nop 0
	global_load_lds_dwordx4 v96, s[62:63]
	v_mov_b32_e32 v96, v206
	s_mov_b32 m0, s53
	s_nop 0
	global_load_lds_dwordx4 v96, s[4:5]
	v_mov_b32_e32 v96, v209
	s_mov_b32 m0, s54
	s_nop 0
	global_load_lds_dwordx4 v96, s[4:5]
	s_waitcnt vmcnt(8)
	s_waitcnt lgkmcnt(0)
	s_barrier
; #define PG8_STAGE(bufoff, gbase, voff) do { _Pragma("unroll") for (int _i = 0; _i < 2; ++_i) \
;         __builtin_amdgcn_global_load_lds((const __attribute__((address_space(1))) unsigned*)((const __attribute__((address_space(1))) char*)(gbase) + (unsigned)lnd_v((int)(voff)[_i])), (LAS unsigned*)(lds + (bufoff) + ldsw + _i * 8192), 16, 0, 0); } while (0)
; #define PG8_LDA(dst, b, h) do { _Pragma("unroll") for (int m = 0; m < 4; ++m) _Pragma("unroll") for (int k = 0; k < 2; ++k) dst[m][k] = *(const LAS bf16x8*)(lds + PG8_SA(b, h) + aoff + m * 2048 + k * 1024); } while (0)
; #define PG8_LDB(dst, b, h) do { _Pragma("unroll") for (int n = 0; n < 2; ++n) _Pragma("unroll") for (int k = 0; k < 2; ++k) dst[n][k] = *(const LAS bf16x8*)(lds + PG8_SB(b, h) + boff + n * 2048 + k * 1024); } while (0)
; #define PG8_MMA(ai, bj, At, Bt) do { __builtin_amdgcn_s_setprio(1); _Pragma("unroll") for (int m = 0; m < 4; ++m) _Pragma("unroll") for (int n = 0; n < 2; ++n) _Pragma("unroll") for (int k = 0; k < 2; ++k) \
;         acc[ai][bj][m][n] = __builtin_amdgcn_mfma_f32_16x16x32_bf16(Bt[n][k], At[m][k], acc[ai][bj][m][n], 0, 0, 0); __builtin_amdgcn_s_setprio(0); } while (0)
; #define PG8_WAIT_V(n) asm volatile("s_waitcnt vmcnt(" #n ")" ::: "memory")
; #define PG8_WAIT_L(n) asm volatile("s_waitcnt lgkmcnt(" #n ")" ::: "memory")
; #define PG8_BAR __builtin_amdgcn_s_barrier()
; #define PG8_SCHED __builtin_amdgcn_sched_barrier(0)
; template <class Desc, class Epi>
; __device__ __forceinline__ void gemm_phase(const int wv_, LAS unsigned char* lds, const Desc& d, const Epi& E) {
;     ...
;             PG8_WAIT_V(8); PG8_WAIT_L(0); PG8_BAR; PG8_MMA(1, 0, At, B0); PG8_MMA(1, 1, At, B1); PG8_BAR; PG8_SCHED;
;             PG8_LDB(B0, 1, 0); PG8_LDB(B1, 1, 1); PG8_SCHED; PG8_LDA(At, 1, 0); PG8_STAGE(PG8_SA(0, 1), a2, sA1);
;             PG8_WAIT_V(8); PG8_WAIT_L(0); PG8_BAR; PG8_MMA(0, 0, At, B0); PG8_MMA(0, 1, At, B1); PG8_BAR; PG8_SCHED;
	v_mfma_f32_16x16x32_bf16 v[60:63], v[130:133], v[162:165], v[60:63]
	v_mfma_f32_16x16x32_bf16 v[56:59], v[138:141], v[162:165], v[56:59]
	v_mfma_f32_16x16x32_bf16 v[44:47], v[130:133], v[170:173], v[44:47]
	v_mfma_f32_16x16x32_bf16 v[40:43], v[138:141], v[170:173], v[40:43]
	v_mfma_f32_16x16x32_bf16 v[24:27], v[130:133], v[178:181], v[24:27]
	v_mfma_f32_16x16x32_bf16 v[16:19], v[138:141], v[178:181], v[16:19]
	v_mfma_f32_16x16x32_bf16 v[4:7], v[130:133], v[186:189], v[4:7]
	v_mfma_f32_16x16x32_bf16 v[0:3], v[138:141], v[186:189], v[0:3]
	v_mfma_f32_16x16x32_bf16 v[60:63], v[134:137], v[166:169], v[60:63]
	v_mfma_f32_16x16x32_bf16 v[56:59], v[142:145], v[166:169], v[56:59]
	v_mfma_f32_16x16x32_bf16 v[44:47], v[134:137], v[174:177], v[44:47]
	v_mfma_f32_16x16x32_bf16 v[40:43], v[142:145], v[174:177], v[40:43]
	v_mfma_f32_16x16x32_bf16 v[24:27], v[134:137], v[182:185], v[24:27]
	v_mfma_f32_16x16x32_bf16 v[16:19], v[142:145], v[182:185], v[16:19]
	v_mfma_f32_16x16x32_bf16 v[4:7], v[134:137], v[190:193], v[4:7]
	v_mfma_f32_16x16x32_bf16 v[0:3], v[142:145], v[190:193], v[0:3]
	v_mfma_f32_16x16x32_bf16 v[52:55], v[146:149], v[162:165], v[52:55]
	v_mfma_f32_16x16x32_bf16 v[48:51], v[154:157], v[162:165], v[48:51]
	v_mfma_f32_16x16x32_bf16 v[28:31], v[146:149], v[170:173], v[28:31]
	v_mfma_f32_16x16x32_bf16 v[20:23], v[154:157], v[170:173], v[20:23]
	v_mfma_f32_16x16x32_bf16 v[36:39], v[146:149], v[178:181], v[36:39]
	v_mfma_f32_16x16x32_bf16 v[32:35], v[154:157], v[178:181], v[32:35]
	v_mfma_f32_16x16x32_bf16 v[12:15], v[146:149], v[186:189], v[12:15]
	v_mfma_f32_16x16x32_bf16 v[8:11], v[154:157], v[186:189], v[8:11]
	v_mfma_f32_16x16x32_bf16 v[52:55], v[150:153], v[166:169], v[52:55]
	v_mfma_f32_16x16x32_bf16 v[48:51], v[158:161], v[166:169], v[48:51]
	v_mfma_f32_16x16x32_bf16 v[28:31], v[150:153], v[174:177], v[28:31]
	v_mfma_f32_16x16x32_bf16 v[20:23], v[158:161], v[174:177], v[20:23]
	v_mfma_f32_16x16x32_bf16 v[36:39], v[150:153], v[182:185], v[36:39]
	v_mfma_f32_16x16x32_bf16 v[32:35], v[158:161], v[182:185], v[32:35]
	v_mfma_f32_16x16x32_bf16 v[12:15], v[150:153], v[190:193], v[12:15]
	v_mfma_f32_16x16x32_bf16 v[8:11], v[158:161], v[190:193], v[8:11]
	s_barrier
	s_add_i32 s62, 0, 0x18000
	v_add_u32_e32 v96, s62, v213
	s_add_i32 s63, 0, 0x1c000
	ds_read_b128 v[130:133], v96
	ds_read_b128 v[134:137], v96 offset:1024
	ds_read_b128 v[138:141], v96 offset:2048
	ds_read_b128 v[142:145], v96 offset:3072
	v_add_u32_e32 v96, s63, v213
	ds_read_b128 v[146:149], v96
	ds_read_b128 v[150:153], v96 offset:1024
	ds_read_b128 v[154:157], v96 offset:2048
	ds_read_b128 v[158:161], v96 offset:3072
	v_mov_b32_e32 v96, v207
	s_mov_b32 m0, s55
	ds_read_b128 v[162:165], v221 offset:32768
	ds_read_b128 v[166:169], v221 offset:33792
	ds_read_b128 v[170:173], v221 offset:34816
	ds_read_b128 v[174:177], v221 offset:35840
	ds_read_b128 v[178:181], v221 offset:36864
	ds_read_b128 v[182:185], v221 offset:37888
	ds_read_b128 v[186:189], v221 offset:38912
	ds_read_b128 v[190:193], v221 offset:39936
	s_nop 0
	global_load_lds_dwordx4 v96, s[4:5]
	v_mov_b32_e32 v96, v210
	s_mov_b32 m0, s56
	s_nop 0
	global_load_lds_dwordx4 v96, s[4:5]
	s_waitcnt vmcnt(8)
	s_waitcnt lgkmcnt(0)
	s_barrier
	v_mfma_f32_16x16x32_bf16 v[126:129], v[130:133], v[162:165], v[126:129]
	v_mfma_f32_16x16x32_bf16 v[122:125], v[138:141], v[162:165], v[122:125]
	v_mfma_f32_16x16x32_bf16 v[110:113], v[130:133], v[170:173], v[110:113]
	v_mfma_f32_16x16x32_bf16 v[106:109], v[138:141], v[170:173], v[106:109]
	v_mfma_f32_16x16x32_bf16 v[92:95], v[130:133], v[178:181], v[92:95]
	v_mfma_f32_16x16x32_bf16 v[88:91], v[138:141], v[178:181], v[88:91]
	v_mfma_f32_16x16x32_bf16 v[76:79], v[130:133], v[186:189], v[76:79]
	v_mfma_f32_16x16x32_bf16 v[72:75], v[138:141], v[186:189], v[72:75]
	v_mfma_f32_16x16x32_bf16 v[126:129], v[134:137], v[166:169], v[126:129]
	v_mfma_f32_16x16x32_bf16 v[122:125], v[142:145], v[166:169], v[122:125]
	v_mfma_f32_16x16x32_bf16 v[110:113], v[134:137], v[174:177], v[110:113]
	v_mfma_f32_16x16x32_bf16 v[106:109], v[142:145], v[174:177], v[106:109]
	v_mfma_f32_16x16x32_bf16 v[92:95], v[134:137], v[182:185], v[92:95]
	v_mfma_f32_16x16x32_bf16 v[88:91], v[142:145], v[182:185], v[88:91]
	v_mfma_f32_16x16x32_bf16 v[76:79], v[134:137], v[190:193], v[76:79]
	v_mfma_f32_16x16x32_bf16 v[72:75], v[142:145], v[190:193], v[72:75]
	v_mfma_f32_16x16x32_bf16 v[118:121], v[146:149], v[162:165], v[118:121]
	v_mfma_f32_16x16x32_bf16 v[114:117], v[154:157], v[162:165], v[114:117]
	v_mfma_f32_16x16x32_bf16 v[102:105], v[146:149], v[170:173], v[102:105]
	v_mfma_f32_16x16x32_bf16 v[98:101], v[154:157], v[170:173], v[98:101]
	v_mfma_f32_16x16x32_bf16 v[84:87], v[146:149], v[178:181], v[84:87]
	v_mfma_f32_16x16x32_bf16 v[80:83], v[154:157], v[178:181], v[80:83]
	v_mfma_f32_16x16x32_bf16 v[68:71], v[146:149], v[186:189], v[68:71]
	v_mfma_f32_16x16x32_bf16 v[64:67], v[154:157], v[186:189], v[64:67]
	v_mfma_f32_16x16x32_bf16 v[118:121], v[150:153], v[166:169], v[118:121]
	v_mfma_f32_16x16x32_bf16 v[114:117], v[158:161], v[166:169], v[114:117]
	v_mfma_f32_16x16x32_bf16 v[102:105], v[150:153], v[174:177], v[102:105]
	v_mfma_f32_16x16x32_bf16 v[98:101], v[158:161], v[174:177], v[98:101]
	v_mfma_f32_16x16x32_bf16 v[84:87], v[150:153], v[182:185], v[84:87]
	v_mfma_f32_16x16x32_bf16 v[80:83], v[158:161], v[182:185], v[80:83]
	v_mfma_f32_16x16x32_bf16 v[68:71], v[150:153], v[190:193], v[68:71]
	v_mfma_f32_16x16x32_bf16 v[64:67], v[158:161], v[190:193], v[64:67]
	s_barrier
; #define PG8_STAGE(bufoff, gbase, voff) do { _Pragma("unroll") for (int _i = 0; _i < 2; ++_i) \
;         __builtin_amdgcn_global_load_lds((const __attribute__((address_space(1))) unsigned*)((const __attribute__((address_space(1))) char*)(gbase) + (unsigned)lnd_v((int)(voff)[_i])), (LAS unsigned*)(lds + (bufoff) + ldsw + _i * 8192), 16, 0, 0); } while (0)
; #define PG8_LDA(dst, b, h) do { _Pragma("unroll") for (int m = 0; m < 4; ++m) _Pragma("unroll") for (int k = 0; k < 2; ++k) dst[m][k] = *(const LAS bf16x8*)(lds + PG8_SA(b, h) + aoff + m * 2048 + k * 1024); } while (0)
; #define PG8_MMA(ai, bj, At, Bt) do { __builtin_amdgcn_s_setprio(1); _Pragma("unroll") for (int m = 0; m < 4; ++m) _Pragma("unroll") for (int n = 0; n < 2; ++n) _Pragma("unroll") for (int k = 0; k < 2; ++k) \
;         acc[ai][bj][m][n] = __builtin_amdgcn_mfma_f32_16x16x32_bf16(Bt[n][k], At[m][k], acc[ai][bj][m][n], 0, 0, 0); __builtin_amdgcn_s_setprio(0); } while (0)
; #define PG8_WAIT_V(n) asm volatile("s_waitcnt vmcnt(" #n ")" ::: "memory")
; #define PG8_WAIT_L(n) asm volatile("s_waitcnt lgkmcnt(" #n ")" ::: "memory")
; #define PG8_BAR __builtin_amdgcn_s_barrier()
; #define PG8_SCHED __builtin_amdgcn_sched_barrier(0)
; template <class Desc, class Epi>
; __device__ __forceinline__ void gemm_phase(const int wv_, LAS unsigned char* lds, const Desc& d, const Epi& E) {
;     ...
;             PG8_LDA(At, 1, 1); PG8_STAGE(PG8_SB(1, 0), b3, voffB); PG8_STAGE(PG8_SB(1, 1), b3 + hstepB, voffB); PG8_STAGE(PG8_SA(1, 0), a3, sA0);
;             PG8_WAIT_V(8); PG8_WAIT_L(0); PG8_BAR; PG8_MMA(1, 0, At, B0); PG8_MMA(1, 1, At, B1); PG8_BAR; PG8_SCHED;
;         }
;         if (wr == 0) PG8_BAR;
	v_mov_b32_e32 v96, v208
	ds_read_b128 v[162:165], v221 offset:49152
	ds_read_b128 v[166:169], v221 offset:50176
	ds_read_b128 v[170:173], v221 offset:51200
	ds_read_b128 v[174:177], v221 offset:52224
	ds_read_b128 v[178:181], v221 offset:53248
	ds_read_b128 v[182:185], v221 offset:54272
	ds_read_b128 v[186:189], v221 offset:55296
	ds_read_b128 v[190:193], v221 offset:56320
	s_add_i32 s62, s62, s52
	v_lshl_add_u64 v[194:195], s[20:21], 0, v[96:97]
	v_lshl_add_u64 v[194:195], v[194:195], 0, s[30:31]
	s_mov_b32 m0, s62
	v_mov_b32_e32 v96, v211
	global_load_lds_dwordx4 v[194:195], off
	s_add_i32 m0, s62, 0x2000
	s_nop 0
	v_lshl_add_u64 v[194:195], s[20:21], 0, v[96:97]
	s_add_u32 s20, s20, 0x40080
	v_lshl_add_u64 v[194:195], v[194:195], 0, s[30:31]
	s_addc_u32 s21, s21, 0
	v_mov_b32_e32 v96, v208
	s_add_i32 s62, s63, s52
	global_load_lds_dwordx4 v[194:195], off
	s_mov_b32 m0, s62
	s_nop 0
	global_load_lds_dwordx4 v96, s[20:21]
	v_mov_b32_e32 v96, v211
	s_add_i32 m0, s62, 0x2000
	s_nop 0
	global_load_lds_dwordx4 v96, s[20:21]
	v_mov_b32_e32 v96, v206
	s_mov_b32 m0, s57
	v_lshl_add_u64 v[194:195], s[4:5], 0, v[96:97]
	v_lshl_add_u64 v[194:195], v[194:195], 0, s[30:31]
	v_mov_b32_e32 v96, v209
	global_load_lds_dwordx4 v[194:195], off
	s_mov_b32 m0, s58
	v_lshl_add_u64 v[194:195], s[4:5], 0, v[96:97]
	v_lshl_add_u64 v[194:195], v[194:195], 0, s[30:31]
	global_load_lds_dwordx4 v[194:195], off
	s_waitcnt vmcnt(8)
	s_waitcnt lgkmcnt(0)
	s_barrier
	v_mfma_f32_16x16x32_bf16 v[60:63], v[130:133], v[162:165], v[60:63]
	v_mfma_f32_16x16x32_bf16 v[56:59], v[138:141], v[162:165], v[56:59]
	v_mfma_f32_16x16x32_bf16 v[44:47], v[130:133], v[170:173], v[44:47]
	v_mfma_f32_16x16x32_bf16 v[40:43], v[138:141], v[170:173], v[40:43]
	v_mfma_f32_16x16x32_bf16 v[24:27], v[130:133], v[178:181], v[24:27]
	v_mfma_f32_16x16x32_bf16 v[16:19], v[138:141], v[178:181], v[16:19]
	v_mfma_f32_16x16x32_bf16 v[4:7], v[130:133], v[186:189], v[4:7]
	v_mfma_f32_16x16x32_bf16 v[0:3], v[138:141], v[186:189], v[0:3]
	v_mfma_f32_16x16x32_bf16 v[60:63], v[134:137], v[166:169], v[60:63]
	v_mfma_f32_16x16x32_bf16 v[56:59], v[142:145], v[166:169], v[56:59]
	v_mfma_f32_16x16x32_bf16 v[44:47], v[134:137], v[174:177], v[44:47]
	v_mfma_f32_16x16x32_bf16 v[40:43], v[142:145], v[174:177], v[40:43]
	v_mfma_f32_16x16x32_bf16 v[24:27], v[134:137], v[182:185], v[24:27]
	v_mfma_f32_16x16x32_bf16 v[16:19], v[142:145], v[182:185], v[16:19]
	v_mfma_f32_16x16x32_bf16 v[4:7], v[134:137], v[190:193], v[4:7]
	v_mfma_f32_16x16x32_bf16 v[0:3], v[142:145], v[190:193], v[0:3]
	v_mfma_f32_16x16x32_bf16 v[52:55], v[146:149], v[162:165], v[52:55]
	v_mfma_f32_16x16x32_bf16 v[48:51], v[154:157], v[162:165], v[48:51]
	v_mfma_f32_16x16x32_bf16 v[28:31], v[146:149], v[170:173], v[28:31]
	v_mfma_f32_16x16x32_bf16 v[20:23], v[154:157], v[170:173], v[20:23]
	v_mfma_f32_16x16x32_bf16 v[36:39], v[146:149], v[178:181], v[36:39]
	v_mfma_f32_16x16x32_bf16 v[32:35], v[154:157], v[178:181], v[32:35]
	v_mfma_f32_16x16x32_bf16 v[12:15], v[146:149], v[186:189], v[12:15]
	v_mfma_f32_16x16x32_bf16 v[8:11], v[154:157], v[186:189], v[8:11]
	v_mfma_f32_16x16x32_bf16 v[52:55], v[150:153], v[166:169], v[52:55]
	v_mfma_f32_16x16x32_bf16 v[48:51], v[158:161], v[166:169], v[48:51]
	v_mfma_f32_16x16x32_bf16 v[28:31], v[150:153], v[174:177], v[28:31]
	v_mfma_f32_16x16x32_bf16 v[20:23], v[158:161], v[174:177], v[20:23]
	v_mfma_f32_16x16x32_bf16 v[36:39], v[150:153], v[182:185], v[36:39]
	v_mfma_f32_16x16x32_bf16 v[32:35], v[158:161], v[182:185], v[32:35]
	v_mfma_f32_16x16x32_bf16 v[12:15], v[150:153], v[190:193], v[12:15]
	v_mfma_f32_16x16x32_bf16 v[8:11], v[158:161], v[190:193], v[8:11]
	s_barrier
	s_add_i32 s61, s61, 2
	s_add_u32 s2, s2, 0x100
	s_addc_u32 s3, s3, 0
	s_add_u32 s29, s29, 0x100
	s_addc_u32 s43, s43, 0
	s_cmp_gt_u32 s61, 13
	s_cbranch_scc0 .LBB0_1262
	s_and_b64 vcc, exec, s[40:41]
	s_cbranch_vccz .LBB0_1265
	s_barrier

; #define PG8_STAGE(bufoff, gbase, voff) do { _Pragma("unroll") for (int _i = 0; _i < 2; ++_i) \
;         __builtin_amdgcn_global_load_lds((const __attribute__((address_space(1))) unsigned*)((const __attribute__((address_space(1))) char*)(gbase) + (unsigned)lnd_v((int)(voff)[_i])), (LAS unsigned*)(lds + (bufoff) + ldsw + _i * 8192), 16, 0, 0); } while (0)
; #define PG8_LDA(dst, b, h) do { _Pragma("unroll") for (int m = 0; m < 4; ++m) _Pragma("unroll") for (int k = 0; k < 2; ++k) dst[m][k] = *(const LAS bf16x8*)(lds + PG8_SA(b, h) + aoff + m * 2048 + k * 1024); } while (0)
; #define PG8_LDB(dst, b, h) do { _Pragma("unroll") for (int n = 0; n < 2; ++n) _Pragma("unroll") for (int k = 0; k < 2; ++k) dst[n][k] = *(const LAS bf16x8*)(lds + PG8_SB(b, h) + boff + n * 2048 + k * 1024); } while (0)
; #define PG8_MMA(ai, bj, At, Bt) do { __builtin_amdgcn_s_setprio(1); _Pragma("unroll") for (int m = 0; m < 4; ++m) _Pragma("unroll") for (int n = 0; n < 2; ++n) _Pragma("unroll") for (int k = 0; k < 2; ++k) \
;         acc[ai][bj][m][n] = __builtin_amdgcn_mfma_f32_16x16x32_bf16(Bt[n][k], At[m][k], acc[ai][bj][m][n], 0, 0, 0); __builtin_amdgcn_s_setprio(0); } while (0)
; template <class Desc, class Epi>
; __device__ __forceinline__ void gemm_phase(const int wv_, LAS unsigned char* lds, const Desc& d, const Epi& E) {
;     ...
;             const bool last = (t == nt - 2);
;             unsigned sA0[2], sA1[2];
;             if constexpr (Desc::GATHER) { sA0[0] = last ? voffAn[0] : voffA[0]; sA0[1] = last ? voffAn[1] : voffA[1]; sA1[0] = last ? voffAn1[0] : voffA1[0]; sA1[1] = last ? voffAn1[1] : voffA1[1]; }
;             else { sA0[0] = voffA[0]; sA0[1] = voffA[1]; sA1[0] = voffA1[0]; sA1[1] = voffA1[1]; }
;             const char* a1 = cA + (size_t)(t + 1) * kstep;
;             const char* a2 = last ? nA : cA + (size_t)(t + 2) * kstep; const char* b2 = last ? nB : cB + (size_t)(t + 2) * kstep;
;             const char* a3 = a2 + kstep; const char* b3 = b2 + kstep;
;             PG8_LDB(B0, 0, 0); PG8_LDB(B1, 0, 1); PG8_SCHED; PG8_LDA(At, 0, 0); PG8_STAGE(PG8_SA(1, 1), a1, voffA1);
;             PG8_WAIT_V(8); PG8_WAIT_L(0); PG8_BAR; PG8_MMA(0, 0, At, B0); PG8_MMA(0, 1, At, B1); PG8_BAR; PG8_SCHED;
;             PG8_LDA(At, 0, 1); PG8_STAGE(PG8_SB(0, 0), b2, voffB); PG8_STAGE(PG8_SB(0, 1), b2 + hstepB, voffB); PG8_STAGE(PG8_SA(0, 0), a2, sA0);
.LBB0_1481:
	s_add_u32 s52, s50, s22
	s_addc_u32 s53, s51, 0
	s_add_u32 s23, s52, 0x100
	s_addc_u32 s24, s53, 0
	s_and_b64 s[4:5], s[20:21], exec
	s_cselect_b32 s4, s42, s23
	s_cselect_b32 s5, s43, s24
	s_add_u32 s22, s48, s22
	s_addc_u32 s23, s49, 0
	s_add_u32 s22, s22, 0x100
	s_addc_u32 s23, s23, 0
	s_add_i32 s77, 0, 0x10000
	s_and_b64 s[20:21], s[20:21], exec
	s_cselect_b32 s21, s45, s23
	s_cselect_b32 s20, s44, s22
	s_add_i32 s23, 0, 0x14000
	v_add_u32_e32 v96, s77, v139
	s_add_i32 s79, s77, s59
	ds_read_b128 v[150:153], v96
	ds_read_b128 v[154:157], v96 offset:1024
	ds_read_b128 v[158:161], v96 offset:2048
	ds_read_b128 v[162:165], v96 offset:3072
	v_add_u32_e32 v96, s23, v139
	s_add_i32 m0, s60, 0xc000
	s_add_i32 s80, s60, 0xe000
	s_add_i32 s75, s79, 0x2000
	ds_read_b128 v[166:169], v96
	ds_read_b128 v[170:173], v96 offset:1024
	ds_read_b128 v[174:177], v96 offset:2048
	ds_read_b128 v[178:181], v96 offset:3072
	s_add_u32 s24, s20, 0x40000
	s_addc_u32 s25, s21, 0
	s_add_i32 s73, 0, 0x18000
	s_add_i32 s76, s23, s59
	s_add_i32 s71, s73, s59
	s_add_i32 s74, s76, 0x2000
	s_add_i32 s72, 0, 0x1c000
	s_add_i32 s29, s71, 0x2000
	s_add_u32 s22, s20, 0x40080
	s_addc_u32 s23, s21, 0
	s_add_i32 s78, s72, s59
	s_add_i32 s77, s78, 0x2000
	v_mov_b32_e32 v96, v133
	ds_read_b128 v[182:185], v149
	ds_read_b128 v[186:189], v149 offset:1024
	ds_read_b128 v[190:193], v149 offset:2048
	ds_read_b128 v[194:197], v149 offset:3072
	ds_read_b128 v[198:201], v149 offset:4096
	ds_read_b128 v[202:205], v149 offset:5120
	ds_read_b128 v[206:209], v149 offset:6144
	ds_read_b128 v[210:213], v149 offset:7168
	s_nop 0
	v_lshl_add_u64 v[130:131], s[52:53], 0, v[96:97]
	v_lshl_add_u64 v[130:131], v[130:131], 0, s[30:31]
	v_mov_b32_e32 v96, v136
	global_load_lds_dwordx4 v[130:131], off
	s_mov_b32 m0, s80
	v_lshl_add_u64 v[130:131], s[52:53], 0, v[96:97]
	v_lshl_add_u64 v[130:131], v[130:131], 0, s[30:31]
	global_load_lds_dwordx4 v[130:131], off
	s_waitcnt vmcnt(8)
	s_waitcnt lgkmcnt(0)
	s_barrier
	v_mfma_f32_16x16x32_bf16 v[126:129], v[150:153], v[182:185], v[126:129]
	v_mfma_f32_16x16x32_bf16 v[122:125], v[158:161], v[182:185], v[122:125]
	v_mfma_f32_16x16x32_bf16 v[110:113], v[150:153], v[190:193], v[110:113]
	v_mfma_f32_16x16x32_bf16 v[106:109], v[158:161], v[190:193], v[106:109]
	v_mfma_f32_16x16x32_bf16 v[92:95], v[150:153], v[198:201], v[92:95]
	v_mfma_f32_16x16x32_bf16 v[88:91], v[158:161], v[198:201], v[88:91]
	v_mfma_f32_16x16x32_bf16 v[76:79], v[150:153], v[206:209], v[76:79]
	v_mfma_f32_16x16x32_bf16 v[72:75], v[158:161], v[206:209], v[72:75]
	v_mfma_f32_16x16x32_bf16 v[126:129], v[154:157], v[186:189], v[126:129]
	v_mfma_f32_16x16x32_bf16 v[122:125], v[162:165], v[186:189], v[122:125]
	v_mfma_f32_16x16x32_bf16 v[110:113], v[154:157], v[194:197], v[110:113]
	v_mfma_f32_16x16x32_bf16 v[106:109], v[162:165], v[194:197], v[106:109]
	v_mfma_f32_16x16x32_bf16 v[92:95], v[154:157], v[202:205], v[92:95]
	v_mfma_f32_16x16x32_bf16 v[88:91], v[162:165], v[202:205], v[88:91]
	v_mfma_f32_16x16x32_bf16 v[76:79], v[154:157], v[210:213], v[76:79]
	v_mfma_f32_16x16x32_bf16 v[72:75], v[162:165], v[210:213], v[72:75]
	v_mfma_f32_16x16x32_bf16 v[118:121], v[166:169], v[182:185], v[118:121]
	v_mfma_f32_16x16x32_bf16 v[114:117], v[174:177], v[182:185], v[114:117]
	v_mfma_f32_16x16x32_bf16 v[102:105], v[166:169], v[190:193], v[102:105]
	v_mfma_f32_16x16x32_bf16 v[98:101], v[174:177], v[190:193], v[98:101]
	v_mfma_f32_16x16x32_bf16 v[84:87], v[166:169], v[198:201], v[84:87]
	v_mfma_f32_16x16x32_bf16 v[80:83], v[174:177], v[198:201], v[80:83]
	v_mfma_f32_16x16x32_bf16 v[68:71], v[166:169], v[206:209], v[68:71]
	v_mfma_f32_16x16x32_bf16 v[64:67], v[174:177], v[206:209], v[64:67]
	v_mfma_f32_16x16x32_bf16 v[118:121], v[170:173], v[186:189], v[118:121]
	v_mfma_f32_16x16x32_bf16 v[114:117], v[178:181], v[186:189], v[114:117]
	v_mfma_f32_16x16x32_bf16 v[102:105], v[170:173], v[194:197], v[102:105]
	v_mfma_f32_16x16x32_bf16 v[98:101], v[178:181], v[194:197], v[98:101]
	v_mfma_f32_16x16x32_bf16 v[84:87], v[170:173], v[202:205], v[84:87]
	v_mfma_f32_16x16x32_bf16 v[80:83], v[178:181], v[202:205], v[80:83]
	v_mfma_f32_16x16x32_bf16 v[68:71], v[170:173], v[210:213], v[68:71]
	v_mfma_f32_16x16x32_bf16 v[64:67], v[178:181], v[210:213], v[64:67]
	s_barrier
	v_mov_b32_e32 v96, v134
	s_mov_b32 m0, s79
	ds_read_b128 v[182:185], v149 offset:16384
	ds_read_b128 v[186:189], v149 offset:17408
	ds_read_b128 v[190:193], v149 offset:18432
	ds_read_b128 v[194:197], v149 offset:19456
	ds_read_b128 v[198:201], v149 offset:20480
	ds_read_b128 v[202:205], v149 offset:21504
	ds_read_b128 v[206:209], v149 offset:22528
	ds_read_b128 v[210:213], v149 offset:23552
	s_nop 0
	global_load_lds_dwordx4 v96, s[20:21]
	v_mov_b32_e32 v96, v137
	s_mov_b32 m0, s75
	s_nop 0
	global_load_lds_dwordx4 v96, s[20:21]
	v_mov_b32_e32 v96, v134
	s_mov_b32 m0, s76
	s_nop 0
	global_load_lds_dwordx4 v96, s[24:25]
	v_mov_b32_e32 v96, v137
	s_mov_b32 m0, s74
	s_nop 0
	global_load_lds_dwordx4 v96, s[24:25]
	v_mov_b32_e32 v96, v132
	s_mov_b32 m0, s60
	s_nop 0
	global_load_lds_dwordx4 v96, s[4:5]
	v_mov_b32_e32 v96, v135
	s_mov_b32 m0, s61
	s_nop 0
	global_load_lds_dwordx4 v96, s[4:5]
	s_waitcnt vmcnt(8)
	s_waitcnt lgkmcnt(0)
	s_barrier
; #define PG8_STAGE(bufoff, gbase, voff) do { _Pragma("unroll") for (int _i = 0; _i < 2; ++_i) \
;         __builtin_amdgcn_global_load_lds((const __attribute__((address_space(1))) unsigned*)((const __attribute__((address_space(1))) char*)(gbase) + (unsigned)lnd_v((int)(voff)[_i])), (LAS unsigned*)(lds + (bufoff) + ldsw + _i * 8192), 16, 0, 0); } while (0)
; #define PG8_LDA(dst, b, h) do { _Pragma("unroll") for (int m = 0; m < 4; ++m) _Pragma("unroll") for (int k = 0; k < 2; ++k) dst[m][k] = *(const LAS bf16x8*)(lds + PG8_SA(b, h) + aoff + m * 2048 + k * 1024); } while (0)
; #define PG8_LDB(dst, b, h) do { _Pragma("unroll") for (int n = 0; n < 2; ++n) _Pragma("unroll") for (int k = 0; k < 2; ++k) dst[n][k] = *(const LAS bf16x8*)(lds + PG8_SB(b, h) + boff + n * 2048 + k * 1024); } while (0)
; #define PG8_MMA(ai, bj, At, Bt) do { __builtin_amdgcn_s_setprio(1); _Pragma("unroll") for (int m = 0; m < 4; ++m) _Pragma("unroll") for (int n = 0; n < 2; ++n) _Pragma("unroll") for (int k = 0; k < 2; ++k) \
;         acc[ai][bj][m][n] = __builtin_amdgcn_mfma_f32_16x16x32_bf16(Bt[n][k], At[m][k], acc[ai][bj][m][n], 0, 0, 0); __builtin_amdgcn_s_setprio(0); } while (0)
; #define PG8_WAIT_V(n) asm volatile("s_waitcnt vmcnt(" #n ")" ::: "memory")
; #define PG8_WAIT_L(n) asm volatile("s_waitcnt lgkmcnt(" #n ")" ::: "memory")
; #define PG8_BAR __builtin_amdgcn_s_barrier()
; #define PG8_SCHED __builtin_amdgcn_sched_barrier(0)
; template <class Desc, class Epi>
; __device__ __forceinline__ void gemm_phase(const int wv_, LAS unsigned char* lds, const Desc& d, const Epi& E) {
;     ...
;             PG8_WAIT_V(8); PG8_WAIT_L(0); PG8_BAR; PG8_MMA(1, 0, At, B0); PG8_MMA(1, 1, At, B1); PG8_BAR; PG8_SCHED;
;             PG8_LDB(B0, 1, 0); PG8_LDB(B1, 1, 1); PG8_SCHED; PG8_LDA(At, 1, 0); PG8_STAGE(PG8_SA(0, 1), a2, sA1);
;             PG8_WAIT_V(8); PG8_WAIT_L(0); PG8_BAR; PG8_MMA(0, 0, At, B0); PG8_MMA(0, 1, At, B1); PG8_BAR; PG8_SCHED;
	v_mfma_f32_16x16x32_bf16 v[60:63], v[150:153], v[182:185], v[60:63]
	v_mfma_f32_16x16x32_bf16 v[56:59], v[158:161], v[182:185], v[56:59]
	v_mfma_f32_16x16x32_bf16 v[44:47], v[150:153], v[190:193], v[44:47]
	v_mfma_f32_16x16x32_bf16 v[32:35], v[158:161], v[190:193], v[32:35]
	v_mfma_f32_16x16x32_bf16 v[16:19], v[150:153], v[198:201], v[16:19]
	v_mfma_f32_16x16x32_bf16 v[8:11], v[158:161], v[198:201], v[8:11]
	v_mfma_f32_16x16x32_bf16 v[4:7], v[150:153], v[206:209], v[4:7]
	v_mfma_f32_16x16x32_bf16 v[0:3], v[158:161], v[206:209], v[0:3]
	v_mfma_f32_16x16x32_bf16 v[60:63], v[154:157], v[186:189], v[60:63]
	v_mfma_f32_16x16x32_bf16 v[56:59], v[162:165], v[186:189], v[56:59]
	v_mfma_f32_16x16x32_bf16 v[44:47], v[154:157], v[194:197], v[44:47]
	v_mfma_f32_16x16x32_bf16 v[32:35], v[162:165], v[194:197], v[32:35]
	v_mfma_f32_16x16x32_bf16 v[16:19], v[154:157], v[202:205], v[16:19]
	v_mfma_f32_16x16x32_bf16 v[8:11], v[162:165], v[202:205], v[8:11]
	v_mfma_f32_16x16x32_bf16 v[4:7], v[154:157], v[210:213], v[4:7]
	v_mfma_f32_16x16x32_bf16 v[0:3], v[162:165], v[210:213], v[0:3]
	v_mfma_f32_16x16x32_bf16 v[52:55], v[166:169], v[182:185], v[52:55]
	v_mfma_f32_16x16x32_bf16 v[48:51], v[174:177], v[182:185], v[48:51]
	v_mfma_f32_16x16x32_bf16 v[28:31], v[166:169], v[190:193], v[28:31]
	v_mfma_f32_16x16x32_bf16 v[12:15], v[174:177], v[190:193], v[12:15]
	v_mfma_f32_16x16x32_bf16 v[36:39], v[166:169], v[198:201], v[36:39]
	v_mfma_f32_16x16x32_bf16 v[40:43], v[174:177], v[198:201], v[40:43]
	v_mfma_f32_16x16x32_bf16 v[20:23], v[166:169], v[206:209], v[20:23]
	v_mfma_f32_16x16x32_bf16 v[24:27], v[174:177], v[206:209], v[24:27]
	v_mfma_f32_16x16x32_bf16 v[52:55], v[170:173], v[186:189], v[52:55]
	v_mfma_f32_16x16x32_bf16 v[48:51], v[178:181], v[186:189], v[48:51]
	v_mfma_f32_16x16x32_bf16 v[28:31], v[170:173], v[194:197], v[28:31]
	v_mfma_f32_16x16x32_bf16 v[12:15], v[178:181], v[194:197], v[12:15]
	v_mfma_f32_16x16x32_bf16 v[36:39], v[170:173], v[202:205], v[36:39]
	v_mfma_f32_16x16x32_bf16 v[40:43], v[178:181], v[202:205], v[40:43]
	v_mfma_f32_16x16x32_bf16 v[20:23], v[170:173], v[210:213], v[20:23]
	v_mfma_f32_16x16x32_bf16 v[24:27], v[178:181], v[210:213], v[24:27]
	s_barrier
	v_add_u32_e32 v96, s73, v139
	ds_read_b128 v[150:153], v96
	ds_read_b128 v[154:157], v96 offset:1024
	ds_read_b128 v[158:161], v96 offset:2048
	ds_read_b128 v[162:165], v96 offset:3072
	v_add_u32_e32 v96, s72, v139
	ds_read_b128 v[166:169], v96
	ds_read_b128 v[170:173], v96 offset:1024
	ds_read_b128 v[174:177], v96 offset:2048
	ds_read_b128 v[178:181], v96 offset:3072
	v_mov_b32_e32 v96, v133
	s_mov_b32 m0, s62
	ds_read_b128 v[182:185], v149 offset:32768
	ds_read_b128 v[186:189], v149 offset:33792
	ds_read_b128 v[190:193], v149 offset:34816
	ds_read_b128 v[194:197], v149 offset:35840
	ds_read_b128 v[198:201], v149 offset:36864
	ds_read_b128 v[202:205], v149 offset:37888
	ds_read_b128 v[206:209], v149 offset:38912
	ds_read_b128 v[210:213], v149 offset:39936
	s_nop 0
	global_load_lds_dwordx4 v96, s[4:5]
	v_mov_b32_e32 v96, v136
	s_mov_b32 m0, s63
	s_nop 0
	global_load_lds_dwordx4 v96, s[4:5]
	s_waitcnt vmcnt(8)
	s_waitcnt lgkmcnt(0)
	s_barrier
	v_mfma_f32_16x16x32_bf16 v[126:129], v[150:153], v[182:185], v[126:129]
	v_mfma_f32_16x16x32_bf16 v[122:125], v[158:161], v[182:185], v[122:125]
	v_mfma_f32_16x16x32_bf16 v[110:113], v[150:153], v[190:193], v[110:113]
	v_mfma_f32_16x16x32_bf16 v[106:109], v[158:161], v[190:193], v[106:109]
	v_mfma_f32_16x16x32_bf16 v[92:95], v[150:153], v[198:201], v[92:95]
	v_mfma_f32_16x16x32_bf16 v[88:91], v[158:161], v[198:201], v[88:91]
	v_mfma_f32_16x16x32_bf16 v[76:79], v[150:153], v[206:209], v[76:79]
	v_mfma_f32_16x16x32_bf16 v[72:75], v[158:161], v[206:209], v[72:75]
	v_mfma_f32_16x16x32_bf16 v[126:129], v[154:157], v[186:189], v[126:129]
	v_mfma_f32_16x16x32_bf16 v[122:125], v[162:165], v[186:189], v[122:125]
	v_mfma_f32_16x16x32_bf16 v[110:113], v[154:157], v[194:197], v[110:113]
	v_mfma_f32_16x16x32_bf16 v[106:109], v[162:165], v[194:197], v[106:109]
	v_mfma_f32_16x16x32_bf16 v[92:95], v[154:157], v[202:205], v[92:95]
	v_mfma_f32_16x16x32_bf16 v[88:91], v[162:165], v[202:205], v[88:91]
	v_mfma_f32_16x16x32_bf16 v[76:79], v[154:157], v[210:213], v[76:79]
	v_mfma_f32_16x16x32_bf16 v[72:75], v[162:165], v[210:213], v[72:75]
	v_mfma_f32_16x16x32_bf16 v[118:121], v[166:169], v[182:185], v[118:121]
	v_mfma_f32_16x16x32_bf16 v[114:117], v[174:177], v[182:185], v[114:117]
	v_mfma_f32_16x16x32_bf16 v[102:105], v[166:169], v[190:193], v[102:105]
	v_mfma_f32_16x16x32_bf16 v[98:101], v[174:177], v[190:193], v[98:101]
	v_mfma_f32_16x16x32_bf16 v[84:87], v[166:169], v[198:201], v[84:87]
	v_mfma_f32_16x16x32_bf16 v[80:83], v[174:177], v[198:201], v[80:83]
	v_mfma_f32_16x16x32_bf16 v[68:71], v[166:169], v[206:209], v[68:71]
	v_mfma_f32_16x16x32_bf16 v[64:67], v[174:177], v[206:209], v[64:67]
	v_mfma_f32_16x16x32_bf16 v[118:121], v[170:173], v[186:189], v[118:121]
	v_mfma_f32_16x16x32_bf16 v[114:117], v[178:181], v[186:189], v[114:117]
	v_mfma_f32_16x16x32_bf16 v[102:105], v[170:173], v[194:197], v[102:105]
	v_mfma_f32_16x16x32_bf16 v[98:101], v[178:181], v[194:197], v[98:101]
	v_mfma_f32_16x16x32_bf16 v[84:87], v[170:173], v[202:205], v[84:87]
	v_mfma_f32_16x16x32_bf16 v[80:83], v[178:181], v[202:205], v[80:83]
	v_mfma_f32_16x16x32_bf16 v[68:71], v[170:173], v[210:213], v[68:71]
	v_mfma_f32_16x16x32_bf16 v[64:67], v[178:181], v[210:213], v[64:67]
	s_barrier
; #define PG8_STAGE(bufoff, gbase, voff) do { _Pragma("unroll") for (int _i = 0; _i < 2; ++_i) \
;         __builtin_amdgcn_global_load_lds((const __attribute__((address_space(1))) unsigned*)((const __attribute__((address_space(1))) char*)(gbase) + (unsigned)lnd_v((int)(voff)[_i])), (LAS unsigned*)(lds + (bufoff) + ldsw + _i * 8192), 16, 0, 0); } while (0)
; #define PG8_LDA(dst, b, h) do { _Pragma("unroll") for (int m = 0; m < 4; ++m) _Pragma("unroll") for (int k = 0; k < 2; ++k) dst[m][k] = *(const LAS bf16x8*)(lds + PG8_SA(b, h) + aoff + m * 2048 + k * 1024); } while (0)
; #define PG8_MMA(ai, bj, At, Bt) do { __builtin_amdgcn_s_setprio(1); _Pragma("unroll") for (int m = 0; m < 4; ++m) _Pragma("unroll") for (int n = 0; n < 2; ++n) _Pragma("unroll") for (int k = 0; k < 2; ++k) \
;         acc[ai][bj][m][n] = __builtin_amdgcn_mfma_f32_16x16x32_bf16(Bt[n][k], At[m][k], acc[ai][bj][m][n], 0, 0, 0); __builtin_amdgcn_s_setprio(0); } while (0)
; #define PG8_WAIT_V(n) asm volatile("s_waitcnt vmcnt(" #n ")" ::: "memory")
; #define PG8_WAIT_L(n) asm volatile("s_waitcnt lgkmcnt(" #n ")" ::: "memory")
; #define PG8_BAR __builtin_amdgcn_s_barrier()
; #define PG8_SCHED __builtin_amdgcn_sched_barrier(0)
; template <class Desc, class Epi>
; __device__ __forceinline__ void gemm_phase(const int wv_, LAS unsigned char* lds, const Desc& d, const Epi& E) {
;     ...
;             PG8_LDA(At, 1, 1); PG8_STAGE(PG8_SB(1, 0), b3, voffB); PG8_STAGE(PG8_SB(1, 1), b3 + hstepB, voffB); PG8_STAGE(PG8_SA(1, 0), a3, sA0);
;             PG8_WAIT_V(8); PG8_WAIT_L(0); PG8_BAR; PG8_MMA(1, 0, At, B0); PG8_MMA(1, 1, At, B1); PG8_BAR; PG8_SCHED;
;         }
;         if (wr == 0) PG8_BAR;
	v_mov_b32_e32 v96, v134
	ds_read_b128 v[182:185], v149 offset:49152
	ds_read_b128 v[186:189], v149 offset:50176
	ds_read_b128 v[190:193], v149 offset:51200
	ds_read_b128 v[194:197], v149 offset:52224
	ds_read_b128 v[198:201], v149 offset:53248
	ds_read_b128 v[202:205], v149 offset:54272
	ds_read_b128 v[206:209], v149 offset:55296
	ds_read_b128 v[210:213], v149 offset:56320
	s_mov_b32 m0, s71
	v_lshl_add_u64 v[130:131], s[20:21], 0, v[96:97]
	v_lshl_add_u64 v[130:131], v[130:131], 0, s[30:31]
	v_mov_b32_e32 v96, v137
	global_load_lds_dwordx4 v[130:131], off
	s_mov_b32 m0, s29
	v_lshl_add_u64 v[130:131], s[20:21], 0, v[96:97]
	v_lshl_add_u64 v[130:131], v[130:131], 0, s[30:31]
	v_mov_b32_e32 v96, v134
	global_load_lds_dwordx4 v[130:131], off
	s_mov_b32 m0, s78
	s_nop 0
	global_load_lds_dwordx4 v96, s[22:23]
	v_mov_b32_e32 v96, v137
	s_mov_b32 m0, s77
	s_nop 0
	global_load_lds_dwordx4 v96, s[22:23]
	v_mov_b32_e32 v96, v132
	s_mov_b32 m0, s65
	v_lshl_add_u64 v[130:131], s[4:5], 0, v[96:97]
	v_lshl_add_u64 v[130:131], v[130:131], 0, s[30:31]
	v_mov_b32_e32 v96, v135
	global_load_lds_dwordx4 v[130:131], off
	s_mov_b32 m0, s66
	v_lshl_add_u64 v[130:131], s[4:5], 0, v[96:97]
	v_lshl_add_u64 v[130:131], v[130:131], 0, s[30:31]
	global_load_lds_dwordx4 v[130:131], off
	s_waitcnt vmcnt(8)
	s_waitcnt lgkmcnt(0)
	s_barrier
	v_mfma_f32_16x16x32_bf16 v[60:63], v[150:153], v[182:185], v[60:63]
	v_mfma_f32_16x16x32_bf16 v[56:59], v[158:161], v[182:185], v[56:59]
	v_mfma_f32_16x16x32_bf16 v[44:47], v[150:153], v[190:193], v[44:47]
	v_mfma_f32_16x16x32_bf16 v[32:35], v[158:161], v[190:193], v[32:35]
	v_mfma_f32_16x16x32_bf16 v[16:19], v[150:153], v[198:201], v[16:19]
	v_mfma_f32_16x16x32_bf16 v[8:11], v[158:161], v[198:201], v[8:11]
	v_mfma_f32_16x16x32_bf16 v[4:7], v[150:153], v[206:209], v[4:7]
	v_mfma_f32_16x16x32_bf16 v[0:3], v[158:161], v[206:209], v[0:3]
	v_mfma_f32_16x16x32_bf16 v[60:63], v[154:157], v[186:189], v[60:63]
	v_mfma_f32_16x16x32_bf16 v[56:59], v[162:165], v[186:189], v[56:59]
	v_mfma_f32_16x16x32_bf16 v[44:47], v[154:157], v[194:197], v[44:47]
	v_mfma_f32_16x16x32_bf16 v[32:35], v[162:165], v[194:197], v[32:35]
	v_mfma_f32_16x16x32_bf16 v[16:19], v[154:157], v[202:205], v[16:19]
	v_mfma_f32_16x16x32_bf16 v[8:11], v[162:165], v[202:205], v[8:11]
	v_mfma_f32_16x16x32_bf16 v[4:7], v[154:157], v[210:213], v[4:7]
	v_mfma_f32_16x16x32_bf16 v[0:3], v[162:165], v[210:213], v[0:3]
	v_mfma_f32_16x16x32_bf16 v[52:55], v[166:169], v[182:185], v[52:55]
	v_mfma_f32_16x16x32_bf16 v[48:51], v[174:177], v[182:185], v[48:51]
	v_mfma_f32_16x16x32_bf16 v[28:31], v[166:169], v[190:193], v[28:31]
	v_mfma_f32_16x16x32_bf16 v[12:15], v[174:177], v[190:193], v[12:15]
	v_mfma_f32_16x16x32_bf16 v[36:39], v[166:169], v[198:201], v[36:39]
	v_mfma_f32_16x16x32_bf16 v[40:43], v[174:177], v[198:201], v[40:43]
	v_mfma_f32_16x16x32_bf16 v[20:23], v[166:169], v[206:209], v[20:23]
	v_mfma_f32_16x16x32_bf16 v[24:27], v[174:177], v[206:209], v[24:27]
	v_mfma_f32_16x16x32_bf16 v[52:55], v[170:173], v[186:189], v[52:55]
	v_mfma_f32_16x16x32_bf16 v[48:51], v[178:181], v[186:189], v[48:51]
	v_mfma_f32_16x16x32_bf16 v[28:31], v[170:173], v[194:197], v[28:31]
	v_mfma_f32_16x16x32_bf16 v[12:15], v[178:181], v[194:197], v[12:15]
	v_mfma_f32_16x16x32_bf16 v[36:39], v[170:173], v[202:205], v[36:39]
	v_mfma_f32_16x16x32_bf16 v[40:43], v[178:181], v[202:205], v[40:43]
	v_mfma_f32_16x16x32_bf16 v[20:23], v[170:173], v[210:213], v[20:23]
	v_mfma_f32_16x16x32_bf16 v[24:27], v[178:181], v[210:213], v[24:27]
	s_barrier
	s_movk_i32 s22, 0x100
	s_andn2_b64 vcc, exec, s[2:3]
	s_mov_b64 s[20:21], -1
	s_mov_b64 s[2:3], 0
	s_cbranch_vccz .LBB0_1481
	s_and_b64 vcc, exec, s[40:41]
	s_cbranch_vccz .LBB0_1484
	s_barrier

; #define PG8_AOFF(ord, U, O0, O1) do { _Pragma("unroll") for (int _i = 0; _i < 2; ++_i) { \
;         O0[_i] = d.rowbyte(U, (int)tix[(ord) * 256 + Rr[_i]]) + (unsigned)(Cc[_i] * 2); O1[_i] = d.rowbyte(U, (int)tix[(ord) * 256 + HALF + Rr[_i]]) + (unsigned)(Cc[_i] * 2); } } while (0)
; #define PG8_STAGE(bufoff, gbase, voff) do { _Pragma("unroll") for (int _i = 0; _i < 2; ++_i) \
;         __builtin_amdgcn_global_load_lds((const __attribute__((address_space(1))) unsigned*)((const __attribute__((address_space(1))) char*)(gbase) + (unsigned)lnd_v((int)(voff)[_i])), (LAS unsigned*)(lds + (bufoff) + ldsw + _i * 8192), 16, 0, 0); } while (0)
; #define PG8_WAIT_V(n) asm volatile("s_waitcnt vmcnt(" #n ")" ::: "memory")
; #define PG8_WAIT_L(n) asm volatile("s_waitcnt lgkmcnt(" #n ")" ::: "memory")
; #define PG8_BAR __builtin_amdgcn_s_barrier()
; template <class Desc, class Epi>
; __device__ __forceinline__ void gemm_phase(const int wv_, LAS unsigned char* lds, const Desc& d, const Epi& E) {
;     ...
;         if constexpr (Desc::GATHER) { if (has_next) PG8_AOFF(ui + 1, nxt, voffAn, voffAn1); else { voffAn[0] = voffA[0]; voffAn[1] = voffA[1]; voffAn1[0] = voffA1[0]; voffAn1[1] = voffA1[1]; } }
;         const char* nA = has_next ? (const char*)nxt.a : cA; const char* nB = has_next ? (const char*)nxt.b : cB;
;         for (int t = 0; t < nt; t += 2) {
;             const bool last = (t == nt - 2);
;             unsigned sA0[2], sA1[2];
;             if constexpr (Desc::GATHER) { sA0[0] = last ? voffAn[0] : voffA[0]; sA0[1] = last ? voffAn[1] : voffA[1]; sA1[0] = last ? voffAn1[0] : voffA1[0]; sA1[1] = last ? voffAn1[1] : voffA1[1]; }
;             else { sA0[0] = voffA[0]; sA0[1] = voffA[1]; sA1[0] = voffA1[0]; sA1[1] = voffA1[1]; }
;             const char* a1 = cA + (size_t)(t + 1) * kstep;
;             const char* a2 = last ? nA : cA + (size_t)(t + 2) * kstep; const char* b2 = last ? nB : cB + (size_t)(t + 2) * kstep;
;             const char* a3 = a2 + kstep; const char* b3 = b2 + kstep;
;             PG8_LDB(B0, 0, 0); PG8_LDB(B1, 0, 1); PG8_SCHED; PG8_LDA(At, 0, 0); PG8_STAGE(PG8_SA(1, 1), a1, voffA1);
;             PG8_WAIT_V(8); PG8_WAIT_L(0); PG8_BAR; PG8_MMA(0, 0, At, B0); PG8_MMA(0, 1, At, B1); PG8_BAR; PG8_SCHED;
;             PG8_LDA(At, 0, 1); PG8_STAGE(PG8_SB(0, 0), b2, voffB); PG8_STAGE(PG8_SB(0, 1), b2 + hstepB, voffB); PG8_STAGE(PG8_SA(0, 0), a2, sA0);
.LBB0_1565:
	s_add_u32 s4, s2, 0x100
	s_addc_u32 s5, s3, 0
	s_add_u32 s22, s29, s2
	s_addc_u32 s23, s59, s3
	s_cmp_eq_u32 s75, 12
	s_cselect_b64 vcc, -1, 0
	s_and_b64 s[20:21], vcc, exec
	s_cselect_b32 s20, 0, s4
	s_cselect_b32 s21, 0, s5
	s_cselect_b32 s22, s54, s22
	s_cselect_b32 s23, s55, s23
	s_add_u32 s20, s42, s20
	s_addc_u32 s21, s43, s21
	s_add_i32 s76, 0, 0x10000
	v_add_u32_e32 v135, s76, v143
	s_add_i32 s77, 0, 0x14000
	ds_read_b128 v[160:163], v135
	ds_read_b128 v[164:167], v135 offset:1024
	ds_read_b128 v[168:171], v135 offset:2048
	ds_read_b128 v[172:175], v135 offset:3072
	v_add_u32_e32 v135, s77, v143
	ds_read_b128 v[176:179], v135
	ds_read_b128 v[180:183], v135 offset:1024
	ds_read_b128 v[184:187], v135 offset:2048
	ds_read_b128 v[188:191], v135 offset:3072
	v_cndmask_b32_e32 v134, v157, v153, vcc
	v_cndmask_b32_e32 v132, v159, v154, vcc
	v_cndmask_b32_e32 v96, v131, v155, vcc
	v_cndmask_b32_e32 v133, v158, v156, vcc
	s_add_i32 m0, s64, 0xc000
	v_mov_b32_e32 v135, v131
	s_add_u32 s2, s40, s2
	ds_read_b128 v[192:195], v152
	ds_read_b128 v[196:199], v152 offset:1024
	ds_read_b128 v[200:203], v152 offset:2048
	ds_read_b128 v[204:207], v152 offset:3072
	ds_read_b128 v[208:211], v152 offset:4096
	ds_read_b128 v[212:215], v152 offset:5120
	ds_read_b128 v[220:223], v152 offset:6144
	ds_read_b128 v[224:227], v152 offset:7168
	s_addc_u32 s3, s41, s3
	global_load_lds_dwordx4 v135, s[2:3]
	v_mov_b32_e32 v135, v158
	s_add_i32 m0, s64, 0xe000
	s_nop 0
	global_load_lds_dwordx4 v135, s[2:3]
	s_waitcnt vmcnt(8)
	s_waitcnt lgkmcnt(0)
	s_barrier
	v_mfma_f32_16x16x32_bf16 v[122:125], v[160:163], v[192:195], v[122:125]
	v_mfma_f32_16x16x32_bf16 v[114:117], v[168:171], v[192:195], v[114:117]
	v_mfma_f32_16x16x32_bf16 v[106:109], v[160:163], v[200:203], v[106:109]
	v_mfma_f32_16x16x32_bf16 v[98:101], v[168:171], v[200:203], v[98:101]
	v_mfma_f32_16x16x32_bf16 v[88:91], v[160:163], v[208:211], v[88:91]
	v_mfma_f32_16x16x32_bf16 v[80:83], v[168:171], v[208:211], v[80:83]
	v_mfma_f32_16x16x32_bf16 v[72:75], v[160:163], v[220:223], v[72:75]
	v_mfma_f32_16x16x32_bf16 v[64:67], v[168:171], v[220:223], v[64:67]
	v_mfma_f32_16x16x32_bf16 v[122:125], v[164:167], v[196:199], v[122:125]
	v_mfma_f32_16x16x32_bf16 v[114:117], v[172:175], v[196:199], v[114:117]
	v_mfma_f32_16x16x32_bf16 v[106:109], v[164:167], v[204:207], v[106:109]
	v_mfma_f32_16x16x32_bf16 v[98:101], v[172:175], v[204:207], v[98:101]
	v_mfma_f32_16x16x32_bf16 v[88:91], v[164:167], v[212:215], v[88:91]
	v_mfma_f32_16x16x32_bf16 v[80:83], v[172:175], v[212:215], v[80:83]
	v_mfma_f32_16x16x32_bf16 v[72:75], v[164:167], v[224:227], v[72:75]
	v_mfma_f32_16x16x32_bf16 v[64:67], v[172:175], v[224:227], v[64:67]
	v_mfma_f32_16x16x32_bf16 v[126:129], v[176:179], v[192:195], v[126:129]
	v_mfma_f32_16x16x32_bf16 v[118:121], v[184:187], v[192:195], v[118:121]
	v_mfma_f32_16x16x32_bf16 v[110:113], v[176:179], v[200:203], v[110:113]
	v_mfma_f32_16x16x32_bf16 v[102:105], v[184:187], v[200:203], v[102:105]
	v_mfma_f32_16x16x32_bf16 v[92:95], v[176:179], v[208:211], v[92:95]
	v_mfma_f32_16x16x32_bf16 v[84:87], v[184:187], v[208:211], v[84:87]
	v_mfma_f32_16x16x32_bf16 v[76:79], v[176:179], v[220:223], v[76:79]
	v_mfma_f32_16x16x32_bf16 v[68:71], v[184:187], v[220:223], v[68:71]
	v_mfma_f32_16x16x32_bf16 v[126:129], v[180:183], v[196:199], v[126:129]
	v_mfma_f32_16x16x32_bf16 v[118:121], v[188:191], v[196:199], v[118:121]
	v_mfma_f32_16x16x32_bf16 v[110:113], v[180:183], v[204:207], v[110:113]
	v_mfma_f32_16x16x32_bf16 v[102:105], v[188:191], v[204:207], v[102:105]
	v_mfma_f32_16x16x32_bf16 v[92:95], v[180:183], v[212:215], v[92:95]
	v_mfma_f32_16x16x32_bf16 v[84:87], v[188:191], v[212:215], v[84:87]
	v_mfma_f32_16x16x32_bf16 v[76:79], v[180:183], v[224:227], v[76:79]
	v_mfma_f32_16x16x32_bf16 v[68:71], v[188:191], v[224:227], v[68:71]
	s_barrier
	v_mov_b32_e32 v135, v138
	s_add_i32 s2, s76, s63
	ds_read_b128 v[192:195], v152 offset:16384
	ds_read_b128 v[196:199], v152 offset:17408
	ds_read_b128 v[200:203], v152 offset:18432
	ds_read_b128 v[204:207], v152 offset:19456
	ds_read_b128 v[208:211], v152 offset:20480
	ds_read_b128 v[212:215], v152 offset:21504
	ds_read_b128 v[220:223], v152 offset:22528
	ds_read_b128 v[224:227], v152 offset:23552
	s_mov_b32 m0, s2
	s_nop 0
	global_load_lds_dwordx4 v135, s[22:23]
	v_mov_b32_e32 v135, v141
	s_add_i32 m0, s2, 0x2000
	s_add_u32 s2, s22, 0x40000
	global_load_lds_dwordx4 v135, s[22:23]
	s_addc_u32 s3, s23, 0
	v_mov_b32_e32 v135, v138
	s_add_i32 s76, s77, s63
	s_mov_b32 m0, s76
	s_nop 0
	global_load_lds_dwordx4 v135, s[2:3]
	v_mov_b32_e32 v135, v141
	s_add_i32 m0, s76, 0x2000
	s_nop 0
	global_load_lds_dwordx4 v135, s[2:3]
	v_mov_b32_e32 v135, v134
	s_mov_b32 m0, s64
	s_nop 0
	global_load_lds_dwordx4 v135, s[20:21]
	v_mov_b32_e32 v135, v132
	s_mov_b32 m0, s65
	s_nop 0
	global_load_lds_dwordx4 v135, s[20:21]
	s_waitcnt vmcnt(8)
	s_waitcnt lgkmcnt(0)
	s_barrier
; #define PG8_STAGE(bufoff, gbase, voff) do { _Pragma("unroll") for (int _i = 0; _i < 2; ++_i) \
;         __builtin_amdgcn_global_load_lds((const __attribute__((address_space(1))) unsigned*)((const __attribute__((address_space(1))) char*)(gbase) + (unsigned)lnd_v((int)(voff)[_i])), (LAS unsigned*)(lds + (bufoff) + ldsw + _i * 8192), 16, 0, 0); } while (0)
; #define PG8_LDA(dst, b, h) do { _Pragma("unroll") for (int m = 0; m < 4; ++m) _Pragma("unroll") for (int k = 0; k < 2; ++k) dst[m][k] = *(const LAS bf16x8*)(lds + PG8_SA(b, h) + aoff + m * 2048 + k * 1024); } while (0)
; #define PG8_LDB(dst, b, h) do { _Pragma("unroll") for (int n = 0; n < 2; ++n) _Pragma("unroll") for (int k = 0; k < 2; ++k) dst[n][k] = *(const LAS bf16x8*)(lds + PG8_SB(b, h) + boff + n * 2048 + k * 1024); } while (0)
; #define PG8_MMA(ai, bj, At, Bt) do { __builtin_amdgcn_s_setprio(1); _Pragma("unroll") for (int m = 0; m < 4; ++m) _Pragma("unroll") for (int n = 0; n < 2; ++n) _Pragma("unroll") for (int k = 0; k < 2; ++k) \
;         acc[ai][bj][m][n] = __builtin_amdgcn_mfma_f32_16x16x32_bf16(Bt[n][k], At[m][k], acc[ai][bj][m][n], 0, 0, 0); __builtin_amdgcn_s_setprio(0); } while (0)
; #define PG8_WAIT_V(n) asm volatile("s_waitcnt vmcnt(" #n ")" ::: "memory")
; #define PG8_WAIT_L(n) asm volatile("s_waitcnt lgkmcnt(" #n ")" ::: "memory")
; #define PG8_BAR __builtin_amdgcn_s_barrier()
; #define PG8_SCHED __builtin_amdgcn_sched_barrier(0)
; template <class Desc, class Epi>
; __device__ __forceinline__ void gemm_phase(const int wv_, LAS unsigned char* lds, const Desc& d, const Epi& E) {
;     ...
;             PG8_WAIT_V(8); PG8_WAIT_L(0); PG8_BAR; PG8_MMA(1, 0, At, B0); PG8_MMA(1, 1, At, B1); PG8_BAR; PG8_SCHED;
;             PG8_LDB(B0, 1, 0); PG8_LDB(B1, 1, 1); PG8_SCHED; PG8_LDA(At, 1, 0); PG8_STAGE(PG8_SA(0, 1), a2, sA1);
;             PG8_WAIT_V(8); PG8_WAIT_L(0); PG8_BAR; PG8_MMA(0, 0, At, B0); PG8_MMA(0, 1, At, B1); PG8_BAR; PG8_SCHED;
	v_mfma_f32_16x16x32_bf16 v[56:59], v[160:163], v[192:195], v[56:59]
	v_mfma_f32_16x16x32_bf16 v[48:51], v[168:171], v[192:195], v[48:51]
	v_mfma_f32_16x16x32_bf16 v[40:43], v[160:163], v[200:203], v[40:43]
	v_mfma_f32_16x16x32_bf16 v[32:35], v[168:171], v[200:203], v[32:35]
	v_mfma_f32_16x16x32_bf16 v[24:27], v[160:163], v[208:211], v[24:27]
	v_mfma_f32_16x16x32_bf16 v[16:19], v[168:171], v[208:211], v[16:19]
	v_mfma_f32_16x16x32_bf16 v[8:11], v[160:163], v[220:223], v[8:11]
	v_mfma_f32_16x16x32_bf16 v[4:7], v[168:171], v[220:223], v[4:7]
	v_mfma_f32_16x16x32_bf16 v[56:59], v[164:167], v[196:199], v[56:59]
	v_mfma_f32_16x16x32_bf16 v[48:51], v[172:175], v[196:199], v[48:51]
	v_mfma_f32_16x16x32_bf16 v[40:43], v[164:167], v[204:207], v[40:43]
	v_mfma_f32_16x16x32_bf16 v[32:35], v[172:175], v[204:207], v[32:35]
	v_mfma_f32_16x16x32_bf16 v[24:27], v[164:167], v[212:215], v[24:27]
	v_mfma_f32_16x16x32_bf16 v[16:19], v[172:175], v[212:215], v[16:19]
	v_mfma_f32_16x16x32_bf16 v[8:11], v[164:167], v[224:227], v[8:11]
	v_mfma_f32_16x16x32_bf16 v[4:7], v[172:175], v[224:227], v[4:7]
	v_mfma_f32_16x16x32_bf16 v[60:63], v[176:179], v[192:195], v[60:63]
	v_mfma_f32_16x16x32_bf16 v[52:55], v[184:187], v[192:195], v[52:55]
	v_mfma_f32_16x16x32_bf16 v[44:47], v[176:179], v[200:203], v[44:47]
	v_mfma_f32_16x16x32_bf16 v[36:39], v[184:187], v[200:203], v[36:39]
	v_mfma_f32_16x16x32_bf16 v[28:31], v[176:179], v[208:211], v[28:31]
	v_mfma_f32_16x16x32_bf16 v[20:23], v[184:187], v[208:211], v[20:23]
	v_mfma_f32_16x16x32_bf16 v[12:15], v[176:179], v[220:223], v[12:15]
	v_mfma_f32_16x16x32_bf16 v[0:3], v[184:187], v[220:223], v[0:3]
	v_mfma_f32_16x16x32_bf16 v[60:63], v[180:183], v[196:199], v[60:63]
	v_mfma_f32_16x16x32_bf16 v[52:55], v[188:191], v[196:199], v[52:55]
	v_mfma_f32_16x16x32_bf16 v[44:47], v[180:183], v[204:207], v[44:47]
	v_mfma_f32_16x16x32_bf16 v[36:39], v[188:191], v[204:207], v[36:39]
	v_mfma_f32_16x16x32_bf16 v[28:31], v[180:183], v[212:215], v[28:31]
	v_mfma_f32_16x16x32_bf16 v[20:23], v[188:191], v[212:215], v[20:23]
	v_mfma_f32_16x16x32_bf16 v[12:15], v[180:183], v[224:227], v[12:15]
	v_mfma_f32_16x16x32_bf16 v[0:3], v[188:191], v[224:227], v[0:3]
	s_barrier
	s_add_i32 s2, 0, 0x18000
	v_add_u32_e32 v135, s2, v143
	s_add_i32 s76, 0, 0x1c000
	ds_read_b128 v[160:163], v135
	ds_read_b128 v[164:167], v135 offset:1024
	ds_read_b128 v[168:171], v135 offset:2048
	ds_read_b128 v[172:175], v135 offset:3072
	v_add_u32_e32 v135, s76, v143
	ds_read_b128 v[176:179], v135
	ds_read_b128 v[180:183], v135 offset:1024
	ds_read_b128 v[184:187], v135 offset:2048
	ds_read_b128 v[188:191], v135 offset:3072
	s_mov_b32 m0, s68
	ds_read_b128 v[192:195], v152 offset:32768
	ds_read_b128 v[196:199], v152 offset:33792
	ds_read_b128 v[200:203], v152 offset:34816
	ds_read_b128 v[204:207], v152 offset:35840
	ds_read_b128 v[208:211], v152 offset:36864
	ds_read_b128 v[212:215], v152 offset:37888
	ds_read_b128 v[220:223], v152 offset:38912
	ds_read_b128 v[224:227], v152 offset:39936
	s_nop 0
	global_load_lds_dwordx4 v96, s[20:21]
	s_mov_b32 m0, s69
	s_nop 0
	global_load_lds_dwordx4 v133, s[20:21]
	s_waitcnt vmcnt(8)
	s_waitcnt lgkmcnt(0)
	s_barrier
	v_mfma_f32_16x16x32_bf16 v[122:125], v[160:163], v[192:195], v[122:125]
	v_mfma_f32_16x16x32_bf16 v[114:117], v[168:171], v[192:195], v[114:117]
	v_mfma_f32_16x16x32_bf16 v[106:109], v[160:163], v[200:203], v[106:109]
	v_mfma_f32_16x16x32_bf16 v[98:101], v[168:171], v[200:203], v[98:101]
	v_mfma_f32_16x16x32_bf16 v[88:91], v[160:163], v[208:211], v[88:91]
	v_mfma_f32_16x16x32_bf16 v[80:83], v[168:171], v[208:211], v[80:83]
	v_mfma_f32_16x16x32_bf16 v[72:75], v[160:163], v[220:223], v[72:75]
	v_mfma_f32_16x16x32_bf16 v[64:67], v[168:171], v[220:223], v[64:67]
	v_mfma_f32_16x16x32_bf16 v[122:125], v[164:167], v[196:199], v[122:125]
	v_mfma_f32_16x16x32_bf16 v[114:117], v[172:175], v[196:199], v[114:117]
	v_mfma_f32_16x16x32_bf16 v[106:109], v[164:167], v[204:207], v[106:109]
	v_mfma_f32_16x16x32_bf16 v[98:101], v[172:175], v[204:207], v[98:101]
	v_mfma_f32_16x16x32_bf16 v[88:91], v[164:167], v[212:215], v[88:91]
	v_mfma_f32_16x16x32_bf16 v[80:83], v[172:175], v[212:215], v[80:83]
	v_mfma_f32_16x16x32_bf16 v[72:75], v[164:167], v[224:227], v[72:75]
	v_mfma_f32_16x16x32_bf16 v[64:67], v[172:175], v[224:227], v[64:67]
	v_mfma_f32_16x16x32_bf16 v[126:129], v[176:179], v[192:195], v[126:129]
	v_mfma_f32_16x16x32_bf16 v[118:121], v[184:187], v[192:195], v[118:121]
	v_mfma_f32_16x16x32_bf16 v[110:113], v[176:179], v[200:203], v[110:113]
	v_mfma_f32_16x16x32_bf16 v[102:105], v[184:187], v[200:203], v[102:105]
	v_mfma_f32_16x16x32_bf16 v[92:95], v[176:179], v[208:211], v[92:95]
	v_mfma_f32_16x16x32_bf16 v[84:87], v[184:187], v[208:211], v[84:87]
	v_mfma_f32_16x16x32_bf16 v[76:79], v[176:179], v[220:223], v[76:79]
	v_mfma_f32_16x16x32_bf16 v[68:71], v[184:187], v[220:223], v[68:71]
	v_mfma_f32_16x16x32_bf16 v[126:129], v[180:183], v[196:199], v[126:129]
	v_mfma_f32_16x16x32_bf16 v[118:121], v[188:191], v[196:199], v[118:121]
	v_mfma_f32_16x16x32_bf16 v[110:113], v[180:183], v[204:207], v[110:113]
	v_mfma_f32_16x16x32_bf16 v[102:105], v[188:191], v[204:207], v[102:105]
	v_mfma_f32_16x16x32_bf16 v[92:95], v[180:183], v[212:215], v[92:95]
	v_mfma_f32_16x16x32_bf16 v[84:87], v[188:191], v[212:215], v[84:87]
	v_mfma_f32_16x16x32_bf16 v[76:79], v[180:183], v[224:227], v[76:79]
	v_mfma_f32_16x16x32_bf16 v[68:71], v[188:191], v[224:227], v[68:71]
	s_barrier
; #define PG8_STAGE(bufoff, gbase, voff) do { _Pragma("unroll") for (int _i = 0; _i < 2; ++_i) \
;         __builtin_amdgcn_global_load_lds((const __attribute__((address_space(1))) unsigned*)((const __attribute__((address_space(1))) char*)(gbase) + (unsigned)lnd_v((int)(voff)[_i])), (LAS unsigned*)(lds + (bufoff) + ldsw + _i * 8192), 16, 0, 0); } while (0)
; #define PG8_LDA(dst, b, h) do { _Pragma("unroll") for (int m = 0; m < 4; ++m) _Pragma("unroll") for (int k = 0; k < 2; ++k) dst[m][k] = *(const LAS bf16x8*)(lds + PG8_SA(b, h) + aoff + m * 2048 + k * 1024); } while (0)
; #define PG8_MMA(ai, bj, At, Bt) do { __builtin_amdgcn_s_setprio(1); _Pragma("unroll") for (int m = 0; m < 4; ++m) _Pragma("unroll") for (int n = 0; n < 2; ++n) _Pragma("unroll") for (int k = 0; k < 2; ++k) \
;         acc[ai][bj][m][n] = __builtin_amdgcn_mfma_f32_16x16x32_bf16(Bt[n][k], At[m][k], acc[ai][bj][m][n], 0, 0, 0); __builtin_amdgcn_s_setprio(0); } while (0)
; #define PG8_WAIT_V(n) asm volatile("s_waitcnt vmcnt(" #n ")" ::: "memory")
; #define PG8_WAIT_L(n) asm volatile("s_waitcnt lgkmcnt(" #n ")" ::: "memory")
; #define PG8_BAR __builtin_amdgcn_s_barrier()
; #define PG8_SCHED __builtin_amdgcn_sched_barrier(0)
; template <class Desc, class Epi>
; __device__ __forceinline__ void gemm_phase(const int wv_, LAS unsigned char* lds, const Desc& d, const Epi& E) {
;     ...
;             PG8_LDA(At, 1, 1); PG8_STAGE(PG8_SB(1, 0), b3, voffB); PG8_STAGE(PG8_SB(1, 1), b3 + hstepB, voffB); PG8_STAGE(PG8_SA(1, 0), a3, sA0);
;             PG8_WAIT_V(8); PG8_WAIT_L(0); PG8_BAR; PG8_MMA(1, 0, At, B0); PG8_MMA(1, 1, At, B1); PG8_BAR; PG8_SCHED;
;         }
;         if (wr == 0) PG8_BAR;
	v_mov_b32_e32 v96, v138
	ds_read_b128 v[192:195], v152 offset:49152
	ds_read_b128 v[196:199], v152 offset:50176
	ds_read_b128 v[200:203], v152 offset:51200
	ds_read_b128 v[204:207], v152 offset:52224
	ds_read_b128 v[208:211], v152 offset:53248
	ds_read_b128 v[212:215], v152 offset:54272
	ds_read_b128 v[220:223], v152 offset:55296
	ds_read_b128 v[224:227], v152 offset:56320
	s_add_i32 s2, s2, s63
	v_lshl_add_u64 v[228:229], s[22:23], 0, v[96:97]
	v_lshl_add_u64 v[228:229], v[228:229], 0, s[30:31]
	s_mov_b32 m0, s2
	v_mov_b32_e32 v96, v141
	global_load_lds_dwordx4 v[228:229], off
	s_add_i32 m0, s2, 0x2000
	s_add_u32 s2, s22, 0x40080
	v_lshl_add_u64 v[228:229], s[22:23], 0, v[96:97]
	v_lshl_add_u64 v[228:229], v[228:229], 0, s[30:31]
	s_addc_u32 s3, s23, 0
	v_mov_b32_e32 v96, v138
	s_add_i32 s22, s76, s63
	global_load_lds_dwordx4 v[228:229], off
	s_mov_b32 m0, s22
	v_mov_b32_e32 v135, v97
	global_load_lds_dwordx4 v96, s[2:3]
	v_mov_b32_e32 v96, v141
	s_add_i32 m0, s22, 0x2000
	v_mov_b32_e32 v133, v97
	global_load_lds_dwordx4 v96, s[2:3]
	s_mov_b32 m0, s70
	v_lshl_add_u64 v[134:135], s[20:21], 0, v[134:135]
	v_lshl_add_u64 v[134:135], v[134:135], 0, s[30:31]
	global_load_lds_dwordx4 v[134:135], off
	s_mov_b32 m0, s71
	v_lshl_add_u64 v[132:133], s[20:21], 0, v[132:133]
	v_lshl_add_u64 v[132:133], v[132:133], 0, s[30:31]
	global_load_lds_dwordx4 v[132:133], off
	s_waitcnt vmcnt(8)
	s_waitcnt lgkmcnt(0)
	s_barrier
	v_mfma_f32_16x16x32_bf16 v[56:59], v[160:163], v[192:195], v[56:59]
	v_mfma_f32_16x16x32_bf16 v[48:51], v[168:171], v[192:195], v[48:51]
	v_mfma_f32_16x16x32_bf16 v[40:43], v[160:163], v[200:203], v[40:43]
	v_mfma_f32_16x16x32_bf16 v[32:35], v[168:171], v[200:203], v[32:35]
	v_mfma_f32_16x16x32_bf16 v[24:27], v[160:163], v[208:211], v[24:27]
	v_mfma_f32_16x16x32_bf16 v[16:19], v[168:171], v[208:211], v[16:19]
	v_mfma_f32_16x16x32_bf16 v[8:11], v[160:163], v[220:223], v[8:11]
	v_mfma_f32_16x16x32_bf16 v[4:7], v[168:171], v[220:223], v[4:7]
	v_mfma_f32_16x16x32_bf16 v[56:59], v[164:167], v[196:199], v[56:59]
	v_mfma_f32_16x16x32_bf16 v[48:51], v[172:175], v[196:199], v[48:51]
	v_mfma_f32_16x16x32_bf16 v[40:43], v[164:167], v[204:207], v[40:43]
	v_mfma_f32_16x16x32_bf16 v[32:35], v[172:175], v[204:207], v[32:35]
	v_mfma_f32_16x16x32_bf16 v[24:27], v[164:167], v[212:215], v[24:27]
	v_mfma_f32_16x16x32_bf16 v[16:19], v[172:175], v[212:215], v[16:19]
	v_mfma_f32_16x16x32_bf16 v[8:11], v[164:167], v[224:227], v[8:11]
	v_mfma_f32_16x16x32_bf16 v[4:7], v[172:175], v[224:227], v[4:7]
	v_mfma_f32_16x16x32_bf16 v[60:63], v[176:179], v[192:195], v[60:63]
	v_mfma_f32_16x16x32_bf16 v[52:55], v[184:187], v[192:195], v[52:55]
	v_mfma_f32_16x16x32_bf16 v[44:47], v[176:179], v[200:203], v[44:47]
	v_mfma_f32_16x16x32_bf16 v[36:39], v[184:187], v[200:203], v[36:39]
	v_mfma_f32_16x16x32_bf16 v[28:31], v[176:179], v[208:211], v[28:31]
	v_mfma_f32_16x16x32_bf16 v[20:23], v[184:187], v[208:211], v[20:23]
	v_mfma_f32_16x16x32_bf16 v[12:15], v[176:179], v[220:223], v[12:15]
	v_mfma_f32_16x16x32_bf16 v[0:3], v[184:187], v[220:223], v[0:3]
	v_mfma_f32_16x16x32_bf16 v[60:63], v[180:183], v[196:199], v[60:63]
	v_mfma_f32_16x16x32_bf16 v[52:55], v[188:191], v[196:199], v[52:55]
	v_mfma_f32_16x16x32_bf16 v[44:47], v[180:183], v[204:207], v[44:47]
	v_mfma_f32_16x16x32_bf16 v[36:39], v[188:191], v[204:207], v[36:39]
	v_mfma_f32_16x16x32_bf16 v[28:31], v[180:183], v[212:215], v[28:31]
	v_mfma_f32_16x16x32_bf16 v[20:23], v[188:191], v[212:215], v[20:23]
	v_mfma_f32_16x16x32_bf16 v[12:15], v[180:183], v[224:227], v[12:15]
	v_mfma_f32_16x16x32_bf16 v[0:3], v[188:191], v[224:227], v[0:3]
	s_barrier
	s_add_i32 s75, s75, 2
	s_cmp_gt_u32 s75, 13
	s_mov_b64 s[2:3], s[4:5]
	s_cbranch_scc0 .LBB0_1565
	s_and_b64 vcc, exec, s[52:53]
	s_cbranch_vccz .LBB0_1568
	s_barrier

; #define PG8_AOFF(ord, U, O0, O1) do { _Pragma("unroll") for (int _i = 0; _i < 2; ++_i) { \
;         O0[_i] = d.rowbyte(U, (int)tix[(ord) * 256 + Rr[_i]]) + (unsigned)(Cc[_i] * 2); O1[_i] = d.rowbyte(U, (int)tix[(ord) * 256 + HALF + Rr[_i]]) + (unsigned)(Cc[_i] * 2); } } while (0)
; #define PG8_STAGE(bufoff, gbase, voff) do { _Pragma("unroll") for (int _i = 0; _i < 2; ++_i) \
;         __builtin_amdgcn_global_load_lds((const __attribute__((address_space(1))) unsigned*)((const __attribute__((address_space(1))) char*)(gbase) + (unsigned)lnd_v((int)(voff)[_i])), (LAS unsigned*)(lds + (bufoff) + ldsw + _i * 8192), 16, 0, 0); } while (0)
; #define PG8_WAIT_V(n) asm volatile("s_waitcnt vmcnt(" #n ")" ::: "memory")
; #define PG8_WAIT_L(n) asm volatile("s_waitcnt lgkmcnt(" #n ")" ::: "memory")
; #define PG8_BAR __builtin_amdgcn_s_barrier()
; template <class Desc, class Epi>
; __device__ __forceinline__ void gemm_phase(const int wv_, LAS unsigned char* lds, const Desc& d, const Epi& E) {
;     ...
;         if constexpr (Desc::GATHER) { if (has_next) PG8_AOFF(ui + 1, nxt, voffAn, voffAn1); else { voffAn[0] = voffA[0]; voffAn[1] = voffA[1]; voffAn1[0] = voffA1[0]; voffAn1[1] = voffA1[1]; } }
;         const char* nA = has_next ? (const char*)nxt.a : cA; const char* nB = has_next ? (const char*)nxt.b : cB;
;         for (int t = 0; t < nt; t += 2) {
;             const bool last = (t == nt - 2);
;             unsigned sA0[2], sA1[2];
;             if constexpr (Desc::GATHER) { sA0[0] = last ? voffAn[0] : voffA[0]; sA0[1] = last ? voffAn[1] : voffA[1]; sA1[0] = last ? voffAn1[0] : voffA1[0]; sA1[1] = last ? voffAn1[1] : voffA1[1]; }
;             else { sA0[0] = voffA[0]; sA0[1] = voffA[1]; sA1[0] = voffA1[0]; sA1[1] = voffA1[1]; }
;             const char* a1 = cA + (size_t)(t + 1) * kstep;
;             const char* a2 = last ? nA : cA + (size_t)(t + 2) * kstep; const char* b2 = last ? nB : cB + (size_t)(t + 2) * kstep;
;             const char* a3 = a2 + kstep; const char* b3 = b2 + kstep;
;             PG8_LDB(B0, 0, 0); PG8_LDB(B1, 0, 1); PG8_SCHED; PG8_LDA(At, 0, 0); PG8_STAGE(PG8_SA(1, 1), a1, voffA1);
;             PG8_WAIT_V(8); PG8_WAIT_L(0); PG8_BAR; PG8_MMA(0, 0, At, B0); PG8_MMA(0, 1, At, B1); PG8_BAR; PG8_SCHED;
;             PG8_LDA(At, 0, 1); PG8_STAGE(PG8_SB(0, 0), b2, voffB); PG8_STAGE(PG8_SB(0, 1), b2 + hstepB, voffB); PG8_STAGE(PG8_SA(0, 0), a2, sA0);
.LBB0_1861:
	s_add_u32 s4, s2, 0x100
	s_addc_u32 s5, s3, 0
	s_add_u32 s22, s29, s2
	s_addc_u32 s23, s51, s3
	s_cmp_eq_u32 s66, 12
	s_cselect_b64 vcc, -1, 0
	s_and_b64 s[20:21], vcc, exec
	s_cselect_b32 s20, 0, s4
	s_cselect_b32 s21, 0, s5
	s_cselect_b32 s22, s46, s22
	s_cselect_b32 s23, s47, s23
	s_add_u32 s20, s42, s20
	s_addc_u32 s21, s43, s21
	s_add_i32 s67, 0, 0x10000
	v_add_u32_e32 v135, s67, v143
	s_add_i32 s68, 0, 0x14000
	ds_read_b128 v[160:163], v135
	ds_read_b128 v[164:167], v135 offset:1024
	ds_read_b128 v[168:171], v135 offset:2048
	ds_read_b128 v[172:175], v135 offset:3072
	v_add_u32_e32 v135, s68, v143
	ds_read_b128 v[176:179], v135
	ds_read_b128 v[180:183], v135 offset:1024
	ds_read_b128 v[184:187], v135 offset:2048
	ds_read_b128 v[188:191], v135 offset:3072
	v_cndmask_b32_e32 v134, v157, v153, vcc
	v_cndmask_b32_e32 v132, v159, v154, vcc
	v_cndmask_b32_e32 v96, v131, v155, vcc
	v_cndmask_b32_e32 v133, v158, v156, vcc
	s_add_i32 m0, s57, 0xc000
	v_mov_b32_e32 v135, v131
	s_add_u32 s2, s38, s2
	ds_read_b128 v[192:195], v152
	ds_read_b128 v[196:199], v152 offset:1024
	ds_read_b128 v[200:203], v152 offset:2048
	ds_read_b128 v[204:207], v152 offset:3072
	ds_read_b128 v[208:211], v152 offset:4096
	ds_read_b128 v[212:215], v152 offset:5120
	ds_read_b128 v[220:223], v152 offset:6144
	ds_read_b128 v[224:227], v152 offset:7168
	s_addc_u32 s3, s39, s3
	global_load_lds_dwordx4 v135, s[2:3]
	v_mov_b32_e32 v135, v158
	s_add_i32 m0, s57, 0xe000
	s_nop 0
	global_load_lds_dwordx4 v135, s[2:3]
	s_waitcnt vmcnt(8)
	s_waitcnt lgkmcnt(0)
	s_barrier
	v_mfma_f32_16x16x32_bf16 v[122:125], v[160:163], v[192:195], v[122:125]
	v_mfma_f32_16x16x32_bf16 v[114:117], v[168:171], v[192:195], v[114:117]
	v_mfma_f32_16x16x32_bf16 v[106:109], v[160:163], v[200:203], v[106:109]
	v_mfma_f32_16x16x32_bf16 v[98:101], v[168:171], v[200:203], v[98:101]
	v_mfma_f32_16x16x32_bf16 v[88:91], v[160:163], v[208:211], v[88:91]
	v_mfma_f32_16x16x32_bf16 v[80:83], v[168:171], v[208:211], v[80:83]
	v_mfma_f32_16x16x32_bf16 v[72:75], v[160:163], v[220:223], v[72:75]
	v_mfma_f32_16x16x32_bf16 v[64:67], v[168:171], v[220:223], v[64:67]
	v_mfma_f32_16x16x32_bf16 v[122:125], v[164:167], v[196:199], v[122:125]
	v_mfma_f32_16x16x32_bf16 v[114:117], v[172:175], v[196:199], v[114:117]
	v_mfma_f32_16x16x32_bf16 v[106:109], v[164:167], v[204:207], v[106:109]
	v_mfma_f32_16x16x32_bf16 v[98:101], v[172:175], v[204:207], v[98:101]
	v_mfma_f32_16x16x32_bf16 v[88:91], v[164:167], v[212:215], v[88:91]
	v_mfma_f32_16x16x32_bf16 v[80:83], v[172:175], v[212:215], v[80:83]
	v_mfma_f32_16x16x32_bf16 v[72:75], v[164:167], v[224:227], v[72:75]
	v_mfma_f32_16x16x32_bf16 v[64:67], v[172:175], v[224:227], v[64:67]
	v_mfma_f32_16x16x32_bf16 v[126:129], v[176:179], v[192:195], v[126:129]
	v_mfma_f32_16x16x32_bf16 v[118:121], v[184:187], v[192:195], v[118:121]
	v_mfma_f32_16x16x32_bf16 v[110:113], v[176:179], v[200:203], v[110:113]
	v_mfma_f32_16x16x32_bf16 v[102:105], v[184:187], v[200:203], v[102:105]
	v_mfma_f32_16x16x32_bf16 v[92:95], v[176:179], v[208:211], v[92:95]
	v_mfma_f32_16x16x32_bf16 v[84:87], v[184:187], v[208:211], v[84:87]
	v_mfma_f32_16x16x32_bf16 v[76:79], v[176:179], v[220:223], v[76:79]
	v_mfma_f32_16x16x32_bf16 v[68:71], v[184:187], v[220:223], v[68:71]
	v_mfma_f32_16x16x32_bf16 v[126:129], v[180:183], v[196:199], v[126:129]
	v_mfma_f32_16x16x32_bf16 v[118:121], v[188:191], v[196:199], v[118:121]
	v_mfma_f32_16x16x32_bf16 v[110:113], v[180:183], v[204:207], v[110:113]
	v_mfma_f32_16x16x32_bf16 v[102:105], v[188:191], v[204:207], v[102:105]
	v_mfma_f32_16x16x32_bf16 v[92:95], v[180:183], v[212:215], v[92:95]
	v_mfma_f32_16x16x32_bf16 v[84:87], v[188:191], v[212:215], v[84:87]
	v_mfma_f32_16x16x32_bf16 v[76:79], v[180:183], v[224:227], v[76:79]
	v_mfma_f32_16x16x32_bf16 v[68:71], v[188:191], v[224:227], v[68:71]
	s_barrier
	v_mov_b32_e32 v135, v138
	s_add_i32 s2, s67, s56
	ds_read_b128 v[192:195], v152 offset:16384
	ds_read_b128 v[196:199], v152 offset:17408
	ds_read_b128 v[200:203], v152 offset:18432
	ds_read_b128 v[204:207], v152 offset:19456
	ds_read_b128 v[208:211], v152 offset:20480
	ds_read_b128 v[212:215], v152 offset:21504
	ds_read_b128 v[220:223], v152 offset:22528
	ds_read_b128 v[224:227], v152 offset:23552
	s_mov_b32 m0, s2
	s_nop 0
	global_load_lds_dwordx4 v135, s[22:23]
	v_mov_b32_e32 v135, v141
	s_add_i32 m0, s2, 0x2000
	s_add_u32 s2, s22, 0x40000
	global_load_lds_dwordx4 v135, s[22:23]
	s_addc_u32 s3, s23, 0
	v_mov_b32_e32 v135, v138
	s_add_i32 s67, s68, s56
	s_mov_b32 m0, s67
	s_nop 0
	global_load_lds_dwordx4 v135, s[2:3]
	v_mov_b32_e32 v135, v141
	s_add_i32 m0, s67, 0x2000
	s_nop 0
	global_load_lds_dwordx4 v135, s[2:3]
	v_mov_b32_e32 v135, v134
	s_mov_b32 m0, s57
	s_nop 0
	global_load_lds_dwordx4 v135, s[20:21]
	v_mov_b32_e32 v135, v132
	s_mov_b32 m0, s58
	s_nop 0
	global_load_lds_dwordx4 v135, s[20:21]
	s_waitcnt vmcnt(8)
	s_waitcnt lgkmcnt(0)
	s_barrier
; #define PG8_STAGE(bufoff, gbase, voff) do { _Pragma("unroll") for (int _i = 0; _i < 2; ++_i) \
;         __builtin_amdgcn_global_load_lds((const __attribute__((address_space(1))) unsigned*)((const __attribute__((address_space(1))) char*)(gbase) + (unsigned)lnd_v((int)(voff)[_i])), (LAS unsigned*)(lds + (bufoff) + ldsw + _i * 8192), 16, 0, 0); } while (0)
; #define PG8_LDA(dst, b, h) do { _Pragma("unroll") for (int m = 0; m < 4; ++m) _Pragma("unroll") for (int k = 0; k < 2; ++k) dst[m][k] = *(const LAS bf16x8*)(lds + PG8_SA(b, h) + aoff + m * 2048 + k * 1024); } while (0)
; #define PG8_LDB(dst, b, h) do { _Pragma("unroll") for (int n = 0; n < 2; ++n) _Pragma("unroll") for (int k = 0; k < 2; ++k) dst[n][k] = *(const LAS bf16x8*)(lds + PG8_SB(b, h) + boff + n * 2048 + k * 1024); } while (0)
; #define PG8_MMA(ai, bj, At, Bt) do { __builtin_amdgcn_s_setprio(1); _Pragma("unroll") for (int m = 0; m < 4; ++m) _Pragma("unroll") for (int n = 0; n < 2; ++n) _Pragma("unroll") for (int k = 0; k < 2; ++k) \
;         acc[ai][bj][m][n] = __builtin_amdgcn_mfma_f32_16x16x32_bf16(Bt[n][k], At[m][k], acc[ai][bj][m][n], 0, 0, 0); __builtin_amdgcn_s_setprio(0); } while (0)
; #define PG8_WAIT_V(n) asm volatile("s_waitcnt vmcnt(" #n ")" ::: "memory")
; #define PG8_WAIT_L(n) asm volatile("s_waitcnt lgkmcnt(" #n ")" ::: "memory")
; #define PG8_BAR __builtin_amdgcn_s_barrier()
; #define PG8_SCHED __builtin_amdgcn_sched_barrier(0)
; template <class Desc, class Epi>
; __device__ __forceinline__ void gemm_phase(const int wv_, LAS unsigned char* lds, const Desc& d, const Epi& E) {
;     ...
;             PG8_WAIT_V(8); PG8_WAIT_L(0); PG8_BAR; PG8_MMA(1, 0, At, B0); PG8_MMA(1, 1, At, B1); PG8_BAR; PG8_SCHED;
;             PG8_LDB(B0, 1, 0); PG8_LDB(B1, 1, 1); PG8_SCHED; PG8_LDA(At, 1, 0); PG8_STAGE(PG8_SA(0, 1), a2, sA1);
;             PG8_WAIT_V(8); PG8_WAIT_L(0); PG8_BAR; PG8_MMA(0, 0, At, B0); PG8_MMA(0, 1, At, B1); PG8_BAR; PG8_SCHED;
	v_mfma_f32_16x16x32_bf16 v[56:59], v[160:163], v[192:195], v[56:59]
	v_mfma_f32_16x16x32_bf16 v[48:51], v[168:171], v[192:195], v[48:51]
	v_mfma_f32_16x16x32_bf16 v[40:43], v[160:163], v[200:203], v[40:43]
	v_mfma_f32_16x16x32_bf16 v[32:35], v[168:171], v[200:203], v[32:35]
	v_mfma_f32_16x16x32_bf16 v[24:27], v[160:163], v[208:211], v[24:27]
	v_mfma_f32_16x16x32_bf16 v[16:19], v[168:171], v[208:211], v[16:19]
	v_mfma_f32_16x16x32_bf16 v[8:11], v[160:163], v[220:223], v[8:11]
	v_mfma_f32_16x16x32_bf16 v[4:7], v[168:171], v[220:223], v[4:7]
	v_mfma_f32_16x16x32_bf16 v[56:59], v[164:167], v[196:199], v[56:59]
	v_mfma_f32_16x16x32_bf16 v[48:51], v[172:175], v[196:199], v[48:51]
	v_mfma_f32_16x16x32_bf16 v[40:43], v[164:167], v[204:207], v[40:43]
	v_mfma_f32_16x16x32_bf16 v[32:35], v[172:175], v[204:207], v[32:35]
	v_mfma_f32_16x16x32_bf16 v[24:27], v[164:167], v[212:215], v[24:27]
	v_mfma_f32_16x16x32_bf16 v[16:19], v[172:175], v[212:215], v[16:19]
	v_mfma_f32_16x16x32_bf16 v[8:11], v[164:167], v[224:227], v[8:11]
	v_mfma_f32_16x16x32_bf16 v[4:7], v[172:175], v[224:227], v[4:7]
	v_mfma_f32_16x16x32_bf16 v[60:63], v[176:179], v[192:195], v[60:63]
	v_mfma_f32_16x16x32_bf16 v[52:55], v[184:187], v[192:195], v[52:55]
	v_mfma_f32_16x16x32_bf16 v[44:47], v[176:179], v[200:203], v[44:47]
	v_mfma_f32_16x16x32_bf16 v[36:39], v[184:187], v[200:203], v[36:39]
	v_mfma_f32_16x16x32_bf16 v[28:31], v[176:179], v[208:211], v[28:31]
	v_mfma_f32_16x16x32_bf16 v[20:23], v[184:187], v[208:211], v[20:23]
	v_mfma_f32_16x16x32_bf16 v[12:15], v[176:179], v[220:223], v[12:15]
	v_mfma_f32_16x16x32_bf16 v[0:3], v[184:187], v[220:223], v[0:3]
	v_mfma_f32_16x16x32_bf16 v[60:63], v[180:183], v[196:199], v[60:63]
	v_mfma_f32_16x16x32_bf16 v[52:55], v[188:191], v[196:199], v[52:55]
	v_mfma_f32_16x16x32_bf16 v[44:47], v[180:183], v[204:207], v[44:47]
	v_mfma_f32_16x16x32_bf16 v[36:39], v[188:191], v[204:207], v[36:39]
	v_mfma_f32_16x16x32_bf16 v[28:31], v[180:183], v[212:215], v[28:31]
	v_mfma_f32_16x16x32_bf16 v[20:23], v[188:191], v[212:215], v[20:23]
	v_mfma_f32_16x16x32_bf16 v[12:15], v[180:183], v[224:227], v[12:15]
	v_mfma_f32_16x16x32_bf16 v[0:3], v[188:191], v[224:227], v[0:3]
	s_barrier
	s_add_i32 s2, 0, 0x18000
	v_add_u32_e32 v135, s2, v143
	s_add_i32 s67, 0, 0x1c000
	ds_read_b128 v[160:163], v135
	ds_read_b128 v[164:167], v135 offset:1024
	ds_read_b128 v[168:171], v135 offset:2048
	ds_read_b128 v[172:175], v135 offset:3072
	v_add_u32_e32 v135, s67, v143
	ds_read_b128 v[176:179], v135
	ds_read_b128 v[180:183], v135 offset:1024
	ds_read_b128 v[184:187], v135 offset:2048
	ds_read_b128 v[188:191], v135 offset:3072
	s_mov_b32 m0, s59
	ds_read_b128 v[192:195], v152 offset:32768
	ds_read_b128 v[196:199], v152 offset:33792
	ds_read_b128 v[200:203], v152 offset:34816
	ds_read_b128 v[204:207], v152 offset:35840
	ds_read_b128 v[208:211], v152 offset:36864
	ds_read_b128 v[212:215], v152 offset:37888
	ds_read_b128 v[220:223], v152 offset:38912
	ds_read_b128 v[224:227], v152 offset:39936
	s_nop 0
	global_load_lds_dwordx4 v96, s[20:21]
	s_mov_b32 m0, s60
	s_nop 0
	global_load_lds_dwordx4 v133, s[20:21]
	s_waitcnt vmcnt(8)
	s_waitcnt lgkmcnt(0)
	s_barrier
	v_mfma_f32_16x16x32_bf16 v[122:125], v[160:163], v[192:195], v[122:125]
	v_mfma_f32_16x16x32_bf16 v[114:117], v[168:171], v[192:195], v[114:117]
	v_mfma_f32_16x16x32_bf16 v[106:109], v[160:163], v[200:203], v[106:109]
	v_mfma_f32_16x16x32_bf16 v[98:101], v[168:171], v[200:203], v[98:101]
	v_mfma_f32_16x16x32_bf16 v[88:91], v[160:163], v[208:211], v[88:91]
	v_mfma_f32_16x16x32_bf16 v[80:83], v[168:171], v[208:211], v[80:83]
	v_mfma_f32_16x16x32_bf16 v[72:75], v[160:163], v[220:223], v[72:75]
	v_mfma_f32_16x16x32_bf16 v[64:67], v[168:171], v[220:223], v[64:67]
	v_mfma_f32_16x16x32_bf16 v[122:125], v[164:167], v[196:199], v[122:125]
	v_mfma_f32_16x16x32_bf16 v[114:117], v[172:175], v[196:199], v[114:117]
	v_mfma_f32_16x16x32_bf16 v[106:109], v[164:167], v[204:207], v[106:109]
	v_mfma_f32_16x16x32_bf16 v[98:101], v[172:175], v[204:207], v[98:101]
	v_mfma_f32_16x16x32_bf16 v[88:91], v[164:167], v[212:215], v[88:91]
	v_mfma_f32_16x16x32_bf16 v[80:83], v[172:175], v[212:215], v[80:83]
	v_mfma_f32_16x16x32_bf16 v[72:75], v[164:167], v[224:227], v[72:75]
	v_mfma_f32_16x16x32_bf16 v[64:67], v[172:175], v[224:227], v[64:67]
	v_mfma_f32_16x16x32_bf16 v[126:129], v[176:179], v[192:195], v[126:129]
	v_mfma_f32_16x16x32_bf16 v[118:121], v[184:187], v[192:195], v[118:121]
	v_mfma_f32_16x16x32_bf16 v[110:113], v[176:179], v[200:203], v[110:113]
	v_mfma_f32_16x16x32_bf16 v[102:105], v[184:187], v[200:203], v[102:105]
	v_mfma_f32_16x16x32_bf16 v[92:95], v[176:179], v[208:211], v[92:95]
	v_mfma_f32_16x16x32_bf16 v[84:87], v[184:187], v[208:211], v[84:87]
	v_mfma_f32_16x16x32_bf16 v[76:79], v[176:179], v[220:223], v[76:79]
	v_mfma_f32_16x16x32_bf16 v[68:71], v[184:187], v[220:223], v[68:71]
	v_mfma_f32_16x16x32_bf16 v[126:129], v[180:183], v[196:199], v[126:129]
	v_mfma_f32_16x16x32_bf16 v[118:121], v[188:191], v[196:199], v[118:121]
	v_mfma_f32_16x16x32_bf16 v[110:113], v[180:183], v[204:207], v[110:113]
	v_mfma_f32_16x16x32_bf16 v[102:105], v[188:191], v[204:207], v[102:105]
	v_mfma_f32_16x16x32_bf16 v[92:95], v[180:183], v[212:215], v[92:95]
	v_mfma_f32_16x16x32_bf16 v[84:87], v[188:191], v[212:215], v[84:87]
	v_mfma_f32_16x16x32_bf16 v[76:79], v[180:183], v[224:227], v[76:79]
	v_mfma_f32_16x16x32_bf16 v[68:71], v[188:191], v[224:227], v[68:71]
	s_barrier
; #define PG8_STAGE(bufoff, gbase, voff) do { _Pragma("unroll") for (int _i = 0; _i < 2; ++_i) \
;         __builtin_amdgcn_global_load_lds((const __attribute__((address_space(1))) unsigned*)((const __attribute__((address_space(1))) char*)(gbase) + (unsigned)lnd_v((int)(voff)[_i])), (LAS unsigned*)(lds + (bufoff) + ldsw + _i * 8192), 16, 0, 0); } while (0)
; #define PG8_LDA(dst, b, h) do { _Pragma("unroll") for (int m = 0; m < 4; ++m) _Pragma("unroll") for (int k = 0; k < 2; ++k) dst[m][k] = *(const LAS bf16x8*)(lds + PG8_SA(b, h) + aoff + m * 2048 + k * 1024); } while (0)
; #define PG8_MMA(ai, bj, At, Bt) do { __builtin_amdgcn_s_setprio(1); _Pragma("unroll") for (int m = 0; m < 4; ++m) _Pragma("unroll") for (int n = 0; n < 2; ++n) _Pragma("unroll") for (int k = 0; k < 2; ++k) \
;         acc[ai][bj][m][n] = __builtin_amdgcn_mfma_f32_16x16x32_bf16(Bt[n][k], At[m][k], acc[ai][bj][m][n], 0, 0, 0); __builtin_amdgcn_s_setprio(0); } while (0)
; #define PG8_WAIT_V(n) asm volatile("s_waitcnt vmcnt(" #n ")" ::: "memory")
; #define PG8_WAIT_L(n) asm volatile("s_waitcnt lgkmcnt(" #n ")" ::: "memory")
; #define PG8_BAR __builtin_amdgcn_s_barrier()
; #define PG8_SCHED __builtin_amdgcn_sched_barrier(0)
; template <class Desc, class Epi>
; __device__ __forceinline__ void gemm_phase(const int wv_, LAS unsigned char* lds, const Desc& d, const Epi& E) {
;     ...
;             PG8_LDA(At, 1, 1); PG8_STAGE(PG8_SB(1, 0), b3, voffB); PG8_STAGE(PG8_SB(1, 1), b3 + hstepB, voffB); PG8_STAGE(PG8_SA(1, 0), a3, sA0);
;             PG8_WAIT_V(8); PG8_WAIT_L(0); PG8_BAR; PG8_MMA(1, 0, At, B0); PG8_MMA(1, 1, At, B1); PG8_BAR; PG8_SCHED;
;         }
;         if (wr == 0) PG8_BAR;
	v_mov_b32_e32 v96, v138
	ds_read_b128 v[192:195], v152 offset:49152
	ds_read_b128 v[196:199], v152 offset:50176
	ds_read_b128 v[200:203], v152 offset:51200
	ds_read_b128 v[204:207], v152 offset:52224
	ds_read_b128 v[208:211], v152 offset:53248
	ds_read_b128 v[212:215], v152 offset:54272
	ds_read_b128 v[220:223], v152 offset:55296
	ds_read_b128 v[224:227], v152 offset:56320
	s_add_i32 s2, s2, s56
	v_lshl_add_u64 v[228:229], s[22:23], 0, v[96:97]
	v_lshl_add_u64 v[228:229], v[228:229], 0, s[30:31]
	s_mov_b32 m0, s2
	v_mov_b32_e32 v96, v141
	global_load_lds_dwordx4 v[228:229], off
	s_add_i32 m0, s2, 0x2000
	s_add_u32 s2, s22, 0x40080
	v_lshl_add_u64 v[228:229], s[22:23], 0, v[96:97]
	v_lshl_add_u64 v[228:229], v[228:229], 0, s[30:31]
	s_addc_u32 s3, s23, 0
	v_mov_b32_e32 v96, v138
	s_add_i32 s22, s67, s56
	global_load_lds_dwordx4 v[228:229], off
	s_mov_b32 m0, s22
	v_mov_b32_e32 v135, v97
	global_load_lds_dwordx4 v96, s[2:3]
	v_mov_b32_e32 v96, v141
	s_add_i32 m0, s22, 0x2000
	v_mov_b32_e32 v133, v97
	global_load_lds_dwordx4 v96, s[2:3]
	s_mov_b32 m0, s61
	v_lshl_add_u64 v[134:135], s[20:21], 0, v[134:135]
	v_lshl_add_u64 v[134:135], v[134:135], 0, s[30:31]
	global_load_lds_dwordx4 v[134:135], off
	s_mov_b32 m0, s62
	v_lshl_add_u64 v[132:133], s[20:21], 0, v[132:133]
	v_lshl_add_u64 v[132:133], v[132:133], 0, s[30:31]
	global_load_lds_dwordx4 v[132:133], off
	s_waitcnt vmcnt(8)
	s_waitcnt lgkmcnt(0)
	s_barrier
	v_mfma_f32_16x16x32_bf16 v[56:59], v[160:163], v[192:195], v[56:59]
	v_mfma_f32_16x16x32_bf16 v[48:51], v[168:171], v[192:195], v[48:51]
	v_mfma_f32_16x16x32_bf16 v[40:43], v[160:163], v[200:203], v[40:43]
	v_mfma_f32_16x16x32_bf16 v[32:35], v[168:171], v[200:203], v[32:35]
	v_mfma_f32_16x16x32_bf16 v[24:27], v[160:163], v[208:211], v[24:27]
	v_mfma_f32_16x16x32_bf16 v[16:19], v[168:171], v[208:211], v[16:19]
	v_mfma_f32_16x16x32_bf16 v[8:11], v[160:163], v[220:223], v[8:11]
	v_mfma_f32_16x16x32_bf16 v[4:7], v[168:171], v[220:223], v[4:7]
	v_mfma_f32_16x16x32_bf16 v[56:59], v[164:167], v[196:199], v[56:59]
	v_mfma_f32_16x16x32_bf16 v[48:51], v[172:175], v[196:199], v[48:51]
	v_mfma_f32_16x16x32_bf16 v[40:43], v[164:167], v[204:207], v[40:43]
	v_mfma_f32_16x16x32_bf16 v[32:35], v[172:175], v[204:207], v[32:35]
	v_mfma_f32_16x16x32_bf16 v[24:27], v[164:167], v[212:215], v[24:27]
	v_mfma_f32_16x16x32_bf16 v[16:19], v[172:175], v[212:215], v[16:19]
	v_mfma_f32_16x16x32_bf16 v[8:11], v[164:167], v[224:227], v[8:11]
	v_mfma_f32_16x16x32_bf16 v[4:7], v[172:175], v[224:227], v[4:7]
	v_mfma_f32_16x16x32_bf16 v[60:63], v[176:179], v[192:195], v[60:63]
	v_mfma_f32_16x16x32_bf16 v[52:55], v[184:187], v[192:195], v[52:55]
	v_mfma_f32_16x16x32_bf16 v[44:47], v[176:179], v[200:203], v[44:47]
	v_mfma_f32_16x16x32_bf16 v[36:39], v[184:187], v[200:203], v[36:39]
	v_mfma_f32_16x16x32_bf16 v[28:31], v[176:179], v[208:211], v[28:31]
	v_mfma_f32_16x16x32_bf16 v[20:23], v[184:187], v[208:211], v[20:23]
	v_mfma_f32_16x16x32_bf16 v[12:15], v[176:179], v[220:223], v[12:15]
	v_mfma_f32_16x16x32_bf16 v[0:3], v[184:187], v[220:223], v[0:3]
	v_mfma_f32_16x16x32_bf16 v[60:63], v[180:183], v[196:199], v[60:63]
	v_mfma_f32_16x16x32_bf16 v[52:55], v[188:191], v[196:199], v[52:55]
	v_mfma_f32_16x16x32_bf16 v[44:47], v[180:183], v[204:207], v[44:47]
	v_mfma_f32_16x16x32_bf16 v[36:39], v[188:191], v[204:207], v[36:39]
	v_mfma_f32_16x16x32_bf16 v[28:31], v[180:183], v[212:215], v[28:31]
	v_mfma_f32_16x16x32_bf16 v[20:23], v[188:191], v[212:215], v[20:23]
	v_mfma_f32_16x16x32_bf16 v[12:15], v[180:183], v[224:227], v[12:15]
	v_mfma_f32_16x16x32_bf16 v[0:3], v[188:191], v[224:227], v[0:3]
	s_barrier
	s_add_i32 s66, s66, 2
	s_cmp_gt_u32 s66, 13
	s_mov_b64 s[2:3], s[4:5]
	s_cbranch_scc0 .LBB0_1861
	s_and_b64 vcc, exec, s[40:41]
	s_cbranch_vccz .LBB0_1864
	s_barrier

; #define PG8_STAGE(bufoff, gbase, voff) do { _Pragma("unroll") for (int _i = 0; _i < 2; ++_i) \
;         __builtin_amdgcn_global_load_lds((const __attribute__((address_space(1))) unsigned*)((const __attribute__((address_space(1))) char*)(gbase) + (unsigned)lnd_v((int)(voff)[_i])), (LAS unsigned*)(lds + (bufoff) + ldsw + _i * 8192), 16, 0, 0); } while (0)
; #define PG8_LDA(dst, b, h) do { _Pragma("unroll") for (int m = 0; m < 4; ++m) _Pragma("unroll") for (int k = 0; k < 2; ++k) dst[m][k] = *(const LAS bf16x8*)(lds + PG8_SA(b, h) + aoff + m * 2048 + k * 1024); } while (0)
; #define PG8_LDB(dst, b, h) do { _Pragma("unroll") for (int n = 0; n < 2; ++n) _Pragma("unroll") for (int k = 0; k < 2; ++k) dst[n][k] = *(const LAS bf16x8*)(lds + PG8_SB(b, h) + boff + n * 2048 + k * 1024); } while (0)
; #define PG8_MMA(ai, bj, At, Bt) do { __builtin_amdgcn_s_setprio(1); _Pragma("unroll") for (int m = 0; m < 4; ++m) _Pragma("unroll") for (int n = 0; n < 2; ++n) _Pragma("unroll") for (int k = 0; k < 2; ++k) \
;         acc[ai][bj][m][n] = __builtin_amdgcn_mfma_f32_16x16x32_bf16(Bt[n][k], At[m][k], acc[ai][bj][m][n], 0, 0, 0); __builtin_amdgcn_s_setprio(0); } while (0)
; template <class Desc, class Epi>
; __device__ __forceinline__ void gemm_phase(const int wv_, LAS unsigned char* lds, const Desc& d, const Epi& E) {
;     ...
;             const bool last = (t == nt - 2);
;             unsigned sA0[2], sA1[2];
;             if constexpr (Desc::GATHER) { sA0[0] = last ? voffAn[0] : voffA[0]; sA0[1] = last ? voffAn[1] : voffA[1]; sA1[0] = last ? voffAn1[0] : voffA1[0]; sA1[1] = last ? voffAn1[1] : voffA1[1]; }
;             else { sA0[0] = voffA[0]; sA0[1] = voffA[1]; sA1[0] = voffA1[0]; sA1[1] = voffA1[1]; }
;             const char* a1 = cA + (size_t)(t + 1) * kstep;
;             const char* a2 = last ? nA : cA + (size_t)(t + 2) * kstep; const char* b2 = last ? nB : cB + (size_t)(t + 2) * kstep;
;             const char* a3 = a2 + kstep; const char* b3 = b2 + kstep;
;             PG8_LDB(B0, 0, 0); PG8_LDB(B1, 0, 1); PG8_SCHED; PG8_LDA(At, 0, 0); PG8_STAGE(PG8_SA(1, 1), a1, voffA1);
;             PG8_WAIT_V(8); PG8_WAIT_L(0); PG8_BAR; PG8_MMA(0, 0, At, B0); PG8_MMA(0, 1, At, B1); PG8_BAR; PG8_SCHED;
;             PG8_LDA(At, 0, 1); PG8_STAGE(PG8_SB(0, 0), b2, voffB); PG8_STAGE(PG8_SB(0, 1), b2 + hstepB, voffB); PG8_STAGE(PG8_SA(0, 0), a2, sA0);
.LBB0_1942:
	s_add_u32 s4, s2, 0x80
	s_addc_u32 s5, s3, 0
	s_add_i32 s63, 0, 0x10000
	s_cmp_eq_u32 s62, 28
	s_cselect_b32 s5, s47, s5
	s_cselect_b32 s4, s46, s4
	v_add_u32_e32 v96, s63, v139
	s_cselect_b32 s21, s45, s43
	s_cselect_b32 s20, s44, s29
	s_add_i32 s66, 0, 0x14000
	ds_read_b128 v[150:153], v96
	ds_read_b128 v[154:157], v96 offset:1024
	ds_read_b128 v[158:161], v96 offset:2048
	ds_read_b128 v[162:165], v96 offset:3072
	v_add_u32_e32 v96, s66, v139
	ds_read_b128 v[166:169], v96
	ds_read_b128 v[170:173], v96 offset:1024
	ds_read_b128 v[174:177], v96 offset:2048
	ds_read_b128 v[178:181], v96 offset:3072
	v_mov_b32_e32 v96, v133
	ds_read_b128 v[182:185], v149
	ds_read_b128 v[186:189], v149 offset:1024
	ds_read_b128 v[190:193], v149 offset:2048
	ds_read_b128 v[194:197], v149 offset:3072
	ds_read_b128 v[198:201], v149 offset:4096
	ds_read_b128 v[202:205], v149 offset:5120
	ds_read_b128 v[206:209], v149 offset:6144
	ds_read_b128 v[210:213], v149 offset:7168
	s_add_i32 m0, s53, 0xc000
	s_nop 0
	global_load_lds_dwordx4 v96, s[2:3]
	v_mov_b32_e32 v96, v136
	s_add_i32 m0, s53, 0xe000
	s_nop 0
	global_load_lds_dwordx4 v96, s[2:3]
	s_waitcnt vmcnt(8)
	s_waitcnt lgkmcnt(0)
	s_barrier
	v_mfma_f32_16x16x32_bf16 v[126:129], v[150:153], v[182:185], v[126:129]
	v_mfma_f32_16x16x32_bf16 v[122:125], v[158:161], v[182:185], v[122:125]
	v_mfma_f32_16x16x32_bf16 v[110:113], v[150:153], v[190:193], v[110:113]
	v_mfma_f32_16x16x32_bf16 v[106:109], v[158:161], v[190:193], v[106:109]
	v_mfma_f32_16x16x32_bf16 v[92:95], v[150:153], v[198:201], v[92:95]
	v_mfma_f32_16x16x32_bf16 v[88:91], v[158:161], v[198:201], v[88:91]
	v_mfma_f32_16x16x32_bf16 v[76:79], v[150:153], v[206:209], v[76:79]
	v_mfma_f32_16x16x32_bf16 v[72:75], v[158:161], v[206:209], v[72:75]
	v_mfma_f32_16x16x32_bf16 v[126:129], v[154:157], v[186:189], v[126:129]
	v_mfma_f32_16x16x32_bf16 v[122:125], v[162:165], v[186:189], v[122:125]
	v_mfma_f32_16x16x32_bf16 v[110:113], v[154:157], v[194:197], v[110:113]
	v_mfma_f32_16x16x32_bf16 v[106:109], v[162:165], v[194:197], v[106:109]
	v_mfma_f32_16x16x32_bf16 v[92:95], v[154:157], v[202:205], v[92:95]
	v_mfma_f32_16x16x32_bf16 v[88:91], v[162:165], v[202:205], v[88:91]
	v_mfma_f32_16x16x32_bf16 v[76:79], v[154:157], v[210:213], v[76:79]
	v_mfma_f32_16x16x32_bf16 v[72:75], v[162:165], v[210:213], v[72:75]
	v_mfma_f32_16x16x32_bf16 v[118:121], v[166:169], v[182:185], v[118:121]
	v_mfma_f32_16x16x32_bf16 v[114:117], v[174:177], v[182:185], v[114:117]
	v_mfma_f32_16x16x32_bf16 v[102:105], v[166:169], v[190:193], v[102:105]
	v_mfma_f32_16x16x32_bf16 v[98:101], v[174:177], v[190:193], v[98:101]
	v_mfma_f32_16x16x32_bf16 v[84:87], v[166:169], v[198:201], v[84:87]
	v_mfma_f32_16x16x32_bf16 v[80:83], v[174:177], v[198:201], v[80:83]
	v_mfma_f32_16x16x32_bf16 v[68:71], v[166:169], v[206:209], v[68:71]
	v_mfma_f32_16x16x32_bf16 v[64:67], v[174:177], v[206:209], v[64:67]
	v_mfma_f32_16x16x32_bf16 v[118:121], v[170:173], v[186:189], v[118:121]
	v_mfma_f32_16x16x32_bf16 v[114:117], v[178:181], v[186:189], v[114:117]
	v_mfma_f32_16x16x32_bf16 v[102:105], v[170:173], v[194:197], v[102:105]
	v_mfma_f32_16x16x32_bf16 v[98:101], v[178:181], v[194:197], v[98:101]
	v_mfma_f32_16x16x32_bf16 v[84:87], v[170:173], v[202:205], v[84:87]
	v_mfma_f32_16x16x32_bf16 v[80:83], v[178:181], v[202:205], v[80:83]
	v_mfma_f32_16x16x32_bf16 v[68:71], v[170:173], v[210:213], v[68:71]
	v_mfma_f32_16x16x32_bf16 v[64:67], v[178:181], v[210:213], v[64:67]
	s_barrier
	v_mov_b32_e32 v96, v134
	s_add_i32 s63, s63, s52
	ds_read_b128 v[182:185], v149 offset:16384
	ds_read_b128 v[186:189], v149 offset:17408
	ds_read_b128 v[190:193], v149 offset:18432
	ds_read_b128 v[194:197], v149 offset:19456
	ds_read_b128 v[198:201], v149 offset:20480
	ds_read_b128 v[202:205], v149 offset:21504
	ds_read_b128 v[206:209], v149 offset:22528
	ds_read_b128 v[210:213], v149 offset:23552
	s_mov_b32 m0, s63
	s_nop 0
	global_load_lds_dwordx4 v96, s[20:21]
	v_mov_b32_e32 v96, v137
	s_add_i32 m0, s63, 0x2000
	s_add_u32 s64, s20, 0x80000
	global_load_lds_dwordx4 v96, s[20:21]
	s_addc_u32 s65, s21, 0
	v_mov_b32_e32 v96, v134
	s_add_i32 s63, s66, s52
	s_mov_b32 m0, s63
	s_nop 0
	global_load_lds_dwordx4 v96, s[64:65]
	v_mov_b32_e32 v96, v137
	s_add_i32 m0, s63, 0x2000
	s_nop 0
	global_load_lds_dwordx4 v96, s[64:65]
	v_mov_b32_e32 v96, v132
	s_mov_b32 m0, s53
	s_nop 0
	global_load_lds_dwordx4 v96, s[4:5]
	v_mov_b32_e32 v96, v135
	s_mov_b32 m0, s54
	s_nop 0
	global_load_lds_dwordx4 v96, s[4:5]
	s_waitcnt vmcnt(8)
	s_waitcnt lgkmcnt(0)
	s_barrier
; #define PG8_STAGE(bufoff, gbase, voff) do { _Pragma("unroll") for (int _i = 0; _i < 2; ++_i) \
;         __builtin_amdgcn_global_load_lds((const __attribute__((address_space(1))) unsigned*)((const __attribute__((address_space(1))) char*)(gbase) + (unsigned)lnd_v((int)(voff)[_i])), (LAS unsigned*)(lds + (bufoff) + ldsw + _i * 8192), 16, 0, 0); } while (0)
; #define PG8_LDA(dst, b, h) do { _Pragma("unroll") for (int m = 0; m < 4; ++m) _Pragma("unroll") for (int k = 0; k < 2; ++k) dst[m][k] = *(const LAS bf16x8*)(lds + PG8_SA(b, h) + aoff + m * 2048 + k * 1024); } while (0)
; #define PG8_LDB(dst, b, h) do { _Pragma("unroll") for (int n = 0; n < 2; ++n) _Pragma("unroll") for (int k = 0; k < 2; ++k) dst[n][k] = *(const LAS bf16x8*)(lds + PG8_SB(b, h) + boff + n * 2048 + k * 1024); } while (0)
; #define PG8_MMA(ai, bj, At, Bt) do { __builtin_amdgcn_s_setprio(1); _Pragma("unroll") for (int m = 0; m < 4; ++m) _Pragma("unroll") for (int n = 0; n < 2; ++n) _Pragma("unroll") for (int k = 0; k < 2; ++k) \
;         acc[ai][bj][m][n] = __builtin_amdgcn_mfma_f32_16x16x32_bf16(Bt[n][k], At[m][k], acc[ai][bj][m][n], 0, 0, 0); __builtin_amdgcn_s_setprio(0); } while (0)
; #define PG8_WAIT_V(n) asm volatile("s_waitcnt vmcnt(" #n ")" ::: "memory")
; #define PG8_WAIT_L(n) asm volatile("s_waitcnt lgkmcnt(" #n ")" ::: "memory")
; #define PG8_BAR __builtin_amdgcn_s_barrier()
; #define PG8_SCHED __builtin_amdgcn_sched_barrier(0)
; template <class Desc, class Epi>
; __device__ __forceinline__ void gemm_phase(const int wv_, LAS unsigned char* lds, const Desc& d, const Epi& E) {
;     ...
;             PG8_WAIT_V(8); PG8_WAIT_L(0); PG8_BAR; PG8_MMA(1, 0, At, B0); PG8_MMA(1, 1, At, B1); PG8_BAR; PG8_SCHED;
;             PG8_LDB(B0, 1, 0); PG8_LDB(B1, 1, 1); PG8_SCHED; PG8_LDA(At, 1, 0); PG8_STAGE(PG8_SA(0, 1), a2, sA1);
;             PG8_WAIT_V(8); PG8_WAIT_L(0); PG8_BAR; PG8_MMA(0, 0, At, B0); PG8_MMA(0, 1, At, B1); PG8_BAR; PG8_SCHED;
	v_mfma_f32_16x16x32_bf16 v[60:63], v[150:153], v[182:185], v[60:63]
	v_mfma_f32_16x16x32_bf16 v[56:59], v[158:161], v[182:185], v[56:59]
	v_mfma_f32_16x16x32_bf16 v[44:47], v[150:153], v[190:193], v[44:47]
	v_mfma_f32_16x16x32_bf16 v[32:35], v[158:161], v[190:193], v[32:35]
	v_mfma_f32_16x16x32_bf16 v[16:19], v[150:153], v[198:201], v[16:19]
	v_mfma_f32_16x16x32_bf16 v[8:11], v[158:161], v[198:201], v[8:11]
	v_mfma_f32_16x16x32_bf16 v[4:7], v[150:153], v[206:209], v[4:7]
	v_mfma_f32_16x16x32_bf16 v[0:3], v[158:161], v[206:209], v[0:3]
	v_mfma_f32_16x16x32_bf16 v[60:63], v[154:157], v[186:189], v[60:63]
	v_mfma_f32_16x16x32_bf16 v[56:59], v[162:165], v[186:189], v[56:59]
	v_mfma_f32_16x16x32_bf16 v[44:47], v[154:157], v[194:197], v[44:47]
	v_mfma_f32_16x16x32_bf16 v[32:35], v[162:165], v[194:197], v[32:35]
	v_mfma_f32_16x16x32_bf16 v[16:19], v[154:157], v[202:205], v[16:19]
	v_mfma_f32_16x16x32_bf16 v[8:11], v[162:165], v[202:205], v[8:11]
	v_mfma_f32_16x16x32_bf16 v[4:7], v[154:157], v[210:213], v[4:7]
	v_mfma_f32_16x16x32_bf16 v[0:3], v[162:165], v[210:213], v[0:3]
	v_mfma_f32_16x16x32_bf16 v[52:55], v[166:169], v[182:185], v[52:55]
	v_mfma_f32_16x16x32_bf16 v[48:51], v[174:177], v[182:185], v[48:51]
	v_mfma_f32_16x16x32_bf16 v[28:31], v[166:169], v[190:193], v[28:31]
	v_mfma_f32_16x16x32_bf16 v[12:15], v[174:177], v[190:193], v[12:15]
	v_mfma_f32_16x16x32_bf16 v[36:39], v[166:169], v[198:201], v[36:39]
	v_mfma_f32_16x16x32_bf16 v[40:43], v[174:177], v[198:201], v[40:43]
	v_mfma_f32_16x16x32_bf16 v[20:23], v[166:169], v[206:209], v[20:23]
	v_mfma_f32_16x16x32_bf16 v[24:27], v[174:177], v[206:209], v[24:27]
	v_mfma_f32_16x16x32_bf16 v[52:55], v[170:173], v[186:189], v[52:55]
	v_mfma_f32_16x16x32_bf16 v[48:51], v[178:181], v[186:189], v[48:51]
	v_mfma_f32_16x16x32_bf16 v[28:31], v[170:173], v[194:197], v[28:31]
	v_mfma_f32_16x16x32_bf16 v[12:15], v[178:181], v[194:197], v[12:15]
	v_mfma_f32_16x16x32_bf16 v[36:39], v[170:173], v[202:205], v[36:39]
	v_mfma_f32_16x16x32_bf16 v[40:43], v[178:181], v[202:205], v[40:43]
	v_mfma_f32_16x16x32_bf16 v[20:23], v[170:173], v[210:213], v[20:23]
	v_mfma_f32_16x16x32_bf16 v[24:27], v[178:181], v[210:213], v[24:27]
	s_barrier
	s_add_i32 s63, 0, 0x18000
	v_add_u32_e32 v96, s63, v139
	s_add_i32 s64, 0, 0x1c000
	ds_read_b128 v[150:153], v96
	ds_read_b128 v[154:157], v96 offset:1024
	ds_read_b128 v[158:161], v96 offset:2048
	ds_read_b128 v[162:165], v96 offset:3072
	v_add_u32_e32 v96, s64, v139
	ds_read_b128 v[166:169], v96
	ds_read_b128 v[170:173], v96 offset:1024
	ds_read_b128 v[174:177], v96 offset:2048
	ds_read_b128 v[178:181], v96 offset:3072
	v_mov_b32_e32 v96, v133
	s_mov_b32 m0, s55
	ds_read_b128 v[182:185], v149 offset:32768
	ds_read_b128 v[186:189], v149 offset:33792
	ds_read_b128 v[190:193], v149 offset:34816
	ds_read_b128 v[194:197], v149 offset:35840
	ds_read_b128 v[198:201], v149 offset:36864
	ds_read_b128 v[202:205], v149 offset:37888
	ds_read_b128 v[206:209], v149 offset:38912
	ds_read_b128 v[210:213], v149 offset:39936
	s_nop 0
	global_load_lds_dwordx4 v96, s[4:5]
	v_mov_b32_e32 v96, v136
	s_mov_b32 m0, s56
	s_nop 0
	global_load_lds_dwordx4 v96, s[4:5]
	s_waitcnt vmcnt(8)
	s_waitcnt lgkmcnt(0)
	s_barrier
	v_mfma_f32_16x16x32_bf16 v[126:129], v[150:153], v[182:185], v[126:129]
	v_mfma_f32_16x16x32_bf16 v[122:125], v[158:161], v[182:185], v[122:125]
	v_mfma_f32_16x16x32_bf16 v[110:113], v[150:153], v[190:193], v[110:113]
	v_mfma_f32_16x16x32_bf16 v[106:109], v[158:161], v[190:193], v[106:109]
	v_mfma_f32_16x16x32_bf16 v[92:95], v[150:153], v[198:201], v[92:95]
	v_mfma_f32_16x16x32_bf16 v[88:91], v[158:161], v[198:201], v[88:91]
	v_mfma_f32_16x16x32_bf16 v[76:79], v[150:153], v[206:209], v[76:79]
	v_mfma_f32_16x16x32_bf16 v[72:75], v[158:161], v[206:209], v[72:75]
	v_mfma_f32_16x16x32_bf16 v[126:129], v[154:157], v[186:189], v[126:129]
	v_mfma_f32_16x16x32_bf16 v[122:125], v[162:165], v[186:189], v[122:125]
	v_mfma_f32_16x16x32_bf16 v[110:113], v[154:157], v[194:197], v[110:113]
	v_mfma_f32_16x16x32_bf16 v[106:109], v[162:165], v[194:197], v[106:109]
	v_mfma_f32_16x16x32_bf16 v[92:95], v[154:157], v[202:205], v[92:95]
	v_mfma_f32_16x16x32_bf16 v[88:91], v[162:165], v[202:205], v[88:91]
	v_mfma_f32_16x16x32_bf16 v[76:79], v[154:157], v[210:213], v[76:79]
	v_mfma_f32_16x16x32_bf16 v[72:75], v[162:165], v[210:213], v[72:75]
	v_mfma_f32_16x16x32_bf16 v[118:121], v[166:169], v[182:185], v[118:121]
	v_mfma_f32_16x16x32_bf16 v[114:117], v[174:177], v[182:185], v[114:117]
	v_mfma_f32_16x16x32_bf16 v[102:105], v[166:169], v[190:193], v[102:105]
	v_mfma_f32_16x16x32_bf16 v[98:101], v[174:177], v[190:193], v[98:101]
	v_mfma_f32_16x16x32_bf16 v[84:87], v[166:169], v[198:201], v[84:87]
	v_mfma_f32_16x16x32_bf16 v[80:83], v[174:177], v[198:201], v[80:83]
	v_mfma_f32_16x16x32_bf16 v[68:71], v[166:169], v[206:209], v[68:71]
	v_mfma_f32_16x16x32_bf16 v[64:67], v[174:177], v[206:209], v[64:67]
	v_mfma_f32_16x16x32_bf16 v[118:121], v[170:173], v[186:189], v[118:121]
	v_mfma_f32_16x16x32_bf16 v[114:117], v[178:181], v[186:189], v[114:117]
	v_mfma_f32_16x16x32_bf16 v[102:105], v[170:173], v[194:197], v[102:105]
	v_mfma_f32_16x16x32_bf16 v[98:101], v[178:181], v[194:197], v[98:101]
	v_mfma_f32_16x16x32_bf16 v[84:87], v[170:173], v[202:205], v[84:87]
	v_mfma_f32_16x16x32_bf16 v[80:83], v[178:181], v[202:205], v[80:83]
	v_mfma_f32_16x16x32_bf16 v[68:71], v[170:173], v[210:213], v[68:71]
	v_mfma_f32_16x16x32_bf16 v[64:67], v[178:181], v[210:213], v[64:67]
	s_barrier
; #define PG8_STAGE(bufoff, gbase, voff) do { _Pragma("unroll") for (int _i = 0; _i < 2; ++_i) \
;         __builtin_amdgcn_global_load_lds((const __attribute__((address_space(1))) unsigned*)((const __attribute__((address_space(1))) char*)(gbase) + (unsigned)lnd_v((int)(voff)[_i])), (LAS unsigned*)(lds + (bufoff) + ldsw + _i * 8192), 16, 0, 0); } while (0)
; #define PG8_LDA(dst, b, h) do { _Pragma("unroll") for (int m = 0; m < 4; ++m) _Pragma("unroll") for (int k = 0; k < 2; ++k) dst[m][k] = *(const LAS bf16x8*)(lds + PG8_SA(b, h) + aoff + m * 2048 + k * 1024); } while (0)
; #define PG8_MMA(ai, bj, At, Bt) do { __builtin_amdgcn_s_setprio(1); _Pragma("unroll") for (int m = 0; m < 4; ++m) _Pragma("unroll") for (int n = 0; n < 2; ++n) _Pragma("unroll") for (int k = 0; k < 2; ++k) \
;         acc[ai][bj][m][n] = __builtin_amdgcn_mfma_f32_16x16x32_bf16(Bt[n][k], At[m][k], acc[ai][bj][m][n], 0, 0, 0); __builtin_amdgcn_s_setprio(0); } while (0)
; #define PG8_WAIT_V(n) asm volatile("s_waitcnt vmcnt(" #n ")" ::: "memory")
; #define PG8_WAIT_L(n) asm volatile("s_waitcnt lgkmcnt(" #n ")" ::: "memory")
; #define PG8_BAR __builtin_amdgcn_s_barrier()
; #define PG8_SCHED __builtin_amdgcn_sched_barrier(0)
; template <class Desc, class Epi>
; __device__ __forceinline__ void gemm_phase(const int wv_, LAS unsigned char* lds, const Desc& d, const Epi& E) {
;     ...
;             PG8_LDA(At, 1, 1); PG8_STAGE(PG8_SB(1, 0), b3, voffB); PG8_STAGE(PG8_SB(1, 1), b3 + hstepB, voffB); PG8_STAGE(PG8_SA(1, 0), a3, sA0);
;             PG8_WAIT_V(8); PG8_WAIT_L(0); PG8_BAR; PG8_MMA(1, 0, At, B0); PG8_MMA(1, 1, At, B1); PG8_BAR; PG8_SCHED;
;         }
;         if (wr == 0) PG8_BAR;
	v_mov_b32_e32 v96, v134
	ds_read_b128 v[182:185], v149 offset:49152
	ds_read_b128 v[186:189], v149 offset:50176
	ds_read_b128 v[190:193], v149 offset:51200
	ds_read_b128 v[194:197], v149 offset:52224
	ds_read_b128 v[198:201], v149 offset:53248
	ds_read_b128 v[202:205], v149 offset:54272
	ds_read_b128 v[206:209], v149 offset:55296
	ds_read_b128 v[210:213], v149 offset:56320
	s_add_i32 s63, s63, s52
	v_lshl_add_u64 v[130:131], s[20:21], 0, v[96:97]
	v_lshl_add_u64 v[130:131], v[130:131], 0, s[30:31]
	s_mov_b32 m0, s63
	v_mov_b32_e32 v96, v137
	global_load_lds_dwordx4 v[130:131], off
	s_add_i32 m0, s63, 0x2000
	s_nop 0
	v_lshl_add_u64 v[130:131], s[20:21], 0, v[96:97]
	s_add_u32 s20, s20, 0x80080
	v_lshl_add_u64 v[130:131], v[130:131], 0, s[30:31]
	s_addc_u32 s21, s21, 0
	v_mov_b32_e32 v96, v134
	s_add_i32 s63, s64, s52
	global_load_lds_dwordx4 v[130:131], off
	s_mov_b32 m0, s63
	s_nop 0
	global_load_lds_dwordx4 v96, s[20:21]
	v_mov_b32_e32 v96, v137
	s_add_i32 m0, s63, 0x2000
	s_nop 0
	global_load_lds_dwordx4 v96, s[20:21]
	v_mov_b32_e32 v96, v132
	s_mov_b32 m0, s57
	v_lshl_add_u64 v[130:131], s[4:5], 0, v[96:97]
	v_lshl_add_u64 v[130:131], v[130:131], 0, s[30:31]
	v_mov_b32_e32 v96, v135
	global_load_lds_dwordx4 v[130:131], off
	s_mov_b32 m0, s58
	v_lshl_add_u64 v[130:131], s[4:5], 0, v[96:97]
	v_lshl_add_u64 v[130:131], v[130:131], 0, s[30:31]
	global_load_lds_dwordx4 v[130:131], off
	s_waitcnt vmcnt(8)
	s_waitcnt lgkmcnt(0)
	s_barrier
	v_mfma_f32_16x16x32_bf16 v[60:63], v[150:153], v[182:185], v[60:63]
	v_mfma_f32_16x16x32_bf16 v[56:59], v[158:161], v[182:185], v[56:59]
	v_mfma_f32_16x16x32_bf16 v[44:47], v[150:153], v[190:193], v[44:47]
	v_mfma_f32_16x16x32_bf16 v[32:35], v[158:161], v[190:193], v[32:35]
	v_mfma_f32_16x16x32_bf16 v[16:19], v[150:153], v[198:201], v[16:19]
	v_mfma_f32_16x16x32_bf16 v[8:11], v[158:161], v[198:201], v[8:11]
	v_mfma_f32_16x16x32_bf16 v[4:7], v[150:153], v[206:209], v[4:7]
	v_mfma_f32_16x16x32_bf16 v[0:3], v[158:161], v[206:209], v[0:3]
	v_mfma_f32_16x16x32_bf16 v[60:63], v[154:157], v[186:189], v[60:63]
	v_mfma_f32_16x16x32_bf16 v[56:59], v[162:165], v[186:189], v[56:59]
	v_mfma_f32_16x16x32_bf16 v[44:47], v[154:157], v[194:197], v[44:47]
	v_mfma_f32_16x16x32_bf16 v[32:35], v[162:165], v[194:197], v[32:35]
	v_mfma_f32_16x16x32_bf16 v[16:19], v[154:157], v[202:205], v[16:19]
	v_mfma_f32_16x16x32_bf16 v[8:11], v[162:165], v[202:205], v[8:11]
	v_mfma_f32_16x16x32_bf16 v[4:7], v[154:157], v[210:213], v[4:7]
	v_mfma_f32_16x16x32_bf16 v[0:3], v[162:165], v[210:213], v[0:3]
	v_mfma_f32_16x16x32_bf16 v[52:55], v[166:169], v[182:185], v[52:55]
	v_mfma_f32_16x16x32_bf16 v[48:51], v[174:177], v[182:185], v[48:51]
	v_mfma_f32_16x16x32_bf16 v[28:31], v[166:169], v[190:193], v[28:31]
	v_mfma_f32_16x16x32_bf16 v[12:15], v[174:177], v[190:193], v[12:15]
	v_mfma_f32_16x16x32_bf16 v[36:39], v[166:169], v[198:201], v[36:39]
	v_mfma_f32_16x16x32_bf16 v[40:43], v[174:177], v[198:201], v[40:43]
	v_mfma_f32_16x16x32_bf16 v[20:23], v[166:169], v[206:209], v[20:23]
	v_mfma_f32_16x16x32_bf16 v[24:27], v[174:177], v[206:209], v[24:27]
	v_mfma_f32_16x16x32_bf16 v[52:55], v[170:173], v[186:189], v[52:55]
	v_mfma_f32_16x16x32_bf16 v[48:51], v[178:181], v[186:189], v[48:51]
	v_mfma_f32_16x16x32_bf16 v[28:31], v[170:173], v[194:197], v[28:31]
	v_mfma_f32_16x16x32_bf16 v[12:15], v[178:181], v[194:197], v[12:15]
	v_mfma_f32_16x16x32_bf16 v[36:39], v[170:173], v[202:205], v[36:39]
	v_mfma_f32_16x16x32_bf16 v[40:43], v[178:181], v[202:205], v[40:43]
	v_mfma_f32_16x16x32_bf16 v[20:23], v[170:173], v[210:213], v[20:23]
	v_mfma_f32_16x16x32_bf16 v[24:27], v[178:181], v[210:213], v[24:27]
	s_barrier
	s_add_i32 s62, s62, 2
	s_add_u32 s2, s2, 0x100
	s_addc_u32 s3, s3, 0
	s_add_u32 s29, s29, 0x100
	s_addc_u32 s43, s43, 0
	s_cmp_gt_u32 s62, 29
	s_cbranch_scc0 .LBB0_1942
	s_and_b64 vcc, exec, s[40:41]
	s_cbranch_vccz .LBB0_1945
	s_barrier
